# GEMM K-loops: scalar-base LDS-DMA addressing; indexer pass B: batched boundary-bin atomics; k_idx tensor stored fragment-major for coalesced indexer loads
# speedup vs baseline: 1.0216x; 1.0079x over previous
.LBB0_823:
	s_add_u32 s48, s46, 0xfff80080
	s_addc_u32 s49, s47, -1
	s_add_i32 s69, 0, 0x10000
	s_cmp_eq_u32 s67, 28
	s_cselect_b32 s83, s31, s49
	s_cselect_b32 s82, s30, s48
	s_cselect_b32 s49, s45, s15
	s_cselect_b32 s48, s44, s14
	s_add_i32 s70, 0, 0x14000
	v_add_u32_e32 v156, s69, v171
	v_add_u32_e32 v168, s70, v171
	ds_read_b128 v[144:147], v156
	ds_read_b128 v[148:151], v156 offset:1024
	ds_read_b128 v[152:155], v156 offset:2048
	ds_read_b128 v[156:159], v156 offset:3072
	ds_read_b128 v[160:163], v168
	ds_read_b128 v[164:167], v168 offset:1024
	ds_read_b128 v[206:209], v168 offset:2048
	ds_read_b128 v[210:213], v168 offset:3072
	s_add_i32 m0, s55, 0xc000
	ds_read_b128 v[214:217], v189
	ds_read_b128 v[218:221], v189 offset:1024
	ds_read_b128 v[222:225], v189 offset:2048
	ds_read_b128 v[226:229], v189 offset:3072
	ds_read_b128 v[230:233], v189 offset:4096
	ds_read_b128 v[234:237], v189 offset:5120
	ds_read_b128 v[238:241], v189 offset:6144
	ds_read_b128 v[242:245], v189 offset:7168
	global_load_lds_dwordx4 v140, s[46:47]
	s_add_i32 m0, s55, 0xe000
	s_nop 0
	global_load_lds_dwordx4 v142, s[46:47]
	s_waitcnt vmcnt(8)
	s_waitcnt lgkmcnt(0)
	s_barrier
	s_setprio 1
	s_waitcnt lgkmcnt(0)
	v_mfma_f32_16x16x32_bf16 v[124:127], v[144:147], v[214:217], v[124:127]
	v_mfma_f32_16x16x32_bf16 v[120:123], v[152:155], v[214:217], v[120:123]
	v_mfma_f32_16x16x32_bf16 v[108:111], v[144:147], v[222:225], v[108:111]
	v_mfma_f32_16x16x32_bf16 v[104:107], v[152:155], v[222:225], v[104:107]
	v_mfma_f32_16x16x32_bf16 v[92:95], v[144:147], v[230:233], v[92:95]
	v_mfma_f32_16x16x32_bf16 v[88:91], v[152:155], v[230:233], v[88:91]
	v_mfma_f32_16x16x32_bf16 v[76:79], v[144:147], v[238:241], v[76:79]
	v_mfma_f32_16x16x32_bf16 v[72:75], v[152:155], v[238:241], v[72:75]
	v_mfma_f32_16x16x32_bf16 v[124:127], v[148:151], v[218:221], v[124:127]
	v_mfma_f32_16x16x32_bf16 v[120:123], v[156:159], v[218:221], v[120:123]
	v_mfma_f32_16x16x32_bf16 v[108:111], v[148:151], v[226:229], v[108:111]
	v_mfma_f32_16x16x32_bf16 v[104:107], v[156:159], v[226:229], v[104:107]
	v_mfma_f32_16x16x32_bf16 v[92:95], v[148:151], v[234:237], v[92:95]
	v_mfma_f32_16x16x32_bf16 v[88:91], v[156:159], v[234:237], v[88:91]
	v_mfma_f32_16x16x32_bf16 v[76:79], v[148:151], v[242:245], v[76:79]
	v_mfma_f32_16x16x32_bf16 v[72:75], v[156:159], v[242:245], v[72:75]
	s_setprio 0
	s_setprio 1
	v_mfma_f32_16x16x32_bf16 v[116:119], v[160:163], v[214:217], v[116:119]
	v_mfma_f32_16x16x32_bf16 v[112:115], v[206:209], v[214:217], v[112:115]
	v_mfma_f32_16x16x32_bf16 v[100:103], v[160:163], v[222:225], v[100:103]
	v_mfma_f32_16x16x32_bf16 v[96:99], v[206:209], v[222:225], v[96:99]
	v_mfma_f32_16x16x32_bf16 v[84:87], v[160:163], v[230:233], v[84:87]
	v_mfma_f32_16x16x32_bf16 v[80:83], v[206:209], v[230:233], v[80:83]
	v_mfma_f32_16x16x32_bf16 v[68:71], v[160:163], v[238:241], v[68:71]
	v_mfma_f32_16x16x32_bf16 v[64:67], v[206:209], v[238:241], v[64:67]
	v_mfma_f32_16x16x32_bf16 v[116:119], v[164:167], v[218:221], v[116:119]
	v_mfma_f32_16x16x32_bf16 v[112:115], v[210:213], v[218:221], v[112:115]
	v_mfma_f32_16x16x32_bf16 v[100:103], v[164:167], v[226:229], v[100:103]
	v_mfma_f32_16x16x32_bf16 v[96:99], v[210:213], v[226:229], v[96:99]
	v_mfma_f32_16x16x32_bf16 v[84:87], v[164:167], v[234:237], v[84:87]
	v_mfma_f32_16x16x32_bf16 v[80:83], v[210:213], v[234:237], v[80:83]
	v_mfma_f32_16x16x32_bf16 v[68:71], v[164:167], v[242:245], v[68:71]
	v_mfma_f32_16x16x32_bf16 v[64:67], v[210:213], v[242:245], v[64:67]
	s_setprio 0
	s_barrier
	s_add_i32 s69, s69, s23
	s_mov_b32 m0, s69
	ds_read_b128 v[214:217], v189 offset:16384
	ds_read_b128 v[218:221], v189 offset:17408
	ds_read_b128 v[222:225], v189 offset:18432
	ds_read_b128 v[226:229], v189 offset:19456
	ds_read_b128 v[230:233], v189 offset:20480
	ds_read_b128 v[234:237], v189 offset:21504
	ds_read_b128 v[238:241], v189 offset:22528
	ds_read_b128 v[242:245], v189 offset:23552
	global_load_lds_dwordx4 v130, s[48:49]
	s_add_i32 m0, s69, 0x2000
	s_add_u32 s84, s48, 0x80000
	s_addc_u32 s85, s49, 0
	s_add_i32 s69, s70, s23
	global_load_lds_dwordx4 v134, s[48:49]
	s_mov_b32 m0, s69
	s_nop 0
	global_load_lds_dwordx4 v130, s[84:85]
	s_add_i32 m0, s69, 0x2000
	s_nop 0
	global_load_lds_dwordx4 v134, s[84:85]
	s_mov_b32 m0, s55
	s_nop 0
	global_load_lds_dwordx4 v128, s[82:83]
	s_mov_b32 m0, s52
	s_nop 0
	global_load_lds_dwordx4 v132, s[82:83]
	s_waitcnt vmcnt(8)
	s_waitcnt lgkmcnt(0)
	s_barrier
	s_setprio 1
	s_waitcnt lgkmcnt(0)
	v_mfma_f32_16x16x32_bf16 v[60:63], v[144:147], v[214:217], v[60:63]
	v_mfma_f32_16x16x32_bf16 v[56:59], v[152:155], v[214:217], v[56:59]
	v_mfma_f32_16x16x32_bf16 v[44:47], v[144:147], v[222:225], v[44:47]
	v_mfma_f32_16x16x32_bf16 v[40:43], v[152:155], v[222:225], v[40:43]
	v_mfma_f32_16x16x32_bf16 v[28:31], v[144:147], v[230:233], v[28:31]
	v_mfma_f32_16x16x32_bf16 v[24:27], v[152:155], v[230:233], v[24:27]
	v_mfma_f32_16x16x32_bf16 v[12:15], v[144:147], v[238:241], v[12:15]
	v_mfma_f32_16x16x32_bf16 v[8:11], v[152:155], v[238:241], v[8:11]
	v_mfma_f32_16x16x32_bf16 v[60:63], v[148:151], v[218:221], v[60:63]
	v_mfma_f32_16x16x32_bf16 v[56:59], v[156:159], v[218:221], v[56:59]
	v_mfma_f32_16x16x32_bf16 v[44:47], v[148:151], v[226:229], v[44:47]
	v_mfma_f32_16x16x32_bf16 v[40:43], v[156:159], v[226:229], v[40:43]
	v_mfma_f32_16x16x32_bf16 v[28:31], v[148:151], v[234:237], v[28:31]
	v_mfma_f32_16x16x32_bf16 v[24:27], v[156:159], v[234:237], v[24:27]
	v_mfma_f32_16x16x32_bf16 v[12:15], v[148:151], v[242:245], v[12:15]
	v_mfma_f32_16x16x32_bf16 v[8:11], v[156:159], v[242:245], v[8:11]
	s_setprio 0
	s_setprio 1
	v_mfma_f32_16x16x32_bf16 v[52:55], v[160:163], v[214:217], v[52:55]
	v_mfma_f32_16x16x32_bf16 v[48:51], v[206:209], v[214:217], v[48:51]
	v_mfma_f32_16x16x32_bf16 v[36:39], v[160:163], v[222:225], v[36:39]
	v_mfma_f32_16x16x32_bf16 v[32:35], v[206:209], v[222:225], v[32:35]
	v_mfma_f32_16x16x32_bf16 v[20:23], v[160:163], v[230:233], v[20:23]
	v_mfma_f32_16x16x32_bf16 v[16:19], v[206:209], v[230:233], v[16:19]
	v_mfma_f32_16x16x32_bf16 v[4:7], v[160:163], v[238:241], v[4:7]
	v_mfma_f32_16x16x32_bf16 v[0:3], v[206:209], v[238:241], v[0:3]
	v_mfma_f32_16x16x32_bf16 v[52:55], v[164:167], v[218:221], v[52:55]
	v_mfma_f32_16x16x32_bf16 v[48:51], v[210:213], v[218:221], v[48:51]
	v_mfma_f32_16x16x32_bf16 v[36:39], v[164:167], v[226:229], v[36:39]
	v_mfma_f32_16x16x32_bf16 v[32:35], v[210:213], v[226:229], v[32:35]
	v_mfma_f32_16x16x32_bf16 v[20:23], v[164:167], v[234:237], v[20:23]
	v_mfma_f32_16x16x32_bf16 v[16:19], v[210:213], v[234:237], v[16:19]
	v_mfma_f32_16x16x32_bf16 v[4:7], v[164:167], v[242:245], v[4:7]
	v_mfma_f32_16x16x32_bf16 v[0:3], v[210:213], v[242:245], v[0:3]
	s_setprio 0
	s_barrier
	s_add_i32 s69, 0, 0x18000
	s_add_i32 s70, 0, 0x1c000
	v_add_u32_e32 v156, s69, v171
	v_add_u32_e32 v176, s70, v171
	ds_read_b128 v[144:147], v156
	ds_read_b128 v[148:151], v156 offset:1024
	ds_read_b128 v[152:155], v156 offset:2048
	ds_read_b128 v[156:159], v156 offset:3072
	ds_read_b128 v[160:163], v176
	ds_read_b128 v[164:167], v176 offset:1024
	ds_read_b128 v[206:209], v176 offset:2048
	ds_read_b128 v[210:213], v176 offset:3072
	s_add_u32 s82, s82, 0x80000
	s_addc_u32 s83, s83, 0
	s_mov_b32 m0, s53
	ds_read_b128 v[214:217], v189 offset:32768
	ds_read_b128 v[218:221], v189 offset:33792
	ds_read_b128 v[222:225], v189 offset:34816
	ds_read_b128 v[226:229], v189 offset:35840
	ds_read_b128 v[230:233], v189 offset:36864
	ds_read_b128 v[234:237], v189 offset:37888
	ds_read_b128 v[238:241], v189 offset:38912
	ds_read_b128 v[242:245], v189 offset:39936
	global_load_lds_dwordx4 v128, s[82:83]
	s_mov_b32 m0, s94
	s_nop 0
	global_load_lds_dwordx4 v132, s[82:83]
	s_waitcnt vmcnt(8)
	s_waitcnt lgkmcnt(0)
	s_barrier
	s_setprio 1
	s_waitcnt lgkmcnt(0)
	v_mfma_f32_16x16x32_bf16 v[124:127], v[144:147], v[214:217], v[124:127]
	v_mfma_f32_16x16x32_bf16 v[120:123], v[152:155], v[214:217], v[120:123]
	v_mfma_f32_16x16x32_bf16 v[108:111], v[144:147], v[222:225], v[108:111]
	v_mfma_f32_16x16x32_bf16 v[104:107], v[152:155], v[222:225], v[104:107]
	v_mfma_f32_16x16x32_bf16 v[92:95], v[144:147], v[230:233], v[92:95]
	v_mfma_f32_16x16x32_bf16 v[88:91], v[152:155], v[230:233], v[88:91]
	v_mfma_f32_16x16x32_bf16 v[76:79], v[144:147], v[238:241], v[76:79]
	v_mfma_f32_16x16x32_bf16 v[72:75], v[152:155], v[238:241], v[72:75]
	v_mfma_f32_16x16x32_bf16 v[124:127], v[148:151], v[218:221], v[124:127]
	v_mfma_f32_16x16x32_bf16 v[120:123], v[156:159], v[218:221], v[120:123]
	v_mfma_f32_16x16x32_bf16 v[108:111], v[148:151], v[226:229], v[108:111]
	v_mfma_f32_16x16x32_bf16 v[104:107], v[156:159], v[226:229], v[104:107]
	v_mfma_f32_16x16x32_bf16 v[92:95], v[148:151], v[234:237], v[92:95]
	v_mfma_f32_16x16x32_bf16 v[88:91], v[156:159], v[234:237], v[88:91]
	v_mfma_f32_16x16x32_bf16 v[76:79], v[148:151], v[242:245], v[76:79]
	v_mfma_f32_16x16x32_bf16 v[72:75], v[156:159], v[242:245], v[72:75]
	s_setprio 0
	s_setprio 1
	v_mfma_f32_16x16x32_bf16 v[116:119], v[160:163], v[214:217], v[116:119]
	v_mfma_f32_16x16x32_bf16 v[112:115], v[206:209], v[214:217], v[112:115]
	v_mfma_f32_16x16x32_bf16 v[100:103], v[160:163], v[222:225], v[100:103]
	v_mfma_f32_16x16x32_bf16 v[96:99], v[206:209], v[222:225], v[96:99]
	v_mfma_f32_16x16x32_bf16 v[84:87], v[160:163], v[230:233], v[84:87]
	v_mfma_f32_16x16x32_bf16 v[80:83], v[206:209], v[230:233], v[80:83]
	v_mfma_f32_16x16x32_bf16 v[68:71], v[160:163], v[238:241], v[68:71]
	v_mfma_f32_16x16x32_bf16 v[64:67], v[206:209], v[238:241], v[64:67]
	v_mfma_f32_16x16x32_bf16 v[116:119], v[164:167], v[218:221], v[116:119]
	v_mfma_f32_16x16x32_bf16 v[112:115], v[210:213], v[218:221], v[112:115]
	v_mfma_f32_16x16x32_bf16 v[100:103], v[164:167], v[226:229], v[100:103]
	v_mfma_f32_16x16x32_bf16 v[96:99], v[210:213], v[226:229], v[96:99]
	v_mfma_f32_16x16x32_bf16 v[84:87], v[164:167], v[234:237], v[84:87]
	v_mfma_f32_16x16x32_bf16 v[80:83], v[210:213], v[234:237], v[80:83]
	v_mfma_f32_16x16x32_bf16 v[68:71], v[164:167], v[242:245], v[68:71]
	v_mfma_f32_16x16x32_bf16 v[64:67], v[210:213], v[242:245], v[64:67]
	s_setprio 0
	s_barrier
	s_add_i32 s69, s69, s23
	s_mov_b32 m0, s69
	ds_read_b128 v[214:217], v189 offset:49152
	ds_read_b128 v[218:221], v189 offset:50176
	ds_read_b128 v[222:225], v189 offset:51200
	ds_read_b128 v[226:229], v189 offset:52224
	ds_read_b128 v[230:233], v189 offset:53248
	ds_read_b128 v[234:237], v189 offset:54272
	ds_read_b128 v[238:241], v189 offset:55296
	ds_read_b128 v[242:245], v189 offset:56320
	s_add_u32 s84, s48, 0x80
	s_addc_u32 s85, s49, 0
	global_load_lds_dwordx4 v130, s[84:85]
	s_add_i32 m0, s69, 0x2000
	s_add_u32 s48, s48, 0x80080
	s_addc_u32 s49, s49, 0
	s_add_i32 s69, s70, s23
	s_add_u32 s84, s48, 0xfff80000
	s_addc_u32 s85, s49, -1
	global_load_lds_dwordx4 v134, s[84:85]
	s_mov_b32 m0, s69
	s_nop 0
	global_load_lds_dwordx4 v130, s[48:49]
	s_add_i32 m0, s69, 0x2000
	s_nop 0
	global_load_lds_dwordx4 v134, s[48:49]
	s_mov_b32 m0, s18
	s_nop 0
	s_add_u32 s84, s82, 0xfff80080
	s_addc_u32 s85, s83, -1
	global_load_lds_dwordx4 v128, s[84:85]
	s_mov_b32 m0, s72
	s_nop 0
	s_add_u32 s84, s82, 0xfff80080
	s_addc_u32 s85, s83, -1
	global_load_lds_dwordx4 v132, s[84:85]
	s_waitcnt vmcnt(8)
	s_waitcnt lgkmcnt(0)
	s_barrier
	s_setprio 1
	s_waitcnt lgkmcnt(0)
	v_mfma_f32_16x16x32_bf16 v[60:63], v[144:147], v[214:217], v[60:63]
	v_mfma_f32_16x16x32_bf16 v[56:59], v[152:155], v[214:217], v[56:59]
	v_mfma_f32_16x16x32_bf16 v[44:47], v[144:147], v[222:225], v[44:47]
	v_mfma_f32_16x16x32_bf16 v[40:43], v[152:155], v[222:225], v[40:43]
	v_mfma_f32_16x16x32_bf16 v[28:31], v[144:147], v[230:233], v[28:31]
	v_mfma_f32_16x16x32_bf16 v[24:27], v[152:155], v[230:233], v[24:27]
	v_mfma_f32_16x16x32_bf16 v[12:15], v[144:147], v[238:241], v[12:15]
	v_mfma_f32_16x16x32_bf16 v[8:11], v[152:155], v[238:241], v[8:11]
	v_mfma_f32_16x16x32_bf16 v[60:63], v[148:151], v[218:221], v[60:63]
	v_mfma_f32_16x16x32_bf16 v[56:59], v[156:159], v[218:221], v[56:59]
	v_mfma_f32_16x16x32_bf16 v[44:47], v[148:151], v[226:229], v[44:47]
	v_mfma_f32_16x16x32_bf16 v[40:43], v[156:159], v[226:229], v[40:43]
	v_mfma_f32_16x16x32_bf16 v[28:31], v[148:151], v[234:237], v[28:31]
	v_mfma_f32_16x16x32_bf16 v[24:27], v[156:159], v[234:237], v[24:27]
	v_mfma_f32_16x16x32_bf16 v[12:15], v[148:151], v[242:245], v[12:15]
	v_mfma_f32_16x16x32_bf16 v[8:11], v[156:159], v[242:245], v[8:11]
	s_setprio 0
	s_setprio 1
	v_mfma_f32_16x16x32_bf16 v[52:55], v[160:163], v[214:217], v[52:55]
	v_mfma_f32_16x16x32_bf16 v[48:51], v[206:209], v[214:217], v[48:51]
	v_mfma_f32_16x16x32_bf16 v[36:39], v[160:163], v[222:225], v[36:39]
	v_mfma_f32_16x16x32_bf16 v[32:35], v[206:209], v[222:225], v[32:35]
	v_mfma_f32_16x16x32_bf16 v[20:23], v[160:163], v[230:233], v[20:23]
	v_mfma_f32_16x16x32_bf16 v[16:19], v[206:209], v[230:233], v[16:19]
	v_mfma_f32_16x16x32_bf16 v[4:7], v[160:163], v[238:241], v[4:7]
	v_mfma_f32_16x16x32_bf16 v[0:3], v[206:209], v[238:241], v[0:3]
	v_mfma_f32_16x16x32_bf16 v[52:55], v[164:167], v[218:221], v[52:55]
	v_mfma_f32_16x16x32_bf16 v[48:51], v[210:213], v[218:221], v[48:51]
	v_mfma_f32_16x16x32_bf16 v[36:39], v[164:167], v[226:229], v[36:39]
	v_mfma_f32_16x16x32_bf16 v[32:35], v[210:213], v[226:229], v[32:35]
	v_mfma_f32_16x16x32_bf16 v[20:23], v[164:167], v[234:237], v[20:23]
	v_mfma_f32_16x16x32_bf16 v[16:19], v[210:213], v[234:237], v[16:19]
	v_mfma_f32_16x16x32_bf16 v[4:7], v[164:167], v[242:245], v[4:7]
	v_mfma_f32_16x16x32_bf16 v[0:3], v[210:213], v[242:245], v[0:3]
	s_setprio 0
	s_barrier
	s_add_i32 s67, s67, 2
	s_add_u32 s46, s46, 0x100
	s_addc_u32 s47, s47, 0
	s_add_u32 s14, s14, 0x100
	s_addc_u32 s15, s15, 0
	s_cmp_gt_u32 s67, 29
	s_cbranch_scc0 .LBB0_823
	s_and_b64 vcc, exec, s[64:65]
	s_cbranch_vccz .LBB0_826
	s_barrier

.LBB0_861:
	s_andn2_saveexec_b64 s[44:45], s[14:15]
	s_cbranch_execz .LBB0_863
	v_ashrrev_i32_e32 v122, 1, v144
	v_ashrrev_i32_e32 v123, 31, v122
	v_lshl_add_u64 v[160:161], s[28:29], 0, v[146:147]
	v_lshl_add_u64 v[122:123], v[122:123], 3, v[160:161]
	global_load_dwordx4 v[160:163], v[122:123], off offset:16
	global_load_dwordx4 v[164:167], v[122:123], off
	s_waitcnt vmcnt(0)
	v_pk_mul_f32 v[122:123], v[158:159], v[166:167]
	v_pk_mul_f32 v[168:169], v[124:125], v[164:165]
	v_pk_mul_f32 v[124:125], v[124:125], v[164:165] op_sel:[0,1] op_sel_hi:[1,0]
	v_sub_f32_e32 v164, v122, v123
	v_add_f32_e32 v157, v124, v125
	v_pk_mul_f32 v[122:123], v[158:159], v[166:167] op_sel:[0,1] op_sel_hi:[1,0]
	v_pk_mul_f32 v[124:125], v[120:121], v[160:161]
	v_pk_mul_f32 v[120:121], v[120:121], v[160:161] op_sel:[0,1] op_sel_hi:[1,0]
	v_sub_f32_e32 v145, v168, v169
	v_add_f32_e32 v158, v122, v123
	v_pk_mul_f32 v[122:123], v[126:127], v[162:163]
	v_sub_f32_e32 v124, v124, v125
	v_add_f32_e32 v125, v120, v121
	v_pk_mul_f32 v[120:121], v[126:127], v[162:163] op_sel:[0,1] op_sel_hi:[1,0]
	v_sub_f32_e32 v123, v122, v123
	v_add_f32_e32 v126, v120, v121
	v_cvt_pk_bf16_f32 v120, v145, v157
	v_cvt_pk_bf16_f32 v121, v164, v158
	v_cvt_pk_bf16_f32 v122, v124, v125
	v_ashrrev_i32_e32 v145, 31, v144
	v_lshl_add_u32 v124, v144, 1, v150
	v_bfe_u32 v125, v124, 7, 4
	v_bfe_u32 v250, v124, 4, 3
	v_lshl_or_b32 v125, v250, 4, v125
	v_and_b32_e32 v124, 0xfffff80f, v124
	v_lshl_or_b32 v124, v125, 4, v124
	v_mov_b32_e32 v125, 0
	v_lshl_add_u64 v[124:125], s[56:57], 0, v[124:125]
	v_cvt_pk_bf16_f32 v123, v123, v126
	global_store_dwordx4 v[124:125], v[120:123], off

.LBB0_911:
	s_andn2_saveexec_b64 s[48:49], s[14:15]
	s_cbranch_execz .LBB0_913
	v_ashrrev_i32_e32 v106, 1, v144
	v_ashrrev_i32_e32 v107, 31, v106
	v_lshl_add_u64 v[126:127], s[28:29], 0, v[112:113]
	v_lshl_add_u64 v[106:107], v[106:107], 3, v[126:127]
	global_load_dwordx4 v[146:149], v[106:107], off offset:16
	global_load_dwordx4 v[150:153], v[106:107], off
	v_ashrrev_i32_e32 v145, 31, v144
	s_waitcnt vmcnt(0)
	v_pk_mul_f32 v[106:107], v[124:125], v[152:153]
	v_pk_mul_f32 v[126:127], v[108:109], v[150:151]
	v_pk_mul_f32 v[108:109], v[108:109], v[150:151] op_sel:[0,1] op_sel_hi:[1,0]
	v_sub_f32_e32 v123, v126, v127
	v_add_f32_e32 v126, v108, v109
	v_sub_f32_e32 v127, v106, v107
	v_pk_mul_f32 v[106:107], v[124:125], v[152:153] op_sel:[0,1] op_sel_hi:[1,0]
	v_pk_mul_f32 v[108:109], v[104:105], v[146:147]
	v_pk_mul_f32 v[104:105], v[104:105], v[146:147] op_sel:[0,1] op_sel_hi:[1,0]
	v_add_f32_e32 v124, v106, v107
	v_pk_mul_f32 v[106:107], v[110:111], v[148:149]
	v_sub_f32_e32 v108, v108, v109
	v_add_f32_e32 v109, v104, v105
	v_pk_mul_f32 v[104:105], v[110:111], v[148:149] op_sel:[0,1] op_sel_hi:[1,0]
	v_sub_f32_e32 v107, v106, v107
	v_add_f32_e32 v110, v104, v105
	v_cvt_pk_bf16_f32 v104, v123, v126
	v_cvt_pk_bf16_f32 v105, v127, v124
	v_cvt_pk_bf16_f32 v106, v108, v109
	v_lshl_add_u32 v108, v144, 1, v116
	v_bfe_u32 v109, v108, 7, 4
	v_bfe_u32 v250, v108, 4, 3
	v_lshl_or_b32 v109, v250, 4, v109
	v_and_b32_e32 v108, 0xfffff80f, v108
	v_lshl_or_b32 v108, v109, 4, v108
	v_mov_b32_e32 v109, 0
	v_lshl_add_u64 v[108:109], s[56:57], 0, v[108:109]
	v_cvt_pk_bf16_f32 v107, v107, v110
	global_store_dwordx4 v[108:109], v[104:107], off

.LBB0_959:
	s_andn2_saveexec_b64 s[48:49], s[14:15]
	s_cbranch_execz .LBB0_961
	v_ashrrev_i32_e32 v90, 1, v144
	v_ashrrev_i32_e32 v91, 31, v90
	v_lshl_add_u64 v[110:111], s[28:29], 0, v[96:97]
	v_lshl_add_u64 v[90:91], v[90:91], 3, v[110:111]
	global_load_dwordx4 v[110:113], v[90:91], off offset:16
	global_load_dwordx4 v[114:117], v[90:91], off
	v_ashrrev_i32_e32 v145, 31, v144
	s_waitcnt vmcnt(0)
	v_pk_mul_f32 v[90:91], v[108:109], v[116:117]
	v_pk_mul_f32 v[118:119], v[92:93], v[114:115]
	v_pk_mul_f32 v[92:93], v[92:93], v[114:115] op_sel:[0,1] op_sel_hi:[1,0]
	v_sub_f32_e32 v115, v90, v91
	v_add_f32_e32 v114, v92, v93
	v_pk_mul_f32 v[90:91], v[108:109], v[116:117] op_sel:[0,1] op_sel_hi:[1,0]
	v_pk_mul_f32 v[92:93], v[88:89], v[110:111]
	v_pk_mul_f32 v[88:89], v[88:89], v[110:111] op_sel:[0,1] op_sel_hi:[1,0]
	v_add_f32_e32 v108, v90, v91
	v_pk_mul_f32 v[90:91], v[94:95], v[112:113]
	v_sub_f32_e32 v92, v92, v93
	v_add_f32_e32 v93, v88, v89
	v_pk_mul_f32 v[88:89], v[94:95], v[112:113] op_sel:[0,1] op_sel_hi:[1,0]
	v_sub_f32_e32 v107, v118, v119
	v_sub_f32_e32 v91, v90, v91
	v_add_f32_e32 v94, v88, v89
	v_cvt_pk_bf16_f32 v88, v107, v114
	v_cvt_pk_bf16_f32 v89, v115, v108
	v_cvt_pk_bf16_f32 v90, v92, v93
	v_lshl_add_u32 v92, v144, 1, v100
	v_bfe_u32 v93, v92, 7, 4
	v_bfe_u32 v250, v92, 4, 3
	v_lshl_or_b32 v93, v250, 4, v93
	v_and_b32_e32 v92, 0xfffff80f, v92
	v_lshl_or_b32 v92, v93, 4, v92
	v_mov_b32_e32 v93, 0
	v_lshl_add_u64 v[92:93], s[56:57], 0, v[92:93]
	v_cvt_pk_bf16_f32 v91, v91, v94
	global_store_dwordx4 v[92:93], v[88:91], off

.LBB0_1007:
	s_andn2_saveexec_b64 s[48:49], s[14:15]
	s_cbranch_execz .LBB0_1009
	v_ashrrev_i32_e32 v74, 1, v144
	v_ashrrev_i32_e32 v75, 31, v74
	v_lshl_add_u64 v[94:95], s[28:29], 0, v[80:81]
	v_lshl_add_u64 v[74:75], v[74:75], 3, v[94:95]
	global_load_dwordx4 v[94:97], v[74:75], off offset:16
	global_load_dwordx4 v[98:101], v[74:75], off
	v_ashrrev_i32_e32 v145, 31, v144
	s_waitcnt vmcnt(0)
	v_pk_mul_f32 v[74:75], v[92:93], v[100:101]
	v_pk_mul_f32 v[102:103], v[76:77], v[98:99]
	v_pk_mul_f32 v[76:77], v[76:77], v[98:99] op_sel:[0,1] op_sel_hi:[1,0]
	v_sub_f32_e32 v99, v74, v75
	v_add_f32_e32 v98, v76, v77
	v_pk_mul_f32 v[74:75], v[92:93], v[100:101] op_sel:[0,1] op_sel_hi:[1,0]
	v_pk_mul_f32 v[76:77], v[72:73], v[94:95]
	v_pk_mul_f32 v[72:73], v[72:73], v[94:95] op_sel:[0,1] op_sel_hi:[1,0]
	v_add_f32_e32 v92, v74, v75
	v_pk_mul_f32 v[74:75], v[78:79], v[96:97]
	v_sub_f32_e32 v76, v76, v77
	v_add_f32_e32 v77, v72, v73
	v_pk_mul_f32 v[72:73], v[78:79], v[96:97] op_sel:[0,1] op_sel_hi:[1,0]
	v_sub_f32_e32 v91, v102, v103
	v_sub_f32_e32 v75, v74, v75
	v_add_f32_e32 v78, v72, v73
	v_cvt_pk_bf16_f32 v72, v91, v98
	v_cvt_pk_bf16_f32 v73, v99, v92
	v_cvt_pk_bf16_f32 v74, v76, v77
	v_lshl_add_u32 v76, v144, 1, v84
	v_bfe_u32 v77, v76, 7, 4
	v_bfe_u32 v250, v76, 4, 3
	v_lshl_or_b32 v77, v250, 4, v77
	v_and_b32_e32 v76, 0xfffff80f, v76
	v_lshl_or_b32 v76, v77, 4, v76
	v_mov_b32_e32 v77, 0
	v_lshl_add_u64 v[76:77], s[56:57], 0, v[76:77]
	v_cvt_pk_bf16_f32 v75, v75, v78
	global_store_dwordx4 v[76:77], v[72:75], off

.LBB0_1055:
	s_andn2_saveexec_b64 s[48:49], s[14:15]
	s_cbranch_execz .LBB0_1057
	v_ashrrev_i32_e32 v58, 1, v144
	v_ashrrev_i32_e32 v59, 31, v58
	v_lshl_add_u64 v[78:79], s[28:29], 0, v[64:65]
	v_lshl_add_u64 v[58:59], v[58:59], 3, v[78:79]
	global_load_dwordx4 v[78:81], v[58:59], off offset:16
	global_load_dwordx4 v[82:85], v[58:59], off
	v_ashrrev_i32_e32 v145, 31, v144
	s_waitcnt vmcnt(0)
	v_pk_mul_f32 v[58:59], v[76:77], v[84:85]
	v_pk_mul_f32 v[86:87], v[60:61], v[82:83]
	v_pk_mul_f32 v[60:61], v[60:61], v[82:83] op_sel:[0,1] op_sel_hi:[1,0]
	v_sub_f32_e32 v83, v58, v59
	v_add_f32_e32 v82, v60, v61
	v_pk_mul_f32 v[58:59], v[76:77], v[84:85] op_sel:[0,1] op_sel_hi:[1,0]
	v_pk_mul_f32 v[60:61], v[56:57], v[78:79]
	v_pk_mul_f32 v[56:57], v[56:57], v[78:79] op_sel:[0,1] op_sel_hi:[1,0]
	v_add_f32_e32 v76, v58, v59
	v_pk_mul_f32 v[58:59], v[62:63], v[80:81]
	v_sub_f32_e32 v60, v60, v61
	v_add_f32_e32 v61, v56, v57
	v_pk_mul_f32 v[56:57], v[62:63], v[80:81] op_sel:[0,1] op_sel_hi:[1,0]
	v_sub_f32_e32 v75, v86, v87
	v_sub_f32_e32 v59, v58, v59
	v_add_f32_e32 v62, v56, v57
	v_cvt_pk_bf16_f32 v56, v75, v82
	v_cvt_pk_bf16_f32 v57, v83, v76
	v_cvt_pk_bf16_f32 v58, v60, v61
	v_lshl_add_u32 v60, v144, 1, v68
	v_bfe_u32 v61, v60, 7, 4
	v_bfe_u32 v250, v60, 4, 3
	v_lshl_or_b32 v61, v250, 4, v61
	v_and_b32_e32 v60, 0xfffff80f, v60
	v_lshl_or_b32 v60, v61, 4, v60
	v_mov_b32_e32 v61, 0
	v_lshl_add_u64 v[60:61], s[56:57], 0, v[60:61]
	v_cvt_pk_bf16_f32 v59, v59, v62
	global_store_dwordx4 v[60:61], v[56:59], off

.LBB0_1103:
	s_andn2_saveexec_b64 s[48:49], s[14:15]
	s_cbranch_execz .LBB0_1105
	v_ashrrev_i32_e32 v42, 1, v144
	v_ashrrev_i32_e32 v43, 31, v42
	v_lshl_add_u64 v[62:63], s[28:29], 0, v[48:49]
	v_lshl_add_u64 v[42:43], v[42:43], 3, v[62:63]
	global_load_dwordx4 v[62:65], v[42:43], off offset:16
	global_load_dwordx4 v[66:69], v[42:43], off
	v_ashrrev_i32_e32 v145, 31, v144
	s_waitcnt vmcnt(0)
	v_pk_mul_f32 v[42:43], v[60:61], v[68:69]
	v_pk_mul_f32 v[70:71], v[44:45], v[66:67]
	v_pk_mul_f32 v[44:45], v[44:45], v[66:67] op_sel:[0,1] op_sel_hi:[1,0]
	v_sub_f32_e32 v67, v42, v43
	v_add_f32_e32 v66, v44, v45
	v_pk_mul_f32 v[42:43], v[60:61], v[68:69] op_sel:[0,1] op_sel_hi:[1,0]
	v_pk_mul_f32 v[44:45], v[40:41], v[62:63]
	v_pk_mul_f32 v[40:41], v[40:41], v[62:63] op_sel:[0,1] op_sel_hi:[1,0]
	v_add_f32_e32 v60, v42, v43
	v_pk_mul_f32 v[42:43], v[46:47], v[64:65]
	v_sub_f32_e32 v44, v44, v45
	v_add_f32_e32 v45, v40, v41
	v_pk_mul_f32 v[40:41], v[46:47], v[64:65] op_sel:[0,1] op_sel_hi:[1,0]
	v_sub_f32_e32 v59, v70, v71
	v_sub_f32_e32 v43, v42, v43
	v_add_f32_e32 v46, v40, v41
	v_cvt_pk_bf16_f32 v40, v59, v66
	v_cvt_pk_bf16_f32 v41, v67, v60
	v_cvt_pk_bf16_f32 v42, v44, v45
	v_lshl_add_u32 v44, v144, 1, v52
	v_bfe_u32 v45, v44, 7, 4
	v_bfe_u32 v250, v44, 4, 3
	v_lshl_or_b32 v45, v250, 4, v45
	v_and_b32_e32 v44, 0xfffff80f, v44
	v_lshl_or_b32 v44, v45, 4, v44
	v_mov_b32_e32 v45, 0
	v_lshl_add_u64 v[44:45], s[56:57], 0, v[44:45]
	v_cvt_pk_bf16_f32 v43, v43, v46
	global_store_dwordx4 v[44:45], v[40:43], off

.LBB0_1151:
	s_andn2_saveexec_b64 s[48:49], s[14:15]
	s_cbranch_execz .LBB0_1153
	v_ashrrev_i32_e32 v26, 1, v144
	v_ashrrev_i32_e32 v27, 31, v26
	v_lshl_add_u64 v[46:47], s[28:29], 0, v[32:33]
	v_lshl_add_u64 v[26:27], v[26:27], 3, v[46:47]
	global_load_dwordx4 v[46:49], v[26:27], off offset:16
	global_load_dwordx4 v[50:53], v[26:27], off
	v_ashrrev_i32_e32 v145, 31, v144
	s_waitcnt vmcnt(0)
	v_pk_mul_f32 v[26:27], v[44:45], v[52:53]
	v_pk_mul_f32 v[54:55], v[28:29], v[50:51]
	v_pk_mul_f32 v[28:29], v[28:29], v[50:51] op_sel:[0,1] op_sel_hi:[1,0]
	v_sub_f32_e32 v51, v26, v27
	v_add_f32_e32 v50, v28, v29
	v_pk_mul_f32 v[26:27], v[44:45], v[52:53] op_sel:[0,1] op_sel_hi:[1,0]
	v_pk_mul_f32 v[28:29], v[24:25], v[46:47]
	v_pk_mul_f32 v[24:25], v[24:25], v[46:47] op_sel:[0,1] op_sel_hi:[1,0]
	v_add_f32_e32 v44, v26, v27
	v_pk_mul_f32 v[26:27], v[30:31], v[48:49]
	v_sub_f32_e32 v28, v28, v29
	v_add_f32_e32 v29, v24, v25
	v_pk_mul_f32 v[24:25], v[30:31], v[48:49] op_sel:[0,1] op_sel_hi:[1,0]
	v_sub_f32_e32 v43, v54, v55
	v_sub_f32_e32 v27, v26, v27
	v_add_f32_e32 v30, v24, v25
	v_cvt_pk_bf16_f32 v24, v43, v50
	v_cvt_pk_bf16_f32 v25, v51, v44
	v_cvt_pk_bf16_f32 v26, v28, v29
	v_lshl_add_u32 v28, v144, 1, v36
	v_bfe_u32 v29, v28, 7, 4
	v_bfe_u32 v250, v28, 4, 3
	v_lshl_or_b32 v29, v250, 4, v29
	v_and_b32_e32 v28, 0xfffff80f, v28
	v_lshl_or_b32 v28, v29, 4, v28
	v_mov_b32_e32 v29, 0
	v_lshl_add_u64 v[28:29], s[56:57], 0, v[28:29]
	v_cvt_pk_bf16_f32 v27, v27, v30
	global_store_dwordx4 v[28:29], v[24:27], off

.LBB0_1199:
	s_andn2_saveexec_b64 s[30:31], s[14:15]
	s_cbranch_execz .LBB0_1201
	v_ashrrev_i32_e32 v10, 1, v144
	v_ashrrev_i32_e32 v11, 31, v10
	v_lshl_add_u64 v[30:31], s[28:29], 0, v[16:17]
	v_lshl_add_u64 v[10:11], v[10:11], 3, v[30:31]
	global_load_dwordx4 v[30:33], v[10:11], off offset:16
	global_load_dwordx4 v[34:37], v[10:11], off
	v_ashrrev_i32_e32 v145, 31, v144
	s_waitcnt vmcnt(0)
	v_pk_mul_f32 v[10:11], v[28:29], v[36:37]
	v_pk_mul_f32 v[38:39], v[12:13], v[34:35]
	v_pk_mul_f32 v[12:13], v[12:13], v[34:35] op_sel:[0,1] op_sel_hi:[1,0]
	v_sub_f32_e32 v35, v10, v11
	v_add_f32_e32 v34, v12, v13
	v_pk_mul_f32 v[10:11], v[28:29], v[36:37] op_sel:[0,1] op_sel_hi:[1,0]
	v_pk_mul_f32 v[12:13], v[8:9], v[30:31]
	v_pk_mul_f32 v[8:9], v[8:9], v[30:31] op_sel:[0,1] op_sel_hi:[1,0]
	v_add_f32_e32 v28, v10, v11
	v_pk_mul_f32 v[10:11], v[14:15], v[32:33]
	v_sub_f32_e32 v12, v12, v13
	v_add_f32_e32 v13, v8, v9
	v_pk_mul_f32 v[8:9], v[14:15], v[32:33] op_sel:[0,1] op_sel_hi:[1,0]
	v_sub_f32_e32 v27, v38, v39
	v_sub_f32_e32 v11, v10, v11
	v_add_f32_e32 v14, v8, v9
	v_cvt_pk_bf16_f32 v8, v27, v34
	v_cvt_pk_bf16_f32 v9, v35, v28
	v_cvt_pk_bf16_f32 v10, v12, v13
	v_lshl_add_u32 v12, v144, 1, v20
	v_bfe_u32 v13, v12, 7, 4
	v_bfe_u32 v250, v12, 4, 3
	v_lshl_or_b32 v13, v250, 4, v13
	v_and_b32_e32 v12, 0xfffff80f, v12
	v_lshl_or_b32 v12, v13, 4, v12
	v_mov_b32_e32 v13, 0
	v_lshl_add_u64 v[12:13], s[56:57], 0, v[12:13]
	v_cvt_pk_bf16_f32 v11, v11, v14
	global_store_dwordx4 v[12:13], v[8:11], off

.LBB0_1302:
	s_and_b64 s[14:15], s[28:29], exec
	s_cselect_b32 s14, s77, s76
	s_lshl_b32 s34, s14, 4
	s_mov_b32 s14, s33
	s_nop 0
	v_lshl_or_b32 v72, s14, 6, v195
	s_nop 0
	v_readfirstlane_b32 s14, v72
	s_ashr_i32 s30, s14, 6
	s_and_b32 s14, s34, 0xffffffc0
	s_add_i32 s14, s14, 64
	s_ashr_i32 s82, s14, 5
	v_and_b32_e32 v126, 63, v72
	v_and_b32_e32 v125, 15, v72
	s_cmpk_gt_i32 s14, 0x100
	s_mov_b64 s[14:15], -1
	s_cbranch_scc0 .LBB0_1545
	v_or_b32_e32 v0, s34, v125
	v_ashrrev_i32_e32 v1, 31, v0
	v_lshlrev_b64 v[2:3], 10, v[0:1]
	v_lshl_add_u64 v[2:3], s[26:27], 0, v[2:3]
	v_and_b32_e32 v176, 48, v126
	v_lshlrev_b64 v[0:1], 5, v[0:1]
	v_lshl_add_u64 v[68:69], v[2:3], 0, v[176:177]
	v_lshl_add_u64 v[12:13], s[24:25], 0, v[0:1]
	global_load_dwordx4 v[0:3], v[68:69], off
	global_load_dwordx4 v[4:7], v[68:69], off offset:64
	global_load_dwordx4 v[8:11], v[12:13], off offset:16
	s_nop 0
	global_load_dwordx4 v[12:15], v[12:13], off
	s_nop 0
	global_load_dwordx4 v[16:19], v[68:69], off offset:128
	global_load_dwordx4 v[20:23], v[68:69], off offset:192
	global_load_dwordx4 v[24:27], v[68:69], off offset:256
	global_load_dwordx4 v[28:31], v[68:69], off offset:320
	global_load_dwordx4 v[32:35], v[68:69], off offset:384
	global_load_dwordx4 v[36:39], v[68:69], off offset:448
	global_load_dwordx4 v[40:43], v[68:69], off offset:512
	global_load_dwordx4 v[44:47], v[68:69], off offset:576
	global_load_dwordx4 v[48:51], v[68:69], off offset:640
	global_load_dwordx4 v[52:55], v[68:69], off offset:704
	global_load_dwordx4 v[56:59], v[68:69], off offset:768
	global_load_dwordx4 v[60:63], v[68:69], off offset:832
	global_load_dwordx4 v[64:67], v[68:69], off offset:896
	s_nop 0
	global_load_dwordx4 v[68:71], v[68:69], off offset:960
	s_mov_b32 s74, s73
	s_mov_b32 s75, s73
	v_lshlrev_b32_e32 v73, 4, v72
	s_mov_b32 s72, s73
	v_mov_b64_e32 v[76:77], s[74:75]
	v_add_u32_e32 v122, 0, v73
	v_mov_b64_e32 v[74:75], s[72:73]
	v_cmp_gt_i32_e32 vcc, 17, v72
	s_waitcnt vmcnt(0)
	s_barrier
	ds_write_b128 v122, v[74:77]
	ds_write_b128 v122, v[74:77] offset:8192
	ds_write_b128 v122, v[74:77] offset:16384
	ds_write_b128 v122, v[74:77] offset:24576
	ds_write_b128 v122, v[74:77] offset:32768
	ds_write_b128 v122, v[74:77] offset:40960
	ds_write_b128 v122, v[74:77] offset:49152
	ds_write_b128 v122, v[74:77] offset:57344
	s_and_saveexec_b64 s[14:15], vcc
	v_lshl_add_u32 v72, v72, 2, s3
	ds_write_b32 v72, v177 offset:192
	s_or_b64 exec, exec, s[14:15]
	s_lshl_b32 s83, s30, 5
	v_or_b32_e32 v72, s83, v125
	v_lshrrev_b32_e32 v127, 4, v126
	v_ashrrev_i32_e32 v73, 31, v72
	v_lshlrev_b32_e32 v74, 3, v127
	v_mul_u32_u24_e32 v229, 0x70, v125
	v_lshlrev_b64 v[72:73], 7, v[72:73]
	v_sub_u32_e32 v72, v72, v229
	v_lshl_add_u64 v[72:73], s[22:23], 0, v[72:73]
	v_lshlrev_b32_e32 v176, 5, v74
	v_lshl_add_u64 v[72:73], v[72:73], 0, v[176:177]
	s_waitcnt lgkmcnt(0)
	s_barrier
	global_load_dwordx4 v[100:103], v[72:73], off
	global_load_dwordx4 v[96:99], v[72:73], off offset:1024
	global_load_dwordx4 v[92:95], v[72:73], off offset:2048
	global_load_dwordx4 v[88:91], v[72:73], off offset:3072
	s_cmp_lt_i32 s30, s82
	v_lshl_add_u32 v128, v125, 12, 0
	s_cselect_b64 s[36:37], -1, 0
	s_cmp_ge_i32 s30, s82
	v_lshl_add_u64 v[120:121], s[22:23], 0, v[176:177]
	s_cbranch_scc1 .LBB0_1310
	s_waitcnt vmcnt(0)
	v_mov_b64_e32 v[106:107], v[90:91]
	s_add_i32 s14, s82, -1
	s_mov_b32 s15, s30
	v_mov_b64_e32 v[104:105], v[88:89]
	v_mov_b32_e32 v116, v100
	v_mov_b32_e32 v117, v101
	v_mov_b32_e32 v118, v102
	v_mov_b32_e32 v119, v103
	v_mov_b32_e32 v108, v96
	v_mov_b32_e32 v109, v97
	v_mov_b32_e32 v110, v98
	v_mov_b32_e32 v111, v99
	v_mov_b32_e32 v112, v92
	v_mov_b32_e32 v113, v93
	v_mov_b32_e32 v114, v94
	v_mov_b32_e32 v115, v95
	s_branch .LBB0_1308

.LBB0_1308:
	s_waitcnt vmcnt(3)
	v_mfma_f32_16x16x32_bf16 v[130:133], v[116:119], v[0:3], 0
	s_add_i32 s31, s15, 8
	s_min_i32 s35, s31, s14
	v_lshl_or_b32 v72, s35, 5, v125
	s_waitcnt vmcnt(1)
	v_mfma_f32_16x16x32_bf16 v[134:137], v[112:115], v[0:3], 0
	v_ashrrev_i32_e32 v73, 31, v72
	v_lshlrev_b64 v[72:73], 7, v[72:73]
	v_sub_u32_e32 v72, v72, v229
	v_lshl_add_u64 v[84:85], v[120:121], 0, v[72:73]
	v_mfma_f32_16x16x32_bf16 v[138:141], v[108:111], v[4:7], v[130:133]
	global_load_dwordx4 v[72:75], v[84:85], off
	global_load_dwordx4 v[76:79], v[84:85], off offset:1024
	global_load_dwordx4 v[80:83], v[84:85], off offset:2048
	s_nop 0
	global_load_dwordx4 v[84:87], v[84:85], off offset:3072
	v_mov_b32_e32 v131, 0
	s_add_i32 s15, s15, 16
	s_waitcnt vmcnt(4)
	v_mfma_f32_16x16x32_bf16 v[132:135], v[104:107], v[4:7], v[134:137]
	v_max_i32_e32 v123, 0, v138
	v_fmac_f32_e32 v131, v12, v123
	v_mov_b32_e32 v123, 0
	s_min_i32 s35, s15, s14
	s_cmp_ge_i32 s31, s82
	s_nop 3
	v_max_i32_e32 v124, 0, v132
	v_fmac_f32_e32 v123, v12, v124
	v_max_i32_e32 v124, 0, v139
	v_mov_b32_e32 v132, 0
	v_fmac_f32_e32 v132, v12, v124
	v_max_i32_e32 v129, 0, v133
	v_mov_b32_e32 v124, 0
	v_fmac_f32_e32 v124, v12, v129
	v_max_i32_e32 v129, 0, v140
	v_mov_b32_e32 v133, 0
	v_fmac_f32_e32 v133, v12, v129
	v_max_i32_e32 v130, 0, v134
	v_mov_b32_e32 v129, 0
	v_mfma_f32_16x16x32_bf16 v[136:139], v[116:119], v[16:19], 0
	v_fmac_f32_e32 v129, v12, v130
	v_max_i32_e32 v130, 0, v141
	v_mov_b32_e32 v134, 0
	v_mfma_f32_16x16x32_bf16 v[140:143], v[112:115], v[16:19], 0
	v_fmac_f32_e32 v134, v12, v130
	v_max_i32_e32 v135, 0, v135
	v_mov_b32_e32 v130, 0
	v_mfma_f32_16x16x32_bf16 v[136:139], v[108:111], v[20:23], v[136:139]
	v_fmac_f32_e32 v130, v12, v135
	v_mfma_f32_16x16x32_bf16 v[140:143], v[104:107], v[20:23], v[140:143]
	s_nop 6
	v_max_i32_e32 v135, 0, v136
	v_fmac_f32_e32 v131, v13, v135
	v_max_i32_e32 v135, 0, v140
	v_fmac_f32_e32 v123, v13, v135
	v_max_i32_e32 v135, 0, v137
	v_fmac_f32_e32 v132, v13, v135
	v_max_i32_e32 v135, 0, v141
	v_fmac_f32_e32 v124, v13, v135
	v_max_i32_e32 v135, 0, v138
	v_fmac_f32_e32 v133, v13, v135
	v_max_i32_e32 v135, 0, v142
	v_fmac_f32_e32 v129, v13, v135
	v_max_i32_e32 v135, 0, v139
	v_mfma_f32_16x16x32_bf16 v[136:139], v[116:119], v[24:27], 0
	v_fmac_f32_e32 v134, v13, v135
	v_max_i32_e32 v135, 0, v143
	v_fmac_f32_e32 v130, v13, v135
	v_mfma_f32_16x16x32_bf16 v[140:143], v[112:115], v[24:27], 0
	v_mfma_f32_16x16x32_bf16 v[136:139], v[108:111], v[28:31], v[136:139]
	v_mfma_f32_16x16x32_bf16 v[140:143], v[104:107], v[28:31], v[140:143]
	s_nop 6
	v_max_i32_e32 v135, 0, v136
	v_fmac_f32_e32 v131, v14, v135
	v_max_i32_e32 v135, 0, v140
	v_fmac_f32_e32 v123, v14, v135
	v_max_i32_e32 v135, 0, v137
	v_fmac_f32_e32 v132, v14, v135
	v_max_i32_e32 v135, 0, v141
	v_fmac_f32_e32 v124, v14, v135
	v_max_i32_e32 v135, 0, v138
	v_fmac_f32_e32 v133, v14, v135
	v_max_i32_e32 v135, 0, v142
	v_fmac_f32_e32 v129, v14, v135
	v_max_i32_e32 v135, 0, v139
	v_mfma_f32_16x16x32_bf16 v[136:139], v[116:119], v[32:35], 0
	v_fmac_f32_e32 v134, v14, v135
	v_max_i32_e32 v135, 0, v143
	v_fmac_f32_e32 v130, v14, v135
	v_mfma_f32_16x16x32_bf16 v[140:143], v[112:115], v[32:35], 0
	v_mfma_f32_16x16x32_bf16 v[136:139], v[108:111], v[36:39], v[136:139]
	v_mfma_f32_16x16x32_bf16 v[140:143], v[104:107], v[36:39], v[140:143]
	s_nop 6
	v_max_i32_e32 v135, 0, v136
	v_fmac_f32_e32 v131, v15, v135
	v_max_i32_e32 v135, 0, v140
	v_fmac_f32_e32 v123, v15, v135
	v_max_i32_e32 v135, 0, v137
	v_fmac_f32_e32 v132, v15, v135
	v_max_i32_e32 v135, 0, v141
	v_fmac_f32_e32 v124, v15, v135
	v_max_i32_e32 v135, 0, v138
	v_fmac_f32_e32 v133, v15, v135
	v_max_i32_e32 v135, 0, v142
	v_fmac_f32_e32 v129, v15, v135
	v_max_i32_e32 v135, 0, v139
	v_mfma_f32_16x16x32_bf16 v[136:139], v[116:119], v[40:43], 0
	v_fmac_f32_e32 v134, v15, v135
	v_max_i32_e32 v135, 0, v143
	v_fmac_f32_e32 v130, v15, v135
	v_mfma_f32_16x16x32_bf16 v[140:143], v[112:115], v[40:43], 0
	v_mfma_f32_16x16x32_bf16 v[136:139], v[108:111], v[44:47], v[136:139]
	v_mfma_f32_16x16x32_bf16 v[140:143], v[104:107], v[44:47], v[140:143]
	s_nop 6
	v_max_i32_e32 v135, 0, v136
	v_fmac_f32_e32 v131, v8, v135
	v_max_i32_e32 v135, 0, v140
	v_fmac_f32_e32 v123, v8, v135
	v_max_i32_e32 v135, 0, v137
	v_fmac_f32_e32 v132, v8, v135
	v_max_i32_e32 v135, 0, v141
	v_fmac_f32_e32 v124, v8, v135
	v_max_i32_e32 v135, 0, v138
	v_fmac_f32_e32 v133, v8, v135
	v_max_i32_e32 v135, 0, v142
	v_fmac_f32_e32 v129, v8, v135
	v_max_i32_e32 v135, 0, v139
	v_mfma_f32_16x16x32_bf16 v[136:139], v[116:119], v[48:51], 0
	v_fmac_f32_e32 v134, v8, v135
	v_max_i32_e32 v135, 0, v143
	v_fmac_f32_e32 v130, v8, v135
	v_mfma_f32_16x16x32_bf16 v[140:143], v[112:115], v[48:51], 0
	v_mfma_f32_16x16x32_bf16 v[136:139], v[108:111], v[52:55], v[136:139]
	v_mfma_f32_16x16x32_bf16 v[140:143], v[104:107], v[52:55], v[140:143]
	s_nop 6
	v_max_i32_e32 v135, 0, v136
	v_fmac_f32_e32 v131, v9, v135
	v_max_i32_e32 v135, 0, v140
	v_fmac_f32_e32 v123, v9, v135
	v_max_i32_e32 v135, 0, v137
	v_fmac_f32_e32 v132, v9, v135
	v_max_i32_e32 v135, 0, v141
	v_fmac_f32_e32 v124, v9, v135
	v_max_i32_e32 v135, 0, v138
	v_fmac_f32_e32 v133, v9, v135
	v_max_i32_e32 v135, 0, v142
	v_fmac_f32_e32 v129, v9, v135
	v_max_i32_e32 v135, 0, v139
	v_mfma_f32_16x16x32_bf16 v[136:139], v[116:119], v[56:59], 0
	v_fmac_f32_e32 v134, v9, v135
	v_max_i32_e32 v135, 0, v143
	v_fmac_f32_e32 v130, v9, v135
	v_mfma_f32_16x16x32_bf16 v[140:143], v[112:115], v[56:59], 0
	v_mfma_f32_16x16x32_bf16 v[112:115], v[112:115], v[64:67], 0
	v_mfma_f32_16x16x32_bf16 v[116:119], v[116:119], v[64:67], 0
	v_mfma_f32_16x16x32_bf16 v[136:139], v[108:111], v[60:63], v[136:139]
	v_mfma_f32_16x16x32_bf16 v[140:143], v[104:107], v[60:63], v[140:143]
	v_mfma_f32_16x16x32_bf16 v[104:107], v[104:107], v[68:71], v[112:115]
	s_nop 5
	v_max_i32_e32 v135, 0, v136
	v_fmac_f32_e32 v131, v10, v135
	v_max_i32_e32 v135, 0, v140
	v_mfma_f32_16x16x32_bf16 v[108:111], v[108:111], v[68:71], v[116:119]
	v_fmac_f32_e32 v123, v10, v135
	v_max_i32_e32 v104, 0, v104
	v_max_i32_e32 v135, 0, v137
	v_fmac_f32_e32 v132, v10, v135
	v_fmac_f32_e32 v123, v11, v104
	s_nop 5
	v_max_i32_e32 v104, 0, v109
	v_max_i32_e32 v135, 0, v141
	v_fmac_f32_e32 v124, v10, v135
	v_fmac_f32_e32 v132, v11, v104
	v_max_i32_e32 v104, 0, v105
	v_max_i32_e32 v135, 0, v138
	v_fmac_f32_e32 v133, v10, v135
	v_fmac_f32_e32 v124, v11, v104
	v_max_i32_e32 v104, 0, v110
	v_max_i32_e32 v135, 0, v142
	v_fmac_f32_e32 v129, v10, v135
	v_fmac_f32_e32 v133, v11, v104
	v_max_i32_e32 v104, 0, v106
	v_max_i32_e32 v135, 0, v139
	v_fmac_f32_e32 v134, v10, v135
	v_fmac_f32_e32 v129, v11, v104
	v_max_i32_e32 v104, 0, v111
	v_max_i32_e32 v135, 0, v143
	v_fmac_f32_e32 v130, v10, v135
	v_fmac_f32_e32 v134, v11, v104
	v_max_i32_e32 v104, 0, v107
	v_max_i32_e32 v108, 0, v108
	v_fmac_f32_e32 v131, v11, v108
	v_fmac_f32_e32 v130, v11, v104
	s_nop 0
	v_lshrrev_b32 v104, 22, v131
	v_bfe_u32 v105, v131, 21, 1
	v_lshl_add_u32 v104, v104, 2, v128
	v_mad_u32_u24 v105, v105, s1, 1
	ds_add_u32 v104, v105
	v_lshrrev_b32 v104, 22, v132
	v_bfe_u32 v105, v132, 21, 1
	v_lshl_add_u32 v104, v104, 2, v128
	v_mad_u32_u24 v105, v105, s1, 1
	ds_add_u32 v104, v105
	v_lshrrev_b32 v104, 22, v133
	v_bfe_u32 v105, v133, 21, 1
	v_lshl_add_u32 v104, v104, 2, v128
	v_mad_u32_u24 v105, v105, s1, 1
	ds_add_u32 v104, v105
	v_lshrrev_b32 v104, 22, v134
	v_bfe_u32 v105, v134, 21, 1
	v_lshl_add_u32 v104, v104, 2, v128
	v_mad_u32_u24 v105, v105, s1, 1
	ds_add_u32 v104, v105
	v_lshrrev_b32 v104, 22, v123
	v_bfe_u32 v105, v123, 21, 1
	v_lshl_add_u32 v104, v104, 2, v128
	v_mad_u32_u24 v105, v105, s1, 1
	ds_add_u32 v104, v105
	v_lshrrev_b32 v104, 22, v124
	v_bfe_u32 v105, v124, 21, 1
	v_lshl_add_u32 v104, v104, 2, v128
	v_mad_u32_u24 v105, v105, s1, 1
	ds_add_u32 v104, v105
	v_lshrrev_b32 v104, 22, v129
	v_bfe_u32 v105, v129, 21, 1
	v_lshl_add_u32 v104, v104, 2, v128
	v_mad_u32_u24 v105, v105, s1, 1
	ds_add_u32 v104, v105
	v_lshrrev_b32 v104, 22, v130
	v_bfe_u32 v105, v130, 21, 1
	v_lshl_add_u32 v104, v104, 2, v128
	v_mad_u32_u24 v105, v105, s1, 1
	ds_add_u32 v104, v105
	v_lshl_or_b32 v104, s35, 5, v125
	v_ashrrev_i32_e32 v105, 31, v104
	v_lshlrev_b64 v[104:105], 7, v[104:105]
	v_sub_u32_e32 v104, v104, v229
	v_lshl_add_u64 v[104:105], v[120:121], 0, v[104:105]
	global_load_dwordx4 v[116:119], v[104:105], off
	global_load_dwordx4 v[108:111], v[104:105], off offset:1024
	global_load_dwordx4 v[112:115], v[104:105], off offset:2048
	s_nop 0
	global_load_dwordx4 v[104:107], v[104:105], off offset:3072
	s_cbranch_scc1 .LBB0_1307
	s_waitcnt vmcnt(7)
	v_mfma_f32_16x16x32_bf16 v[130:133], v[72:75], v[0:3], 0
	s_waitcnt vmcnt(5)
	v_mfma_f32_16x16x32_bf16 v[134:137], v[80:83], v[0:3], 0
	v_mfma_f32_16x16x32_bf16 v[138:141], v[76:79], v[4:7], v[130:133]
	s_waitcnt vmcnt(4)
	v_mfma_f32_16x16x32_bf16 v[132:135], v[84:87], v[4:7], v[134:137]
	s_nop 2
	v_mov_b32_e32 v131, 0
	s_nop 1
	v_max_i32_e32 v123, 0, v138
	v_fmac_f32_e32 v131, v12, v123
	v_mov_b32_e32 v123, 0
	v_max_i32_e32 v124, 0, v132
	v_fmac_f32_e32 v123, v12, v124
	v_max_i32_e32 v124, 0, v139
	v_mov_b32_e32 v132, 0
	v_fmac_f32_e32 v132, v12, v124
	v_max_i32_e32 v129, 0, v133
	v_mov_b32_e32 v124, 0
	v_fmac_f32_e32 v124, v12, v129
	v_max_i32_e32 v129, 0, v140
	v_mov_b32_e32 v133, 0
	v_fmac_f32_e32 v133, v12, v129
	v_max_i32_e32 v130, 0, v134
	v_mov_b32_e32 v129, 0
	v_mfma_f32_16x16x32_bf16 v[136:139], v[72:75], v[16:19], 0
	v_fmac_f32_e32 v129, v12, v130
	v_max_i32_e32 v130, 0, v141
	v_mov_b32_e32 v134, 0
	v_mfma_f32_16x16x32_bf16 v[140:143], v[80:83], v[16:19], 0
	v_fmac_f32_e32 v134, v12, v130
	v_max_i32_e32 v135, 0, v135
	v_mov_b32_e32 v130, 0
	v_mfma_f32_16x16x32_bf16 v[136:139], v[76:79], v[20:23], v[136:139]
	v_fmac_f32_e32 v130, v12, v135
	v_mfma_f32_16x16x32_bf16 v[140:143], v[84:87], v[20:23], v[140:143]
	s_nop 6
	v_max_i32_e32 v135, 0, v136
	v_fmac_f32_e32 v131, v13, v135
	v_max_i32_e32 v135, 0, v140
	v_fmac_f32_e32 v123, v13, v135
	v_max_i32_e32 v135, 0, v137
	v_fmac_f32_e32 v132, v13, v135
	v_max_i32_e32 v135, 0, v141
	v_fmac_f32_e32 v124, v13, v135
	v_max_i32_e32 v135, 0, v138
	v_fmac_f32_e32 v133, v13, v135
	v_max_i32_e32 v135, 0, v142
	v_fmac_f32_e32 v129, v13, v135
	v_max_i32_e32 v135, 0, v139
	v_mfma_f32_16x16x32_bf16 v[136:139], v[72:75], v[24:27], 0
	v_fmac_f32_e32 v134, v13, v135
	v_max_i32_e32 v135, 0, v143
	v_fmac_f32_e32 v130, v13, v135
	v_mfma_f32_16x16x32_bf16 v[140:143], v[80:83], v[24:27], 0
	v_mfma_f32_16x16x32_bf16 v[136:139], v[76:79], v[28:31], v[136:139]
	v_mfma_f32_16x16x32_bf16 v[140:143], v[84:87], v[28:31], v[140:143]
	s_nop 6
	v_max_i32_e32 v135, 0, v136
	v_fmac_f32_e32 v131, v14, v135
	v_max_i32_e32 v135, 0, v140
	v_fmac_f32_e32 v123, v14, v135
	v_max_i32_e32 v135, 0, v137
	v_fmac_f32_e32 v132, v14, v135
	v_max_i32_e32 v135, 0, v141
	v_fmac_f32_e32 v124, v14, v135
	v_max_i32_e32 v135, 0, v138
	v_fmac_f32_e32 v133, v14, v135
	v_max_i32_e32 v135, 0, v142
	v_fmac_f32_e32 v129, v14, v135
	v_max_i32_e32 v135, 0, v139
	v_mfma_f32_16x16x32_bf16 v[136:139], v[72:75], v[32:35], 0
	v_fmac_f32_e32 v134, v14, v135
	v_max_i32_e32 v135, 0, v143
	v_fmac_f32_e32 v130, v14, v135
	v_mfma_f32_16x16x32_bf16 v[140:143], v[80:83], v[32:35], 0
	v_mfma_f32_16x16x32_bf16 v[136:139], v[76:79], v[36:39], v[136:139]
	v_mfma_f32_16x16x32_bf16 v[140:143], v[84:87], v[36:39], v[140:143]
	s_nop 6
	v_max_i32_e32 v135, 0, v136
	v_fmac_f32_e32 v131, v15, v135
	v_max_i32_e32 v135, 0, v140
	v_fmac_f32_e32 v123, v15, v135
	v_max_i32_e32 v135, 0, v137
	v_fmac_f32_e32 v132, v15, v135
	v_max_i32_e32 v135, 0, v141
	v_fmac_f32_e32 v124, v15, v135
	v_max_i32_e32 v135, 0, v138
	v_fmac_f32_e32 v133, v15, v135
	v_max_i32_e32 v135, 0, v142
	v_fmac_f32_e32 v129, v15, v135
	v_max_i32_e32 v135, 0, v139
	v_mfma_f32_16x16x32_bf16 v[136:139], v[72:75], v[40:43], 0
	v_fmac_f32_e32 v134, v15, v135
	v_max_i32_e32 v135, 0, v143
	v_fmac_f32_e32 v130, v15, v135
	v_mfma_f32_16x16x32_bf16 v[140:143], v[80:83], v[40:43], 0
	v_mfma_f32_16x16x32_bf16 v[136:139], v[76:79], v[44:47], v[136:139]
	v_mfma_f32_16x16x32_bf16 v[140:143], v[84:87], v[44:47], v[140:143]
	s_nop 6
	v_max_i32_e32 v135, 0, v136
	v_fmac_f32_e32 v131, v8, v135
	v_max_i32_e32 v135, 0, v140
	v_fmac_f32_e32 v123, v8, v135
	v_max_i32_e32 v135, 0, v137
	v_fmac_f32_e32 v132, v8, v135
	v_max_i32_e32 v135, 0, v141
	v_fmac_f32_e32 v124, v8, v135
	v_max_i32_e32 v135, 0, v138
	v_fmac_f32_e32 v133, v8, v135
	v_max_i32_e32 v135, 0, v142
	v_fmac_f32_e32 v129, v8, v135
	v_max_i32_e32 v135, 0, v139
	v_mfma_f32_16x16x32_bf16 v[136:139], v[72:75], v[48:51], 0
	v_fmac_f32_e32 v134, v8, v135
	v_max_i32_e32 v135, 0, v143
	v_fmac_f32_e32 v130, v8, v135
	v_mfma_f32_16x16x32_bf16 v[140:143], v[80:83], v[48:51], 0
	v_mfma_f32_16x16x32_bf16 v[136:139], v[76:79], v[52:55], v[136:139]
	v_mfma_f32_16x16x32_bf16 v[140:143], v[84:87], v[52:55], v[140:143]
	s_nop 6
	v_max_i32_e32 v135, 0, v136
	v_fmac_f32_e32 v131, v9, v135
	v_max_i32_e32 v135, 0, v140
	v_fmac_f32_e32 v123, v9, v135
	v_max_i32_e32 v135, 0, v137
	v_fmac_f32_e32 v132, v9, v135
	v_max_i32_e32 v135, 0, v141
	v_fmac_f32_e32 v124, v9, v135
	v_max_i32_e32 v135, 0, v138
	v_fmac_f32_e32 v133, v9, v135
	v_max_i32_e32 v135, 0, v142
	v_fmac_f32_e32 v129, v9, v135
	v_max_i32_e32 v135, 0, v139
	v_mfma_f32_16x16x32_bf16 v[136:139], v[72:75], v[56:59], 0
	v_fmac_f32_e32 v134, v9, v135
	v_max_i32_e32 v135, 0, v143
	v_fmac_f32_e32 v130, v9, v135
	v_mfma_f32_16x16x32_bf16 v[140:143], v[80:83], v[56:59], 0
	v_mfma_f32_16x16x32_bf16 v[136:139], v[76:79], v[60:63], v[136:139]
	v_mfma_f32_16x16x32_bf16 v[140:143], v[84:87], v[60:63], v[140:143]
	s_nop 6
	v_max_i32_e32 v135, 0, v136
	v_fmac_f32_e32 v131, v10, v135
	v_max_i32_e32 v135, 0, v140
	v_fmac_f32_e32 v123, v10, v135
	v_max_i32_e32 v135, 0, v137
	v_fmac_f32_e32 v132, v10, v135
	v_max_i32_e32 v135, 0, v141
	v_fmac_f32_e32 v124, v10, v135
	v_max_i32_e32 v135, 0, v138
	v_fmac_f32_e32 v133, v10, v135
	v_max_i32_e32 v135, 0, v142
	v_fmac_f32_e32 v129, v10, v135
	v_max_i32_e32 v135, 0, v139
	v_mfma_f32_16x16x32_bf16 v[136:139], v[72:75], v[64:67], 0
	v_fmac_f32_e32 v134, v10, v135
	v_max_i32_e32 v135, 0, v143
	v_fmac_f32_e32 v130, v10, v135
	v_mfma_f32_16x16x32_bf16 v[140:143], v[80:83], v[64:67], 0
	v_mfma_f32_16x16x32_bf16 v[136:139], v[76:79], v[68:71], v[136:139]
	v_mfma_f32_16x16x32_bf16 v[140:143], v[84:87], v[68:71], v[140:143]
	s_nop 6
	v_max_i32_e32 v135, 0, v136
	v_fmac_f32_e32 v131, v11, v135
	v_max_i32_e32 v135, 0, v140
	v_fmac_f32_e32 v123, v11, v135
	v_max_i32_e32 v135, 0, v137
	v_fmac_f32_e32 v132, v11, v135
	v_max_i32_e32 v135, 0, v141
	v_fmac_f32_e32 v124, v11, v135
	v_max_i32_e32 v135, 0, v138
	v_fmac_f32_e32 v133, v11, v135
	v_max_i32_e32 v135, 0, v142
	v_fmac_f32_e32 v129, v11, v135
	v_max_i32_e32 v135, 0, v139
	v_fmac_f32_e32 v134, v11, v135
	v_max_i32_e32 v135, 0, v143
	v_fmac_f32_e32 v130, v11, v135
	v_lshrrev_b32 v135, 22, v131
	v_bfe_u32 v131, v131, 21, 1
	v_mad_u32_u24 v131, v131, s1, 1
	v_lshl_add_u32 v135, v135, 2, v128
	ds_add_u32 v135, v131
	v_lshrrev_b32 v131, 22, v132
	v_bfe_u32 v132, v132, 21, 1
	v_lshl_add_u32 v131, v131, 2, v128
	v_mad_u32_u24 v132, v132, s1, 1
	ds_add_u32 v131, v132
	v_lshrrev_b32 v131, 22, v133
	v_bfe_u32 v132, v133, 21, 1
	v_lshl_add_u32 v131, v131, 2, v128
	v_mad_u32_u24 v132, v132, s1, 1
	ds_add_u32 v131, v132
	v_lshrrev_b32 v131, 22, v134
	v_bfe_u32 v132, v134, 21, 1
	v_lshl_add_u32 v131, v131, 2, v128
	v_mad_u32_u24 v132, v132, s1, 1
	ds_add_u32 v131, v132
	v_lshrrev_b32 v131, 22, v123
	v_bfe_u32 v123, v123, 21, 1
	v_mad_u32_u24 v123, v123, s1, 1
	v_lshl_add_u32 v131, v131, 2, v128
	ds_add_u32 v131, v123
	v_lshrrev_b32 v123, 22, v124
	v_bfe_u32 v124, v124, 21, 1
	v_lshl_add_u32 v123, v123, 2, v128
	v_mad_u32_u24 v124, v124, s1, 1
	ds_add_u32 v123, v124
	v_lshrrev_b32 v123, 22, v129
	v_bfe_u32 v124, v129, 21, 1
	v_lshl_add_u32 v123, v123, 2, v128
	v_mad_u32_u24 v124, v124, s1, 1
	ds_add_u32 v123, v124
	v_lshrrev_b32 v123, 22, v130
	v_bfe_u32 v124, v130, 21, 1
	v_lshl_add_u32 v123, v123, 2, v128
	v_mad_u32_u24 v124, v124, s1, 1
	ds_add_u32 v123, v124
	s_branch .LBB0_1307

.LBB0_1438:
	s_waitcnt vmcnt(3) lgkmcnt(0)
	v_mfma_f32_16x16x32_bf16 v[146:149], v[116:119], v[0:3], 0
	s_add_i32 s85, s31, 8
	s_min_i32 s14, s85, s72
	v_lshl_or_b32 v72, s14, 5, v125
	s_waitcnt vmcnt(1)
	v_mfma_f32_16x16x32_bf16 v[150:153], v[112:115], v[0:3], 0
	v_ashrrev_i32_e32 v73, 31, v72
	v_lshlrev_b64 v[72:73], 7, v[72:73]
	v_sub_u32_e32 v72, v72, v229
	v_lshl_add_u64 v[84:85], v[120:121], 0, v[72:73]
	v_mfma_f32_16x16x32_bf16 v[154:157], v[108:111], v[4:7], v[146:149]
	global_load_dwordx4 v[72:75], v[84:85], off
	global_load_dwordx4 v[76:79], v[84:85], off offset:1024
	global_load_dwordx4 v[80:83], v[84:85], off offset:2048
	s_nop 0
	global_load_dwordx4 v[84:87], v[84:85], off offset:3072
	v_mov_b32_e32 v149, 0
	v_mov_b32_e32 v148, 0
	s_waitcnt vmcnt(4)
	v_mfma_f32_16x16x32_bf16 v[158:161], v[104:107], v[4:7], v[150:153]
	v_max_i32_e32 v146, 0, v154
	v_mov_b32_e32 v147, 0
	s_nop 0
	v_mov_b32_e32 v153, 0
	v_fmac_f32_e32 v153, v12, v146
	s_nop 3
	v_max_i32_e32 v146, 0, v158
	v_fmac_f32_e32 v149, v12, v146
	v_max_i32_e32 v146, 0, v155
	v_mov_b32_e32 v152, 0
	v_fmac_f32_e32 v152, v12, v146
	v_max_i32_e32 v146, 0, v159
	v_fmac_f32_e32 v148, v12, v146
	v_max_i32_e32 v146, 0, v156
	v_mov_b32_e32 v151, 0
	v_fmac_f32_e32 v151, v12, v146
	v_max_i32_e32 v146, 0, v160
	v_fmac_f32_e32 v147, v12, v146
	v_max_i32_e32 v146, 0, v157
	v_mov_b32_e32 v150, 0
	v_fmac_f32_e32 v150, v12, v146
	v_max_i32_e32 v154, 0, v161
	v_mov_b32_e32 v146, 0
	v_fmac_f32_e32 v146, v12, v154
	v_mfma_f32_16x16x32_bf16 v[154:157], v[116:119], v[16:19], 0
	v_mfma_f32_16x16x32_bf16 v[158:161], v[112:115], v[16:19], 0
	v_mfma_f32_16x16x32_bf16 v[154:157], v[108:111], v[20:23], v[154:157]
	v_mfma_f32_16x16x32_bf16 v[158:161], v[104:107], v[20:23], v[158:161]
	s_nop 6
	v_max_i32_e32 v154, 0, v154
	v_fmac_f32_e32 v153, v13, v154
	v_max_i32_e32 v154, 0, v158
	v_fmac_f32_e32 v149, v13, v154
	v_max_i32_e32 v154, 0, v155
	v_fmac_f32_e32 v152, v13, v154
	v_max_i32_e32 v154, 0, v159
	v_fmac_f32_e32 v148, v13, v154
	v_max_i32_e32 v154, 0, v156
	v_fmac_f32_e32 v151, v13, v154
	v_max_i32_e32 v154, 0, v160
	v_fmac_f32_e32 v147, v13, v154
	v_max_i32_e32 v154, 0, v157
	v_fmac_f32_e32 v150, v13, v154
	v_max_i32_e32 v154, 0, v161
	v_fmac_f32_e32 v146, v13, v154
	v_mfma_f32_16x16x32_bf16 v[154:157], v[116:119], v[24:27], 0
	v_mfma_f32_16x16x32_bf16 v[158:161], v[112:115], v[24:27], 0
	v_mfma_f32_16x16x32_bf16 v[154:157], v[108:111], v[28:31], v[154:157]
	v_mfma_f32_16x16x32_bf16 v[158:161], v[104:107], v[28:31], v[158:161]
	s_nop 6
	v_max_i32_e32 v154, 0, v154
	v_fmac_f32_e32 v153, v14, v154
	v_max_i32_e32 v154, 0, v158
	v_fmac_f32_e32 v149, v14, v154
	v_max_i32_e32 v154, 0, v155
	v_fmac_f32_e32 v152, v14, v154
	v_max_i32_e32 v154, 0, v159
	v_fmac_f32_e32 v148, v14, v154
	v_max_i32_e32 v154, 0, v156
	v_fmac_f32_e32 v151, v14, v154
	v_max_i32_e32 v154, 0, v160
	v_fmac_f32_e32 v147, v14, v154
	v_max_i32_e32 v154, 0, v157
	v_fmac_f32_e32 v150, v14, v154
	v_max_i32_e32 v154, 0, v161
	v_fmac_f32_e32 v146, v14, v154
	v_mfma_f32_16x16x32_bf16 v[154:157], v[116:119], v[32:35], 0
	v_mfma_f32_16x16x32_bf16 v[158:161], v[112:115], v[32:35], 0
	v_mfma_f32_16x16x32_bf16 v[154:157], v[108:111], v[36:39], v[154:157]
	v_mfma_f32_16x16x32_bf16 v[158:161], v[104:107], v[36:39], v[158:161]
	s_nop 6
	v_max_i32_e32 v154, 0, v154
	v_fmac_f32_e32 v153, v15, v154
	v_max_i32_e32 v154, 0, v158
	v_fmac_f32_e32 v149, v15, v154
	v_max_i32_e32 v154, 0, v155
	v_fmac_f32_e32 v152, v15, v154
	v_max_i32_e32 v154, 0, v159
	v_fmac_f32_e32 v148, v15, v154
	v_max_i32_e32 v154, 0, v156
	v_fmac_f32_e32 v151, v15, v154
	v_max_i32_e32 v154, 0, v160
	v_fmac_f32_e32 v147, v15, v154
	v_max_i32_e32 v154, 0, v157
	v_fmac_f32_e32 v150, v15, v154
	v_max_i32_e32 v154, 0, v161
	v_fmac_f32_e32 v146, v15, v154
	v_mfma_f32_16x16x32_bf16 v[154:157], v[116:119], v[40:43], 0
	v_mfma_f32_16x16x32_bf16 v[158:161], v[112:115], v[40:43], 0
	v_mfma_f32_16x16x32_bf16 v[154:157], v[108:111], v[44:47], v[154:157]
	v_mfma_f32_16x16x32_bf16 v[158:161], v[104:107], v[44:47], v[158:161]
	s_nop 6
	v_max_i32_e32 v154, 0, v154
	v_fmac_f32_e32 v153, v8, v154
	v_max_i32_e32 v154, 0, v158
	v_fmac_f32_e32 v149, v8, v154
	v_max_i32_e32 v154, 0, v155
	v_fmac_f32_e32 v152, v8, v154
	v_max_i32_e32 v154, 0, v159
	v_fmac_f32_e32 v148, v8, v154
	v_max_i32_e32 v154, 0, v156
	v_fmac_f32_e32 v151, v8, v154
	v_max_i32_e32 v154, 0, v160
	v_fmac_f32_e32 v147, v8, v154
	v_max_i32_e32 v154, 0, v157
	v_fmac_f32_e32 v150, v8, v154
	v_max_i32_e32 v154, 0, v161
	v_fmac_f32_e32 v146, v8, v154
	v_mfma_f32_16x16x32_bf16 v[154:157], v[116:119], v[48:51], 0
	v_mfma_f32_16x16x32_bf16 v[158:161], v[112:115], v[48:51], 0
	v_mfma_f32_16x16x32_bf16 v[154:157], v[108:111], v[52:55], v[154:157]
	v_mfma_f32_16x16x32_bf16 v[158:161], v[104:107], v[52:55], v[158:161]
	s_nop 6
	v_max_i32_e32 v154, 0, v154
	v_fmac_f32_e32 v153, v9, v154
	v_max_i32_e32 v154, 0, v158
	v_fmac_f32_e32 v149, v9, v154
	v_max_i32_e32 v154, 0, v155
	v_fmac_f32_e32 v152, v9, v154
	v_max_i32_e32 v154, 0, v159
	v_fmac_f32_e32 v148, v9, v154
	v_max_i32_e32 v154, 0, v156
	v_fmac_f32_e32 v151, v9, v154
	v_max_i32_e32 v154, 0, v160
	v_fmac_f32_e32 v147, v9, v154
	v_max_i32_e32 v154, 0, v157
	v_fmac_f32_e32 v150, v9, v154
	v_max_i32_e32 v154, 0, v161
	v_fmac_f32_e32 v146, v9, v154
	v_mfma_f32_16x16x32_bf16 v[154:157], v[116:119], v[56:59], 0
	v_mfma_f32_16x16x32_bf16 v[158:161], v[112:115], v[56:59], 0
	v_mfma_f32_16x16x32_bf16 v[112:115], v[112:115], v[64:67], 0
	v_mfma_f32_16x16x32_bf16 v[116:119], v[116:119], v[64:67], 0
	v_mfma_f32_16x16x32_bf16 v[154:157], v[108:111], v[60:63], v[154:157]
	v_mfma_f32_16x16x32_bf16 v[158:161], v[104:107], v[60:63], v[158:161]
	v_mfma_f32_16x16x32_bf16 v[104:107], v[104:107], v[68:71], v[112:115]
	s_nop 5
	v_max_i32_e32 v154, 0, v154
	v_fmac_f32_e32 v153, v10, v154
	v_max_i32_e32 v154, 0, v158
	v_mfma_f32_16x16x32_bf16 v[108:111], v[108:111], v[68:71], v[116:119]
	v_fmac_f32_e32 v149, v10, v154
	v_max_i32_e32 v154, 0, v155
	v_max_i32_e32 v104, 0, v104
	v_fmac_f32_e32 v152, v10, v154
	v_max_i32_e32 v154, 0, v159
	v_fmac_f32_e32 v149, v11, v104
	s_nop 4
	v_max_i32_e32 v104, 0, v109
	v_fmac_f32_e32 v148, v10, v154
	v_max_i32_e32 v154, 0, v156
	v_fmac_f32_e32 v152, v11, v104
	v_max_i32_e32 v104, 0, v105
	v_fmac_f32_e32 v151, v10, v154
	v_max_i32_e32 v154, 0, v160
	v_fmac_f32_e32 v148, v11, v104
	v_max_i32_e32 v104, 0, v110
	v_fmac_f32_e32 v147, v10, v154
	v_max_i32_e32 v154, 0, v157
	v_max_i32_e32 v108, 0, v108
	v_fmac_f32_e32 v153, v11, v108
	v_fmac_f32_e32 v151, v11, v104
	v_max_i32_e32 v104, 0, v106
	v_fmac_f32_e32 v150, v10, v154
	v_max_i32_e32 v154, 0, v161
	v_fmac_f32_e32 v146, v10, v154
	v_fmac_f32_e32 v147, v11, v104
	v_max_i32_e32 v104, 0, v111
	v_fmac_f32_e32 v150, v11, v104
	v_max_i32_e32 v104, 0, v107
	v_fmac_f32_e32 v146, v11, v104
	v_cmp_ge_f32_e64 s[66:67], v153, v140
	v_cmp_ge_f32_e64 s[50:51], v153, v139
	v_cmp_ge_f32_e32 vcc, v152, v140
	v_cmp_ge_f32_e64 s[52:53], v152, v139
	v_cndmask_b32_e64 v224, 0, 1, s[66:67]
	v_cndmask_b32_e64 v225, 0, 2, vcc
	s_andn2_b64 s[50:51], s[50:51], s[66:67]
	s_andn2_b64 s[52:53], s[52:53], vcc
	v_or_b32_e32 v228, v224, v225
	v_cmp_ge_f32_e64 s[66:67], v151, v140
	v_cmp_ge_f32_e64 s[54:55], v151, v139
	v_cmp_ge_f32_e32 vcc, v150, v140
	v_cmp_ge_f32_e64 s[56:57], v150, v139
	v_cndmask_b32_e64 v224, 0, 4, s[66:67]
	v_cndmask_b32_e64 v225, 0, 8, vcc
	s_andn2_b64 s[54:55], s[54:55], s[66:67]
	s_andn2_b64 s[56:57], s[56:57], vcc
	v_or3_b32 v228, v228, v224, v225
	v_cmp_ge_f32_e64 s[66:67], v149, v140
	v_cmp_ge_f32_e64 s[58:59], v149, v139
	v_cmp_ge_f32_e32 vcc, v148, v140
	v_cmp_ge_f32_e64 s[60:61], v148, v139
	v_cndmask_b32_e64 v224, 0, v201, s[66:67]
	v_cndmask_b32_e64 v225, 0, v200, vcc
	s_andn2_b64 s[58:59], s[58:59], s[66:67]
	s_andn2_b64 s[60:61], s[60:61], vcc
	v_or3_b32 v228, v228, v224, v225
	v_cmp_ge_f32_e64 s[66:67], v147, v140
	v_cmp_ge_f32_e64 s[62:63], v147, v139
	v_cmp_ge_f32_e32 vcc, v146, v140
	v_cmp_ge_f32_e64 s[64:65], v146, v139
	v_cndmask_b32_e64 v224, 0, v199, s[66:67]
	v_cndmask_b32_e64 v225, 0, v198, vcc
	s_andn2_b64 s[62:63], s[62:63], s[66:67]
	s_andn2_b64 s[64:65], s[64:65], vcc
	v_or3_b32 v228, v228, v224, v225
	v_add_u32_e32 v226, s74, v124
	v_mov_b32_e32 v227, s96
	s_mov_b64 s[14:15], exec
	s_mov_b64 exec, s[50:51]
	v_ashrrev_i32_e32 v206, 31, v153
	v_xor_b32_e32 v206, v206, v153
	v_lshrrev_b32_e32 v222, 9, v206
	v_lshrrev_b32_e32 v223, 6, v206
	v_and_b32_e32 v222, 0xffc, v222
	v_and_b32_e32 v223, 16, v223
	v_add_u32_e32 v222, v128, v222
	v_lshlrev_b32_e64 v223, v223, 1
	ds_add_u32 v222, v223
	s_mov_b64 exec, s[52:53]
	v_ashrrev_i32_e32 v207, 31, v152
	v_xor_b32_e32 v207, v207, v152
	v_lshrrev_b32_e32 v222, 9, v207
	v_lshrrev_b32_e32 v223, 6, v207
	v_and_b32_e32 v222, 0xffc, v222
	v_and_b32_e32 v223, 16, v223
	v_add_u32_e32 v222, v128, v222
	v_lshlrev_b32_e64 v223, v223, 1
	ds_add_u32 v222, v223
	s_mov_b64 exec, s[54:55]
	v_ashrrev_i32_e32 v208, 31, v151
	v_xor_b32_e32 v208, v208, v151
	v_lshrrev_b32_e32 v222, 9, v208
	v_lshrrev_b32_e32 v223, 6, v208
	v_and_b32_e32 v222, 0xffc, v222
	v_and_b32_e32 v223, 16, v223
	v_add_u32_e32 v222, v128, v222
	v_lshlrev_b32_e64 v223, v223, 1
	ds_add_u32 v222, v223
	s_mov_b64 exec, s[56:57]
	v_ashrrev_i32_e32 v209, 31, v150
	v_xor_b32_e32 v209, v209, v150
	v_lshrrev_b32_e32 v222, 9, v209
	v_lshrrev_b32_e32 v223, 6, v209
	v_and_b32_e32 v222, 0xffc, v222
	v_and_b32_e32 v223, 16, v223
	v_add_u32_e32 v222, v128, v222
	v_lshlrev_b32_e64 v223, v223, 1
	ds_add_u32 v222, v223
	s_mov_b64 exec, s[58:59]
	v_ashrrev_i32_e32 v210, 31, v149
	v_xor_b32_e32 v210, v210, v149
	v_lshrrev_b32_e32 v222, 9, v210
	v_lshrrev_b32_e32 v223, 6, v210
	v_and_b32_e32 v222, 0xffc, v222
	v_and_b32_e32 v223, 16, v223
	v_add_u32_e32 v222, v128, v222
	v_lshlrev_b32_e64 v223, v223, 1
	ds_add_u32 v222, v223
	s_mov_b64 exec, s[60:61]
	v_ashrrev_i32_e32 v211, 31, v148
	v_xor_b32_e32 v211, v211, v148
	v_lshrrev_b32_e32 v222, 9, v211
	v_lshrrev_b32_e32 v223, 6, v211
	v_and_b32_e32 v222, 0xffc, v222
	v_and_b32_e32 v223, 16, v223
	v_add_u32_e32 v222, v128, v222
	v_lshlrev_b32_e64 v223, v223, 1
	ds_add_u32 v222, v223
	s_mov_b64 exec, s[62:63]
	v_ashrrev_i32_e32 v212, 31, v147
	v_xor_b32_e32 v212, v212, v147
	v_lshrrev_b32_e32 v222, 9, v212
	v_lshrrev_b32_e32 v223, 6, v212
	v_and_b32_e32 v222, 0xffc, v222
	v_and_b32_e32 v223, 16, v223
	v_add_u32_e32 v222, v128, v222
	v_lshlrev_b32_e64 v223, v223, 1
	ds_add_u32 v222, v223
	s_mov_b64 exec, s[64:65]
	v_ashrrev_i32_e32 v213, 31, v146
	v_xor_b32_e32 v213, v213, v146
	v_lshrrev_b32_e32 v222, 9, v213
	v_lshrrev_b32_e32 v223, 6, v213
	v_and_b32_e32 v222, 0xffc, v222
	v_and_b32_e32 v223, 16, v223
	v_add_u32_e32 v222, v128, v222
	v_lshlrev_b32_e64 v223, v223, 1
	ds_add_u32 v222, v223
	s_waitcnt lgkmcnt(6)
	s_mov_b64 exec, s[50:51]
	ds_add_rtn_u32 v214, v142, v193
	s_mov_b64 exec, s[52:53]
	ds_add_rtn_u32 v215, v142, v193
	s_mov_b64 exec, s[54:55]
	ds_add_rtn_u32 v216, v142, v193
	s_mov_b64 exec, s[56:57]
	ds_add_rtn_u32 v217, v142, v193
	s_mov_b64 exec, s[58:59]
	ds_add_rtn_u32 v218, v142, v193
	s_mov_b64 exec, s[60:61]
	ds_add_rtn_u32 v219, v142, v193
	s_mov_b64 exec, s[62:63]
	ds_add_rtn_u32 v220, v142, v193
	s_mov_b64 exec, s[64:65]
	ds_add_rtn_u32 v221, v142, v193
	s_waitcnt lgkmcnt(0)
	s_mov_b64 exec, s[50:51]
	v_cmp_lt_u32_e64 s[66:67], s0, v214
	v_bfe_u32 v224, v206, 10, 11
	v_add_u32_e32 v225, 0x0, v226
	v_lshl_add_u32 v222, v214, 2, v141
	v_add_u32_e32 v224, v225, v224
	s_andn2_b64 exec, exec, s[66:67]
	ds_write_b32 v222, v224
	s_mov_b64 exec, s[66:67]
	ds_write_b32 v227, v193
	s_mov_b64 exec, s[52:53]
	v_cmp_lt_u32_e64 s[66:67], s0, v215
	v_bfe_u32 v224, v207, 10, 11
	v_add_u32_e32 v225, 0x800, v226
	v_lshl_add_u32 v222, v215, 2, v141
	v_add_u32_e32 v224, v225, v224
	s_andn2_b64 exec, exec, s[66:67]
	ds_write_b32 v222, v224
	s_mov_b64 exec, s[66:67]
	ds_write_b32 v227, v193
	s_mov_b64 exec, s[54:55]
	v_cmp_lt_u32_e64 s[66:67], s0, v216
	v_bfe_u32 v224, v208, 10, 11
	v_add_u32_e32 v225, 0x1000, v226
	v_lshl_add_u32 v222, v216, 2, v141
	v_add_u32_e32 v224, v225, v224
	s_andn2_b64 exec, exec, s[66:67]
	ds_write_b32 v222, v224
	s_mov_b64 exec, s[66:67]
	ds_write_b32 v227, v193
	s_mov_b64 exec, s[56:57]
	v_cmp_lt_u32_e64 s[66:67], s0, v217
	v_bfe_u32 v224, v209, 10, 11
	v_add_u32_e32 v225, 0x1800, v226
	v_lshl_add_u32 v222, v217, 2, v141
	v_add_u32_e32 v224, v225, v224
	s_andn2_b64 exec, exec, s[66:67]
	ds_write_b32 v222, v224
	s_mov_b64 exec, s[66:67]
	ds_write_b32 v227, v193
	s_waitcnt lgkmcnt(4)
	s_mov_b64 exec, s[58:59]
	v_cmp_lt_u32_e64 s[66:67], s0, v218
	v_bfe_u32 v224, v210, 10, 11
	v_add_u32_e32 v225, 0x8000, v226
	v_lshl_add_u32 v222, v218, 2, v141
	v_add_u32_e32 v224, v225, v224
	s_andn2_b64 exec, exec, s[66:67]
	ds_write_b32 v222, v224
	s_mov_b64 exec, s[66:67]
	ds_write_b32 v227, v193
	s_mov_b64 exec, s[60:61]
	v_cmp_lt_u32_e64 s[66:67], s0, v219
	v_bfe_u32 v224, v211, 10, 11
	v_add_u32_e32 v225, 0x8800, v226
	v_lshl_add_u32 v222, v219, 2, v141
	v_add_u32_e32 v224, v225, v224
	s_andn2_b64 exec, exec, s[66:67]
	ds_write_b32 v222, v224
	s_mov_b64 exec, s[66:67]
	ds_write_b32 v227, v193
	s_mov_b64 exec, s[62:63]
	v_cmp_lt_u32_e64 s[66:67], s0, v220
	v_bfe_u32 v224, v212, 10, 11
	v_add_u32_e32 v225, 0x9000, v226
	v_lshl_add_u32 v222, v220, 2, v141
	v_add_u32_e32 v224, v225, v224
	s_andn2_b64 exec, exec, s[66:67]
	ds_write_b32 v222, v224
	s_mov_b64 exec, s[66:67]
	ds_write_b32 v227, v193
	s_mov_b64 exec, s[64:65]
	v_cmp_lt_u32_e64 s[66:67], s0, v221
	v_bfe_u32 v224, v213, 10, 11
	v_add_u32_e32 v225, 0x9800, v226
	v_lshl_add_u32 v222, v221, 2, v141
	v_add_u32_e32 v224, v225, v224
	s_andn2_b64 exec, exec, s[66:67]
	ds_write_b32 v222, v224
	s_mov_b64 exec, s[66:67]
	ds_write_b32 v227, v193
	s_mov_b64 exec, s[14:15]
	v_mov_b32_e32 v104, v228
	v_lshlrev_b32_e32 v104, v143, v104
	ds_bpermute_b32 v105, v144, v104
	s_waitcnt lgkmcnt(0)
	v_or_b32_e32 v104, v105, v104
	ds_bpermute_b32 v105, v145, v104
	s_and_saveexec_b64 s[14:15], s[38:39]
	s_cbranch_execz .LBB0_1480
	s_waitcnt lgkmcnt(0)
	v_or_b32_e32 v106, v104, v105
	v_lshl_add_u64 v[104:105], v[122:123], 0, s[74:75]
	v_add_co_u32_e32 v104, vcc, 0x3f700000, v104
	s_nop 1
	v_addc_co_u32_e32 v105, vcc, 0, v105, vcc
	global_store_dword v[104:105], v106, off
.LBB0_1480:
	s_or_b64 exec, exec, s[14:15]
	s_add_i32 s31, s31, 16
	s_min_i32 s14, s31, s72
	v_lshl_or_b32 v104, s14, 5, v125
	s_waitcnt lgkmcnt(0)
	v_ashrrev_i32_e32 v105, 31, v104
	v_lshlrev_b64 v[104:105], 7, v[104:105]
	v_sub_u32_e32 v104, v104, v229
	v_lshl_add_u64 v[104:105], v[120:121], 0, v[104:105]
	global_load_dwordx4 v[116:119], v[104:105], off
	global_load_dwordx4 v[108:111], v[104:105], off offset:1024
	global_load_dwordx4 v[112:115], v[104:105], off offset:2048
	s_nop 0
	global_load_dwordx4 v[104:107], v[104:105], off offset:3072
	s_cmp_ge_i32 s85, s82
	s_cbranch_scc1 .LBB0_1437
	s_waitcnt vmcnt(7)
	v_mfma_f32_16x16x32_bf16 v[146:149], v[72:75], v[0:3], 0
	s_waitcnt vmcnt(5)
	v_mfma_f32_16x16x32_bf16 v[150:153], v[80:83], v[0:3], 0
	v_mfma_f32_16x16x32_bf16 v[154:157], v[76:79], v[4:7], v[146:149]
	s_waitcnt vmcnt(4)
	v_mfma_f32_16x16x32_bf16 v[158:161], v[84:87], v[4:7], v[150:153]
	s_nop 2
	v_mov_b32_e32 v149, 0
	s_nop 1
	v_max_i32_e32 v146, 0, v154
	v_mov_b32_e32 v148, 0
	v_mov_b32_e32 v153, 0
	v_fmac_f32_e32 v153, v12, v146
	v_max_i32_e32 v146, 0, v158
	v_fmac_f32_e32 v149, v12, v146
	v_max_i32_e32 v146, 0, v155
	v_mov_b32_e32 v152, 0
	v_fmac_f32_e32 v152, v12, v146
	v_max_i32_e32 v146, 0, v159
	v_fmac_f32_e32 v148, v12, v146
	v_max_i32_e32 v146, 0, v156
	v_mov_b32_e32 v151, 0
	v_fmac_f32_e32 v151, v12, v146
	v_max_i32_e32 v146, 0, v160
	v_mov_b32_e32 v147, 0
	v_fmac_f32_e32 v147, v12, v146
	v_max_i32_e32 v146, 0, v157
	v_mov_b32_e32 v150, 0
	v_fmac_f32_e32 v150, v12, v146
	v_max_i32_e32 v154, 0, v161
	v_mov_b32_e32 v146, 0
	v_fmac_f32_e32 v146, v12, v154
	v_mfma_f32_16x16x32_bf16 v[154:157], v[72:75], v[16:19], 0
	v_mfma_f32_16x16x32_bf16 v[158:161], v[80:83], v[16:19], 0
	v_mfma_f32_16x16x32_bf16 v[154:157], v[76:79], v[20:23], v[154:157]
	v_mfma_f32_16x16x32_bf16 v[158:161], v[84:87], v[20:23], v[158:161]
	s_nop 6
	v_max_i32_e32 v154, 0, v154
	v_fmac_f32_e32 v153, v13, v154
	v_max_i32_e32 v154, 0, v158
	v_fmac_f32_e32 v149, v13, v154
	v_max_i32_e32 v154, 0, v155
	v_fmac_f32_e32 v152, v13, v154
	v_max_i32_e32 v154, 0, v159
	v_fmac_f32_e32 v148, v13, v154
	v_max_i32_e32 v154, 0, v156
	v_fmac_f32_e32 v151, v13, v154
	v_max_i32_e32 v154, 0, v160
	v_fmac_f32_e32 v147, v13, v154
	v_max_i32_e32 v154, 0, v157
	v_fmac_f32_e32 v150, v13, v154
	v_max_i32_e32 v154, 0, v161
	v_fmac_f32_e32 v146, v13, v154
	v_mfma_f32_16x16x32_bf16 v[154:157], v[72:75], v[24:27], 0
	v_mfma_f32_16x16x32_bf16 v[158:161], v[80:83], v[24:27], 0
	v_mfma_f32_16x16x32_bf16 v[154:157], v[76:79], v[28:31], v[154:157]
	v_mfma_f32_16x16x32_bf16 v[158:161], v[84:87], v[28:31], v[158:161]
	s_nop 6
	v_max_i32_e32 v154, 0, v154
	v_fmac_f32_e32 v153, v14, v154
	v_max_i32_e32 v154, 0, v158
	v_fmac_f32_e32 v149, v14, v154
	v_max_i32_e32 v154, 0, v155
	v_fmac_f32_e32 v152, v14, v154
	v_max_i32_e32 v154, 0, v159
	v_fmac_f32_e32 v148, v14, v154
	v_max_i32_e32 v154, 0, v156
	v_fmac_f32_e32 v151, v14, v154
	v_max_i32_e32 v154, 0, v160
	v_fmac_f32_e32 v147, v14, v154
	v_max_i32_e32 v154, 0, v157
	v_fmac_f32_e32 v150, v14, v154
	v_max_i32_e32 v154, 0, v161
	v_fmac_f32_e32 v146, v14, v154
	v_mfma_f32_16x16x32_bf16 v[154:157], v[72:75], v[32:35], 0
	v_mfma_f32_16x16x32_bf16 v[158:161], v[80:83], v[32:35], 0
	v_mfma_f32_16x16x32_bf16 v[154:157], v[76:79], v[36:39], v[154:157]
	v_mfma_f32_16x16x32_bf16 v[158:161], v[84:87], v[36:39], v[158:161]
	s_nop 6
	v_max_i32_e32 v154, 0, v154
	v_fmac_f32_e32 v153, v15, v154
	v_max_i32_e32 v154, 0, v158
	v_fmac_f32_e32 v149, v15, v154
	v_max_i32_e32 v154, 0, v155
	v_fmac_f32_e32 v152, v15, v154
	v_max_i32_e32 v154, 0, v159
	v_fmac_f32_e32 v148, v15, v154
	v_max_i32_e32 v154, 0, v156
	v_fmac_f32_e32 v151, v15, v154
	v_max_i32_e32 v154, 0, v160
	v_fmac_f32_e32 v147, v15, v154
	v_max_i32_e32 v154, 0, v157
	v_fmac_f32_e32 v150, v15, v154
	v_max_i32_e32 v154, 0, v161
	v_fmac_f32_e32 v146, v15, v154
	v_mfma_f32_16x16x32_bf16 v[154:157], v[72:75], v[40:43], 0
	v_mfma_f32_16x16x32_bf16 v[158:161], v[80:83], v[40:43], 0
	v_mfma_f32_16x16x32_bf16 v[154:157], v[76:79], v[44:47], v[154:157]
	v_mfma_f32_16x16x32_bf16 v[158:161], v[84:87], v[44:47], v[158:161]
	s_nop 6
	v_max_i32_e32 v154, 0, v154
	v_fmac_f32_e32 v153, v8, v154
	v_max_i32_e32 v154, 0, v158
	v_fmac_f32_e32 v149, v8, v154
	v_max_i32_e32 v154, 0, v155
	v_fmac_f32_e32 v152, v8, v154
	v_max_i32_e32 v154, 0, v159
	v_fmac_f32_e32 v148, v8, v154
	v_max_i32_e32 v154, 0, v156
	v_fmac_f32_e32 v151, v8, v154
	v_max_i32_e32 v154, 0, v160
	v_fmac_f32_e32 v147, v8, v154
	v_max_i32_e32 v154, 0, v157
	v_fmac_f32_e32 v150, v8, v154
	v_max_i32_e32 v154, 0, v161
	v_fmac_f32_e32 v146, v8, v154
	v_mfma_f32_16x16x32_bf16 v[154:157], v[72:75], v[48:51], 0
	v_mfma_f32_16x16x32_bf16 v[158:161], v[80:83], v[48:51], 0
	v_mfma_f32_16x16x32_bf16 v[154:157], v[76:79], v[52:55], v[154:157]
	v_mfma_f32_16x16x32_bf16 v[158:161], v[84:87], v[52:55], v[158:161]
	s_nop 6
	v_max_i32_e32 v154, 0, v154
	v_fmac_f32_e32 v153, v9, v154
	v_max_i32_e32 v154, 0, v158
	v_fmac_f32_e32 v149, v9, v154
	v_max_i32_e32 v154, 0, v155
	v_fmac_f32_e32 v152, v9, v154
	v_max_i32_e32 v154, 0, v159
	v_fmac_f32_e32 v148, v9, v154
	v_max_i32_e32 v154, 0, v156
	v_fmac_f32_e32 v151, v9, v154
	v_max_i32_e32 v154, 0, v160
	v_fmac_f32_e32 v147, v9, v154
	v_max_i32_e32 v154, 0, v157
	v_fmac_f32_e32 v150, v9, v154
	v_max_i32_e32 v154, 0, v161
	v_fmac_f32_e32 v146, v9, v154
	v_mfma_f32_16x16x32_bf16 v[154:157], v[72:75], v[56:59], 0
	v_mfma_f32_16x16x32_bf16 v[158:161], v[80:83], v[56:59], 0
	v_mfma_f32_16x16x32_bf16 v[154:157], v[76:79], v[60:63], v[154:157]
	v_mfma_f32_16x16x32_bf16 v[158:161], v[84:87], v[60:63], v[158:161]
	s_nop 6
	v_max_i32_e32 v154, 0, v154
	v_fmac_f32_e32 v153, v10, v154
	v_max_i32_e32 v154, 0, v158
	v_fmac_f32_e32 v149, v10, v154
	v_max_i32_e32 v154, 0, v155
	v_fmac_f32_e32 v152, v10, v154
	v_max_i32_e32 v154, 0, v159
	v_fmac_f32_e32 v148, v10, v154
	v_max_i32_e32 v154, 0, v156
	v_fmac_f32_e32 v151, v10, v154
	v_max_i32_e32 v154, 0, v160
	v_fmac_f32_e32 v147, v10, v154
	v_max_i32_e32 v154, 0, v157
	v_fmac_f32_e32 v150, v10, v154
	v_max_i32_e32 v154, 0, v161
	v_fmac_f32_e32 v146, v10, v154
	v_mfma_f32_16x16x32_bf16 v[154:157], v[72:75], v[64:67], 0
	v_mfma_f32_16x16x32_bf16 v[158:161], v[80:83], v[64:67], 0
	v_mfma_f32_16x16x32_bf16 v[154:157], v[76:79], v[68:71], v[154:157]
	v_mfma_f32_16x16x32_bf16 v[158:161], v[84:87], v[68:71], v[158:161]
	s_nop 6
	v_max_i32_e32 v154, 0, v154
	v_fmac_f32_e32 v153, v11, v154
	v_max_i32_e32 v154, 0, v158
	v_fmac_f32_e32 v149, v11, v154
	v_max_i32_e32 v154, 0, v155
	v_fmac_f32_e32 v152, v11, v154
	v_max_i32_e32 v154, 0, v159
	v_fmac_f32_e32 v148, v11, v154
	v_max_i32_e32 v154, 0, v156
	v_fmac_f32_e32 v151, v11, v154
	v_max_i32_e32 v154, 0, v160
	v_fmac_f32_e32 v147, v11, v154
	v_max_i32_e32 v154, 0, v157
	v_fmac_f32_e32 v150, v11, v154
	v_max_i32_e32 v154, 0, v161
	v_fmac_f32_e32 v146, v11, v154
	v_cmp_ge_f32_e64 s[66:67], v153, v140
	v_cmp_ge_f32_e64 s[50:51], v153, v139
	v_cmp_ge_f32_e32 vcc, v152, v140
	v_cmp_ge_f32_e64 s[52:53], v152, v139
	v_cndmask_b32_e64 v224, 0, 1, s[66:67]
	v_cndmask_b32_e64 v225, 0, 2, vcc
	s_andn2_b64 s[50:51], s[50:51], s[66:67]
	s_andn2_b64 s[52:53], s[52:53], vcc
	v_or_b32_e32 v228, v224, v225
	v_cmp_ge_f32_e64 s[66:67], v151, v140
	v_cmp_ge_f32_e64 s[54:55], v151, v139
	v_cmp_ge_f32_e32 vcc, v150, v140
	v_cmp_ge_f32_e64 s[56:57], v150, v139
	v_cndmask_b32_e64 v224, 0, 4, s[66:67]
	v_cndmask_b32_e64 v225, 0, 8, vcc
	s_andn2_b64 s[54:55], s[54:55], s[66:67]
	s_andn2_b64 s[56:57], s[56:57], vcc
	v_or3_b32 v228, v228, v224, v225
	v_cmp_ge_f32_e64 s[66:67], v149, v140
	v_cmp_ge_f32_e64 s[58:59], v149, v139
	v_cmp_ge_f32_e32 vcc, v148, v140
	v_cmp_ge_f32_e64 s[60:61], v148, v139
	v_cndmask_b32_e64 v224, 0, v201, s[66:67]
	v_cndmask_b32_e64 v225, 0, v200, vcc
	s_andn2_b64 s[58:59], s[58:59], s[66:67]
	s_andn2_b64 s[60:61], s[60:61], vcc
	v_or3_b32 v228, v228, v224, v225
	v_cmp_ge_f32_e64 s[66:67], v147, v140
	v_cmp_ge_f32_e64 s[62:63], v147, v139
	v_cmp_ge_f32_e32 vcc, v146, v140
	v_cmp_ge_f32_e64 s[64:65], v146, v139
	v_cndmask_b32_e64 v224, 0, v199, s[66:67]
	v_cndmask_b32_e64 v225, 0, v198, vcc
	s_andn2_b64 s[62:63], s[62:63], s[66:67]
	s_andn2_b64 s[64:65], s[64:65], vcc
	v_or3_b32 v228, v228, v224, v225
	v_add_u32_e32 v226, s74, v124
	v_mov_b32_e32 v227, s96
	s_mov_b64 s[14:15], exec
	s_mov_b64 exec, s[50:51]
	v_ashrrev_i32_e32 v206, 31, v153
	v_xor_b32_e32 v206, v206, v153
	v_lshrrev_b32_e32 v222, 9, v206
	v_lshrrev_b32_e32 v223, 6, v206
	v_and_b32_e32 v222, 0xffc, v222
	v_and_b32_e32 v223, 16, v223
	v_add_u32_e32 v222, v128, v222
	v_lshlrev_b32_e64 v223, v223, 1
	ds_add_u32 v222, v223
	s_mov_b64 exec, s[52:53]
	v_ashrrev_i32_e32 v207, 31, v152
	v_xor_b32_e32 v207, v207, v152
	v_lshrrev_b32_e32 v222, 9, v207
	v_lshrrev_b32_e32 v223, 6, v207
	v_and_b32_e32 v222, 0xffc, v222
	v_and_b32_e32 v223, 16, v223
	v_add_u32_e32 v222, v128, v222
	v_lshlrev_b32_e64 v223, v223, 1
	ds_add_u32 v222, v223
	s_mov_b64 exec, s[54:55]
	v_ashrrev_i32_e32 v208, 31, v151
	v_xor_b32_e32 v208, v208, v151
	v_lshrrev_b32_e32 v222, 9, v208
	v_lshrrev_b32_e32 v223, 6, v208
	v_and_b32_e32 v222, 0xffc, v222
	v_and_b32_e32 v223, 16, v223
	v_add_u32_e32 v222, v128, v222
	v_lshlrev_b32_e64 v223, v223, 1
	ds_add_u32 v222, v223
	s_mov_b64 exec, s[56:57]
	v_ashrrev_i32_e32 v209, 31, v150
	v_xor_b32_e32 v209, v209, v150
	v_lshrrev_b32_e32 v222, 9, v209
	v_lshrrev_b32_e32 v223, 6, v209
	v_and_b32_e32 v222, 0xffc, v222
	v_and_b32_e32 v223, 16, v223
	v_add_u32_e32 v222, v128, v222
	v_lshlrev_b32_e64 v223, v223, 1
	ds_add_u32 v222, v223
	s_mov_b64 exec, s[58:59]
	v_ashrrev_i32_e32 v210, 31, v149
	v_xor_b32_e32 v210, v210, v149
	v_lshrrev_b32_e32 v222, 9, v210
	v_lshrrev_b32_e32 v223, 6, v210
	v_and_b32_e32 v222, 0xffc, v222
	v_and_b32_e32 v223, 16, v223
	v_add_u32_e32 v222, v128, v222
	v_lshlrev_b32_e64 v223, v223, 1
	ds_add_u32 v222, v223
	s_mov_b64 exec, s[60:61]
	v_ashrrev_i32_e32 v211, 31, v148
	v_xor_b32_e32 v211, v211, v148
	v_lshrrev_b32_e32 v222, 9, v211
	v_lshrrev_b32_e32 v223, 6, v211
	v_and_b32_e32 v222, 0xffc, v222
	v_and_b32_e32 v223, 16, v223
	v_add_u32_e32 v222, v128, v222
	v_lshlrev_b32_e64 v223, v223, 1
	ds_add_u32 v222, v223
	s_mov_b64 exec, s[62:63]
	v_ashrrev_i32_e32 v212, 31, v147
	v_xor_b32_e32 v212, v212, v147
	v_lshrrev_b32_e32 v222, 9, v212
	v_lshrrev_b32_e32 v223, 6, v212
	v_and_b32_e32 v222, 0xffc, v222
	v_and_b32_e32 v223, 16, v223
	v_add_u32_e32 v222, v128, v222
	v_lshlrev_b32_e64 v223, v223, 1
	ds_add_u32 v222, v223
	s_mov_b64 exec, s[64:65]
	v_ashrrev_i32_e32 v213, 31, v146
	v_xor_b32_e32 v213, v213, v146
	v_lshrrev_b32_e32 v222, 9, v213
	v_lshrrev_b32_e32 v223, 6, v213
	v_and_b32_e32 v222, 0xffc, v222
	v_and_b32_e32 v223, 16, v223
	v_add_u32_e32 v222, v128, v222
	v_lshlrev_b32_e64 v223, v223, 1
	ds_add_u32 v222, v223
	s_waitcnt lgkmcnt(6)
	s_mov_b64 exec, s[50:51]
	ds_add_rtn_u32 v214, v142, v193
	s_mov_b64 exec, s[52:53]
	ds_add_rtn_u32 v215, v142, v193
	s_mov_b64 exec, s[54:55]
	ds_add_rtn_u32 v216, v142, v193
	s_mov_b64 exec, s[56:57]
	ds_add_rtn_u32 v217, v142, v193
	s_mov_b64 exec, s[58:59]
	ds_add_rtn_u32 v218, v142, v193
	s_mov_b64 exec, s[60:61]
	ds_add_rtn_u32 v219, v142, v193
	s_mov_b64 exec, s[62:63]
	ds_add_rtn_u32 v220, v142, v193
	s_mov_b64 exec, s[64:65]
	ds_add_rtn_u32 v221, v142, v193
	s_waitcnt lgkmcnt(0)
	s_mov_b64 exec, s[50:51]
	v_cmp_lt_u32_e64 s[66:67], s0, v214
	v_bfe_u32 v224, v206, 10, 11
	v_add_u32_e32 v225, 0x80000, v226
	v_lshl_add_u32 v222, v214, 2, v141
	v_add_u32_e32 v224, v225, v224
	s_andn2_b64 exec, exec, s[66:67]
	ds_write_b32 v222, v224
	s_mov_b64 exec, s[66:67]
	ds_write_b32 v227, v193
	s_mov_b64 exec, s[52:53]
	v_cmp_lt_u32_e64 s[66:67], s0, v215
	v_bfe_u32 v224, v207, 10, 11
	v_add_u32_e32 v225, 0x80800, v226
	v_lshl_add_u32 v222, v215, 2, v141
	v_add_u32_e32 v224, v225, v224
	s_andn2_b64 exec, exec, s[66:67]
	ds_write_b32 v222, v224
	s_mov_b64 exec, s[66:67]
	ds_write_b32 v227, v193
	s_mov_b64 exec, s[54:55]
	v_cmp_lt_u32_e64 s[66:67], s0, v216
	v_bfe_u32 v224, v208, 10, 11
	v_add_u32_e32 v225, 0x81000, v226
	v_lshl_add_u32 v222, v216, 2, v141
	v_add_u32_e32 v224, v225, v224
	s_andn2_b64 exec, exec, s[66:67]
	ds_write_b32 v222, v224
	s_mov_b64 exec, s[66:67]
	ds_write_b32 v227, v193
	s_mov_b64 exec, s[56:57]
	v_cmp_lt_u32_e64 s[66:67], s0, v217
	v_bfe_u32 v224, v209, 10, 11
	v_add_u32_e32 v225, 0x81800, v226
	v_lshl_add_u32 v222, v217, 2, v141
	v_add_u32_e32 v224, v225, v224
	s_andn2_b64 exec, exec, s[66:67]
	ds_write_b32 v222, v224
	s_mov_b64 exec, s[66:67]
	ds_write_b32 v227, v193
	s_waitcnt lgkmcnt(4)
	s_mov_b64 exec, s[58:59]
	v_cmp_lt_u32_e64 s[66:67], s0, v218
	v_bfe_u32 v224, v210, 10, 11
	v_add_u32_e32 v225, 0x88000, v226
	v_lshl_add_u32 v222, v218, 2, v141
	v_add_u32_e32 v224, v225, v224
	s_andn2_b64 exec, exec, s[66:67]
	ds_write_b32 v222, v224
	s_mov_b64 exec, s[66:67]
	ds_write_b32 v227, v193
	s_mov_b64 exec, s[60:61]
	v_cmp_lt_u32_e64 s[66:67], s0, v219
	v_bfe_u32 v224, v211, 10, 11
	v_add_u32_e32 v225, 0x88800, v226
	v_lshl_add_u32 v222, v219, 2, v141
	v_add_u32_e32 v224, v225, v224
	s_andn2_b64 exec, exec, s[66:67]
	ds_write_b32 v222, v224
	s_mov_b64 exec, s[66:67]
	ds_write_b32 v227, v193
	s_mov_b64 exec, s[62:63]
	v_cmp_lt_u32_e64 s[66:67], s0, v220
	v_bfe_u32 v224, v212, 10, 11
	v_add_u32_e32 v225, 0x89000, v226
	v_lshl_add_u32 v222, v220, 2, v141
	v_add_u32_e32 v224, v225, v224
	s_andn2_b64 exec, exec, s[66:67]
	ds_write_b32 v222, v224
	s_mov_b64 exec, s[66:67]
	ds_write_b32 v227, v193
	s_mov_b64 exec, s[64:65]
	v_cmp_lt_u32_e64 s[66:67], s0, v221
	v_bfe_u32 v224, v213, 10, 11
	v_add_u32_e32 v225, 0x89800, v226
	v_lshl_add_u32 v222, v221, 2, v141
	v_add_u32_e32 v224, v225, v224
	s_andn2_b64 exec, exec, s[66:67]
	ds_write_b32 v222, v224
	s_mov_b64 exec, s[66:67]
	ds_write_b32 v227, v193
	s_mov_b64 exec, s[14:15]
	v_mov_b32_e32 v146, v228
	v_lshlrev_b32_e32 v146, v143, v146
	ds_bpermute_b32 v147, v144, v146
	s_waitcnt lgkmcnt(0)
	v_or_b32_e32 v146, v147, v146
	ds_bpermute_b32 v147, v145, v146
	s_and_saveexec_b64 s[14:15], s[38:39]
	s_cbranch_execz .LBB0_1436
	s_waitcnt lgkmcnt(0)
	v_or_b32_e32 v148, v146, v147
	v_lshl_add_u64 v[146:147], v[122:123], 0, s[74:75]
	v_add_co_u32_e32 v146, vcc, 0x3f780000, v146
	s_nop 1
	v_addc_co_u32_e32 v147, vcc, 0, v147, vcc
	global_store_dword v[146:147], v148, off
	s_branch .LBB0_1436

.LBB0_1531:
	s_add_i32 s31, s31, 8
	s_cmp_ge_i32 s31, s82
	s_cselect_b64 s[36:37], -1, 0
	s_and_b64 vcc, exec, s[36:37]
	s_cbranch_vccnz .LBB0_1533
	v_ashrrev_i32_e32 v107, 31, v106
	v_lshlrev_b64 v[72:73], 7, v[106:107]
	v_sub_u32_e32 v72, v72, v229
	v_lshl_add_u64 v[84:85], v[120:121], 0, v[72:73]
	global_load_dwordx4 v[72:75], v[84:85], off
	global_load_dwordx4 v[76:79], v[84:85], off offset:1024
	global_load_dwordx4 v[80:83], v[84:85], off offset:2048
	s_nop 0
	global_load_dwordx4 v[84:87], v[84:85], off offset:3072

.LBB0_2001:
	s_add_u32 s5, s48, 0xfff80080
	s_addc_u32 s10, s49, -1
	s_add_i32 s31, 0, 0x10000
	s_cmp_eq_u32 s29, 28
	s_cselect_b32 s53, s45, s10
	s_cselect_b32 s52, s44, s5
	v_add_u32_e32 v144, s31, v146
	s_cselect_b32 s51, s47, s15
	s_cselect_b32 s50, s46, s14
	s_add_i32 s5, 0, 0x14000
	ds_read_b128 v[140:143], v144
	ds_read_b128 v[150:153], v144 offset:1024
	ds_read_b128 v[154:157], v144 offset:2048
	ds_read_b128 v[158:161], v144 offset:3072
	v_add_u32_e32 v144, s5, v146
	ds_read_b128 v[162:165], v144
	ds_read_b128 v[166:169], v144 offset:1024
	ds_read_b128 v[170:173], v144 offset:2048
	ds_read_b128 v[182:185], v144 offset:3072
	s_add_i32 m0, s59, 0xc000
	ds_read_b128 v[186:189], v149
	ds_read_b128 v[206:209], v149 offset:1024
	ds_read_b128 v[210:213], v149 offset:2048
	ds_read_b128 v[214:217], v149 offset:3072
	ds_read_b128 v[218:221], v149 offset:4096
	ds_read_b128 v[222:225], v149 offset:5120
	ds_read_b128 v[226:229], v149 offset:6144
	ds_read_b128 v[230:233], v149 offset:7168
	global_load_lds_dwordx4 v136, s[48:49]
	s_add_i32 m0, s59, 0xe000
	s_nop 0
	global_load_lds_dwordx4 v138, s[48:49]
	s_waitcnt vmcnt(8)
	s_waitcnt lgkmcnt(0)
	s_barrier
	s_setprio 1
	s_waitcnt lgkmcnt(0)
	v_mfma_f32_16x16x32_bf16 v[124:127], v[140:143], v[186:189], v[124:127]
	v_mfma_f32_16x16x32_bf16 v[120:123], v[154:157], v[186:189], v[120:123]
	v_mfma_f32_16x16x32_bf16 v[108:111], v[140:143], v[210:213], v[108:111]
	v_mfma_f32_16x16x32_bf16 v[104:107], v[154:157], v[210:213], v[104:107]
	v_mfma_f32_16x16x32_bf16 v[92:95], v[140:143], v[218:221], v[92:95]
	v_mfma_f32_16x16x32_bf16 v[88:91], v[154:157], v[218:221], v[88:91]
	v_mfma_f32_16x16x32_bf16 v[76:79], v[140:143], v[226:229], v[76:79]
	v_mfma_f32_16x16x32_bf16 v[72:75], v[154:157], v[226:229], v[72:75]
	v_mfma_f32_16x16x32_bf16 v[124:127], v[150:153], v[206:209], v[124:127]
	v_mfma_f32_16x16x32_bf16 v[120:123], v[158:161], v[206:209], v[120:123]
	v_mfma_f32_16x16x32_bf16 v[108:111], v[150:153], v[214:217], v[108:111]
	v_mfma_f32_16x16x32_bf16 v[104:107], v[158:161], v[214:217], v[104:107]
	v_mfma_f32_16x16x32_bf16 v[92:95], v[150:153], v[222:225], v[92:95]
	v_mfma_f32_16x16x32_bf16 v[88:91], v[158:161], v[222:225], v[88:91]
	v_mfma_f32_16x16x32_bf16 v[76:79], v[150:153], v[230:233], v[76:79]
	v_mfma_f32_16x16x32_bf16 v[72:75], v[158:161], v[230:233], v[72:75]
	s_setprio 0
	s_setprio 1
	v_mfma_f32_16x16x32_bf16 v[116:119], v[162:165], v[186:189], v[116:119]
	v_mfma_f32_16x16x32_bf16 v[112:115], v[170:173], v[186:189], v[112:115]
	v_mfma_f32_16x16x32_bf16 v[100:103], v[162:165], v[210:213], v[100:103]
	v_mfma_f32_16x16x32_bf16 v[96:99], v[170:173], v[210:213], v[96:99]
	v_mfma_f32_16x16x32_bf16 v[84:87], v[162:165], v[218:221], v[84:87]
	v_mfma_f32_16x16x32_bf16 v[80:83], v[170:173], v[218:221], v[80:83]
	v_mfma_f32_16x16x32_bf16 v[68:71], v[162:165], v[226:229], v[68:71]
	v_mfma_f32_16x16x32_bf16 v[64:67], v[170:173], v[226:229], v[64:67]
	v_mfma_f32_16x16x32_bf16 v[116:119], v[166:169], v[206:209], v[116:119]
	v_mfma_f32_16x16x32_bf16 v[112:115], v[182:185], v[206:209], v[112:115]
	v_mfma_f32_16x16x32_bf16 v[100:103], v[166:169], v[214:217], v[100:103]
	v_mfma_f32_16x16x32_bf16 v[96:99], v[182:185], v[214:217], v[96:99]
	v_mfma_f32_16x16x32_bf16 v[84:87], v[166:169], v[222:225], v[84:87]
	v_mfma_f32_16x16x32_bf16 v[80:83], v[182:185], v[222:225], v[80:83]
	v_mfma_f32_16x16x32_bf16 v[68:71], v[166:169], v[230:233], v[68:71]
	v_mfma_f32_16x16x32_bf16 v[64:67], v[182:185], v[230:233], v[64:67]
	s_setprio 0
	s_barrier
	s_add_i32 s10, s31, s58
	s_mov_b32 m0, s10
	ds_read_b128 v[186:189], v149 offset:16384
	ds_read_b128 v[206:209], v149 offset:17408
	ds_read_b128 v[210:213], v149 offset:18432
	ds_read_b128 v[214:217], v149 offset:19456
	ds_read_b128 v[218:221], v149 offset:20480
	ds_read_b128 v[222:225], v149 offset:21504
	ds_read_b128 v[226:229], v149 offset:22528
	ds_read_b128 v[230:233], v149 offset:23552
	global_load_lds_dwordx4 v176, s[50:51]
	s_add_i32 m0, s10, 0x2000
	s_add_u32 s74, s50, 0x80000
	s_addc_u32 s75, s51, 0
	s_add_i32 s5, s5, s58
	global_load_lds_dwordx4 v132, s[50:51]
	s_mov_b32 m0, s5
	s_nop 0
	global_load_lds_dwordx4 v176, s[74:75]
	s_add_i32 m0, s5, 0x2000
	s_nop 0
	global_load_lds_dwordx4 v132, s[74:75]
	s_mov_b32 m0, s59
	s_nop 0
	global_load_lds_dwordx4 v128, s[52:53]
	s_mov_b32 m0, s60
	s_nop 0
	global_load_lds_dwordx4 v130, s[52:53]
	s_waitcnt vmcnt(8)
	s_waitcnt lgkmcnt(0)
	s_barrier
	s_setprio 1
	s_waitcnt lgkmcnt(0)
	v_mfma_f32_16x16x32_bf16 v[60:63], v[140:143], v[186:189], v[60:63]
	v_mfma_f32_16x16x32_bf16 v[56:59], v[154:157], v[186:189], v[56:59]
	v_mfma_f32_16x16x32_bf16 v[44:47], v[140:143], v[210:213], v[44:47]
	v_mfma_f32_16x16x32_bf16 v[40:43], v[154:157], v[210:213], v[40:43]
	v_mfma_f32_16x16x32_bf16 v[28:31], v[140:143], v[218:221], v[28:31]
	v_mfma_f32_16x16x32_bf16 v[24:27], v[154:157], v[218:221], v[24:27]
	v_mfma_f32_16x16x32_bf16 v[12:15], v[140:143], v[226:229], v[12:15]
	v_mfma_f32_16x16x32_bf16 v[8:11], v[154:157], v[226:229], v[8:11]
	v_mfma_f32_16x16x32_bf16 v[60:63], v[150:153], v[206:209], v[60:63]
	v_mfma_f32_16x16x32_bf16 v[56:59], v[158:161], v[206:209], v[56:59]
	v_mfma_f32_16x16x32_bf16 v[44:47], v[150:153], v[214:217], v[44:47]
	v_mfma_f32_16x16x32_bf16 v[40:43], v[158:161], v[214:217], v[40:43]
	v_mfma_f32_16x16x32_bf16 v[28:31], v[150:153], v[222:225], v[28:31]
	v_mfma_f32_16x16x32_bf16 v[24:27], v[158:161], v[222:225], v[24:27]
	v_mfma_f32_16x16x32_bf16 v[12:15], v[150:153], v[230:233], v[12:15]
	v_mfma_f32_16x16x32_bf16 v[8:11], v[158:161], v[230:233], v[8:11]
	s_setprio 0
	s_setprio 1
	v_mfma_f32_16x16x32_bf16 v[52:55], v[162:165], v[186:189], v[52:55]
	v_mfma_f32_16x16x32_bf16 v[48:51], v[170:173], v[186:189], v[48:51]
	v_mfma_f32_16x16x32_bf16 v[36:39], v[162:165], v[210:213], v[36:39]
	v_mfma_f32_16x16x32_bf16 v[32:35], v[170:173], v[210:213], v[32:35]
	v_mfma_f32_16x16x32_bf16 v[20:23], v[162:165], v[218:221], v[20:23]
	v_mfma_f32_16x16x32_bf16 v[16:19], v[170:173], v[218:221], v[16:19]
	v_mfma_f32_16x16x32_bf16 v[4:7], v[162:165], v[226:229], v[4:7]
	v_mfma_f32_16x16x32_bf16 v[0:3], v[170:173], v[226:229], v[0:3]
	v_mfma_f32_16x16x32_bf16 v[52:55], v[166:169], v[206:209], v[52:55]
	v_mfma_f32_16x16x32_bf16 v[48:51], v[182:185], v[206:209], v[48:51]
	v_mfma_f32_16x16x32_bf16 v[36:39], v[166:169], v[214:217], v[36:39]
	v_mfma_f32_16x16x32_bf16 v[32:35], v[182:185], v[214:217], v[32:35]
	v_mfma_f32_16x16x32_bf16 v[20:23], v[166:169], v[222:225], v[20:23]
	v_mfma_f32_16x16x32_bf16 v[16:19], v[182:185], v[222:225], v[16:19]
	v_mfma_f32_16x16x32_bf16 v[4:7], v[166:169], v[230:233], v[4:7]
	v_mfma_f32_16x16x32_bf16 v[0:3], v[182:185], v[230:233], v[0:3]
	s_setprio 0
	s_barrier
	s_add_i32 s5, 0, 0x18000
	s_add_i32 s10, 0, 0x1c000
	v_add_u32_e32 v158, s5, v146
	v_add_u32_e32 v178, s10, v146
	ds_read_b128 v[140:143], v158
	ds_read_b128 v[150:153], v158 offset:1024
	ds_read_b128 v[154:157], v158 offset:2048
	ds_read_b128 v[158:161], v158 offset:3072
	ds_read_b128 v[162:165], v178
	ds_read_b128 v[166:169], v178 offset:1024
	ds_read_b128 v[170:173], v178 offset:2048
	ds_read_b128 v[182:185], v178 offset:3072
	s_add_u32 s52, s52, 0x80000
	s_addc_u32 s53, s53, 0
	s_mov_b32 m0, s61
	ds_read_b128 v[186:189], v149 offset:32768
	ds_read_b128 v[206:209], v149 offset:33792
	ds_read_b128 v[210:213], v149 offset:34816
	ds_read_b128 v[214:217], v149 offset:35840
	ds_read_b128 v[218:221], v149 offset:36864
	ds_read_b128 v[222:225], v149 offset:37888
	ds_read_b128 v[226:229], v149 offset:38912
	ds_read_b128 v[230:233], v149 offset:39936
	global_load_lds_dwordx4 v128, s[52:53]
	s_mov_b32 m0, s62
	s_nop 0
	global_load_lds_dwordx4 v130, s[52:53]
	s_waitcnt vmcnt(8)
	s_waitcnt lgkmcnt(0)
	s_barrier
	s_setprio 1
	s_waitcnt lgkmcnt(0)
	v_mfma_f32_16x16x32_bf16 v[124:127], v[140:143], v[186:189], v[124:127]
	v_mfma_f32_16x16x32_bf16 v[120:123], v[154:157], v[186:189], v[120:123]
	v_mfma_f32_16x16x32_bf16 v[108:111], v[140:143], v[210:213], v[108:111]
	v_mfma_f32_16x16x32_bf16 v[104:107], v[154:157], v[210:213], v[104:107]
	v_mfma_f32_16x16x32_bf16 v[92:95], v[140:143], v[218:221], v[92:95]
	v_mfma_f32_16x16x32_bf16 v[88:91], v[154:157], v[218:221], v[88:91]
	v_mfma_f32_16x16x32_bf16 v[76:79], v[140:143], v[226:229], v[76:79]
	v_mfma_f32_16x16x32_bf16 v[72:75], v[154:157], v[226:229], v[72:75]
	v_mfma_f32_16x16x32_bf16 v[124:127], v[150:153], v[206:209], v[124:127]
	v_mfma_f32_16x16x32_bf16 v[120:123], v[158:161], v[206:209], v[120:123]
	v_mfma_f32_16x16x32_bf16 v[108:111], v[150:153], v[214:217], v[108:111]
	v_mfma_f32_16x16x32_bf16 v[104:107], v[158:161], v[214:217], v[104:107]
	v_mfma_f32_16x16x32_bf16 v[92:95], v[150:153], v[222:225], v[92:95]
	v_mfma_f32_16x16x32_bf16 v[88:91], v[158:161], v[222:225], v[88:91]
	v_mfma_f32_16x16x32_bf16 v[76:79], v[150:153], v[230:233], v[76:79]
	v_mfma_f32_16x16x32_bf16 v[72:75], v[158:161], v[230:233], v[72:75]
	s_setprio 0
	s_setprio 1
	v_mfma_f32_16x16x32_bf16 v[116:119], v[162:165], v[186:189], v[116:119]
	v_mfma_f32_16x16x32_bf16 v[112:115], v[170:173], v[186:189], v[112:115]
	v_mfma_f32_16x16x32_bf16 v[100:103], v[162:165], v[210:213], v[100:103]
	v_mfma_f32_16x16x32_bf16 v[96:99], v[170:173], v[210:213], v[96:99]
	v_mfma_f32_16x16x32_bf16 v[84:87], v[162:165], v[218:221], v[84:87]
	v_mfma_f32_16x16x32_bf16 v[80:83], v[170:173], v[218:221], v[80:83]
	v_mfma_f32_16x16x32_bf16 v[68:71], v[162:165], v[226:229], v[68:71]
	v_mfma_f32_16x16x32_bf16 v[64:67], v[170:173], v[226:229], v[64:67]
	v_mfma_f32_16x16x32_bf16 v[116:119], v[166:169], v[206:209], v[116:119]
	v_mfma_f32_16x16x32_bf16 v[112:115], v[182:185], v[206:209], v[112:115]
	v_mfma_f32_16x16x32_bf16 v[100:103], v[166:169], v[214:217], v[100:103]
	v_mfma_f32_16x16x32_bf16 v[96:99], v[182:185], v[214:217], v[96:99]
	v_mfma_f32_16x16x32_bf16 v[84:87], v[166:169], v[222:225], v[84:87]
	v_mfma_f32_16x16x32_bf16 v[80:83], v[182:185], v[222:225], v[80:83]
	v_mfma_f32_16x16x32_bf16 v[68:71], v[166:169], v[230:233], v[68:71]
	v_mfma_f32_16x16x32_bf16 v[64:67], v[182:185], v[230:233], v[64:67]
	s_setprio 0
	s_barrier
	s_add_i32 s5, s5, s58
	s_mov_b32 m0, s5
	ds_read_b128 v[186:189], v149 offset:49152
	ds_read_b128 v[206:209], v149 offset:50176
	ds_read_b128 v[210:213], v149 offset:51200
	ds_read_b128 v[214:217], v149 offset:52224
	ds_read_b128 v[218:221], v149 offset:53248
	ds_read_b128 v[222:225], v149 offset:54272
	ds_read_b128 v[226:229], v149 offset:55296
	ds_read_b128 v[230:233], v149 offset:56320
	s_add_u32 s74, s50, 0x80
	s_addc_u32 s75, s51, 0
	global_load_lds_dwordx4 v176, s[74:75]
	s_add_i32 m0, s5, 0x2000
	s_add_u32 s50, s50, 0x80080
	s_addc_u32 s51, s51, 0
	s_add_i32 s5, s10, s58
	s_add_u32 s74, s50, 0xfff80000
	s_addc_u32 s75, s51, -1
	global_load_lds_dwordx4 v132, s[74:75]
	s_mov_b32 m0, s5
	s_nop 0
	global_load_lds_dwordx4 v176, s[50:51]
	s_add_i32 m0, s5, 0x2000
	s_nop 0
	global_load_lds_dwordx4 v132, s[50:51]
	s_mov_b32 m0, s64
	s_nop 0
	s_add_u32 s74, s52, 0xfff80080
	s_addc_u32 s75, s53, -1
	global_load_lds_dwordx4 v128, s[74:75]
	s_mov_b32 m0, s65
	s_nop 0
	s_add_u32 s74, s52, 0xfff80080
	s_addc_u32 s75, s53, -1
	global_load_lds_dwordx4 v130, s[74:75]
	s_waitcnt vmcnt(8)
	s_waitcnt lgkmcnt(0)
	s_barrier
	s_setprio 1
	s_waitcnt lgkmcnt(0)
	v_mfma_f32_16x16x32_bf16 v[60:63], v[140:143], v[186:189], v[60:63]
	v_mfma_f32_16x16x32_bf16 v[56:59], v[154:157], v[186:189], v[56:59]
	v_mfma_f32_16x16x32_bf16 v[44:47], v[140:143], v[210:213], v[44:47]
	v_mfma_f32_16x16x32_bf16 v[40:43], v[154:157], v[210:213], v[40:43]
	v_mfma_f32_16x16x32_bf16 v[28:31], v[140:143], v[218:221], v[28:31]
	v_mfma_f32_16x16x32_bf16 v[24:27], v[154:157], v[218:221], v[24:27]
	v_mfma_f32_16x16x32_bf16 v[12:15], v[140:143], v[226:229], v[12:15]
	v_mfma_f32_16x16x32_bf16 v[8:11], v[154:157], v[226:229], v[8:11]
	v_mfma_f32_16x16x32_bf16 v[60:63], v[150:153], v[206:209], v[60:63]
	v_mfma_f32_16x16x32_bf16 v[56:59], v[158:161], v[206:209], v[56:59]
	v_mfma_f32_16x16x32_bf16 v[44:47], v[150:153], v[214:217], v[44:47]
	v_mfma_f32_16x16x32_bf16 v[40:43], v[158:161], v[214:217], v[40:43]
	v_mfma_f32_16x16x32_bf16 v[28:31], v[150:153], v[222:225], v[28:31]
	v_mfma_f32_16x16x32_bf16 v[24:27], v[158:161], v[222:225], v[24:27]
	v_mfma_f32_16x16x32_bf16 v[12:15], v[150:153], v[230:233], v[12:15]
	v_mfma_f32_16x16x32_bf16 v[8:11], v[158:161], v[230:233], v[8:11]
	s_setprio 0
	s_setprio 1
	v_mfma_f32_16x16x32_bf16 v[52:55], v[162:165], v[186:189], v[52:55]
	v_mfma_f32_16x16x32_bf16 v[48:51], v[170:173], v[186:189], v[48:51]
	v_mfma_f32_16x16x32_bf16 v[36:39], v[162:165], v[210:213], v[36:39]
	v_mfma_f32_16x16x32_bf16 v[32:35], v[170:173], v[210:213], v[32:35]
	v_mfma_f32_16x16x32_bf16 v[20:23], v[162:165], v[218:221], v[20:23]
	v_mfma_f32_16x16x32_bf16 v[16:19], v[170:173], v[218:221], v[16:19]
	v_mfma_f32_16x16x32_bf16 v[4:7], v[162:165], v[226:229], v[4:7]
	v_mfma_f32_16x16x32_bf16 v[0:3], v[170:173], v[226:229], v[0:3]
	v_mfma_f32_16x16x32_bf16 v[52:55], v[166:169], v[206:209], v[52:55]
	v_mfma_f32_16x16x32_bf16 v[48:51], v[182:185], v[206:209], v[48:51]
	v_mfma_f32_16x16x32_bf16 v[36:39], v[166:169], v[214:217], v[36:39]
	v_mfma_f32_16x16x32_bf16 v[32:35], v[182:185], v[214:217], v[32:35]
	v_mfma_f32_16x16x32_bf16 v[20:23], v[166:169], v[222:225], v[20:23]
	v_mfma_f32_16x16x32_bf16 v[16:19], v[182:185], v[222:225], v[16:19]
	v_mfma_f32_16x16x32_bf16 v[4:7], v[166:169], v[230:233], v[4:7]
	v_mfma_f32_16x16x32_bf16 v[0:3], v[182:185], v[230:233], v[0:3]
	s_setprio 0
	s_barrier
	s_add_i32 s29, s29, 2
	s_add_u32 s48, s48, 0x100
	s_addc_u32 s49, s49, 0
	s_add_u32 s14, s14, 0x100
	s_addc_u32 s15, s15, 0
	s_cmp_gt_u32 s29, 29
	s_cbranch_scc0 .LBB0_2001
	s_and_b64 vcc, exec, s[26:27]
	s_cbranch_vccz .LBB0_2004
	s_barrier

.LBB0_2084:
	s_add_u32 s5, s50, 0xfff80080
	s_addc_u32 s10, s51, -1
	s_add_i32 s29, 0, 0x10000
	s_cmp_eq_u32 s27, 28
	s_cselect_b32 s55, s47, s10
	s_cselect_b32 s54, s46, s5
	v_add_u32_e32 v154, s29, v157
	s_cselect_b32 s53, s49, s15
	s_cselect_b32 s52, s48, s14
	s_add_i32 s5, 0, 0x14000
	ds_read_b128 v[142:145], v154
	ds_read_b128 v[146:149], v154 offset:1024
	ds_read_b128 v[150:153], v154 offset:2048
	ds_read_b128 v[188:191], v154 offset:3072
	v_add_u32_e32 v154, s5, v157
	ds_read_b128 v[206:209], v154
	ds_read_b128 v[210:213], v154 offset:1024
	ds_read_b128 v[214:217], v154 offset:2048
	ds_read_b128 v[218:221], v154 offset:3072
	s_add_i32 m0, s60, 0xc000
	ds_read_b128 v[222:225], v186
	ds_read_b128 v[226:229], v186 offset:1024
	ds_read_b128 v[230:233], v186 offset:2048
	ds_read_b128 v[234:237], v186 offset:3072
	ds_read_b128 v[238:241], v186 offset:4096
	ds_read_b128 v[242:245], v186 offset:5120
	ds_read_b128 v[246:249], v186 offset:6144
	ds_read_b128 v[250:253], v186 offset:7168
	global_load_lds_dwordx4 v138, s[50:51]
	s_add_i32 m0, s60, 0xe000
	s_nop 0
	global_load_lds_dwordx4 v140, s[50:51]
	s_waitcnt vmcnt(8)
	s_waitcnt lgkmcnt(0)
	s_barrier
	s_setprio 1
	s_waitcnt lgkmcnt(0)
	v_mfma_f32_16x16x32_bf16 v[124:127], v[142:145], v[222:225], v[124:127]
	v_mfma_f32_16x16x32_bf16 v[120:123], v[150:153], v[222:225], v[120:123]
	v_mfma_f32_16x16x32_bf16 v[108:111], v[142:145], v[230:233], v[108:111]
	v_mfma_f32_16x16x32_bf16 v[104:107], v[150:153], v[230:233], v[104:107]
	v_mfma_f32_16x16x32_bf16 v[92:95], v[142:145], v[238:241], v[92:95]
	v_mfma_f32_16x16x32_bf16 v[88:91], v[150:153], v[238:241], v[88:91]
	v_mfma_f32_16x16x32_bf16 v[76:79], v[142:145], v[246:249], v[76:79]
	v_mfma_f32_16x16x32_bf16 v[72:75], v[150:153], v[246:249], v[72:75]
	v_mfma_f32_16x16x32_bf16 v[124:127], v[146:149], v[226:229], v[124:127]
	v_mfma_f32_16x16x32_bf16 v[120:123], v[188:191], v[226:229], v[120:123]
	v_mfma_f32_16x16x32_bf16 v[108:111], v[146:149], v[234:237], v[108:111]
	v_mfma_f32_16x16x32_bf16 v[104:107], v[188:191], v[234:237], v[104:107]
	v_mfma_f32_16x16x32_bf16 v[92:95], v[146:149], v[242:245], v[92:95]
	v_mfma_f32_16x16x32_bf16 v[88:91], v[188:191], v[242:245], v[88:91]
	v_mfma_f32_16x16x32_bf16 v[76:79], v[146:149], v[250:253], v[76:79]
	v_mfma_f32_16x16x32_bf16 v[72:75], v[188:191], v[250:253], v[72:75]
	s_setprio 0
	s_setprio 1
	v_mfma_f32_16x16x32_bf16 v[116:119], v[206:209], v[222:225], v[116:119]
	v_mfma_f32_16x16x32_bf16 v[112:115], v[214:217], v[222:225], v[112:115]
	v_mfma_f32_16x16x32_bf16 v[100:103], v[206:209], v[230:233], v[100:103]
	v_mfma_f32_16x16x32_bf16 v[96:99], v[214:217], v[230:233], v[96:99]
	v_mfma_f32_16x16x32_bf16 v[84:87], v[206:209], v[238:241], v[84:87]
	v_mfma_f32_16x16x32_bf16 v[80:83], v[214:217], v[238:241], v[80:83]
	v_mfma_f32_16x16x32_bf16 v[68:71], v[206:209], v[246:249], v[68:71]
	v_mfma_f32_16x16x32_bf16 v[64:67], v[214:217], v[246:249], v[64:67]
	v_mfma_f32_16x16x32_bf16 v[116:119], v[210:213], v[226:229], v[116:119]
	v_mfma_f32_16x16x32_bf16 v[112:115], v[218:221], v[226:229], v[112:115]
	v_mfma_f32_16x16x32_bf16 v[100:103], v[210:213], v[234:237], v[100:103]
	v_mfma_f32_16x16x32_bf16 v[96:99], v[218:221], v[234:237], v[96:99]
	v_mfma_f32_16x16x32_bf16 v[84:87], v[210:213], v[242:245], v[84:87]
	v_mfma_f32_16x16x32_bf16 v[80:83], v[218:221], v[242:245], v[80:83]
	v_mfma_f32_16x16x32_bf16 v[68:71], v[210:213], v[250:253], v[68:71]
	v_mfma_f32_16x16x32_bf16 v[64:67], v[218:221], v[250:253], v[64:67]
	s_setprio 0
	s_barrier
	s_add_i32 s10, s29, s45
	s_mov_b32 m0, s10
	ds_read_b128 v[222:225], v186 offset:16384
	ds_read_b128 v[226:229], v186 offset:17408
	ds_read_b128 v[230:233], v186 offset:18432
	ds_read_b128 v[234:237], v186 offset:19456
	ds_read_b128 v[238:241], v186 offset:20480
	ds_read_b128 v[242:245], v186 offset:21504
	ds_read_b128 v[246:249], v186 offset:22528
	ds_read_b128 v[250:253], v186 offset:23552
	global_load_lds_dwordx4 v130, s[52:53]
	s_add_i32 m0, s10, 0x2000
	s_add_u32 s74, s52, 0x80000
	s_addc_u32 s75, s53, 0
	s_add_i32 s5, s5, s45
	global_load_lds_dwordx4 v134, s[52:53]
	s_mov_b32 m0, s5
	s_nop 0
	global_load_lds_dwordx4 v130, s[74:75]
	s_add_i32 m0, s5, 0x2000
	s_nop 0
	global_load_lds_dwordx4 v134, s[74:75]
	s_mov_b32 m0, s60
	s_nop 0
	global_load_lds_dwordx4 v128, s[54:55]
	s_mov_b32 m0, s61
	s_nop 0
	global_load_lds_dwordx4 v132, s[54:55]
	s_waitcnt vmcnt(8)
	s_waitcnt lgkmcnt(0)
	s_barrier
	s_setprio 1
	s_waitcnt lgkmcnt(0)
	v_mfma_f32_16x16x32_bf16 v[60:63], v[142:145], v[222:225], v[60:63]
	v_mfma_f32_16x16x32_bf16 v[56:59], v[150:153], v[222:225], v[56:59]
	v_mfma_f32_16x16x32_bf16 v[44:47], v[142:145], v[230:233], v[44:47]
	v_mfma_f32_16x16x32_bf16 v[40:43], v[150:153], v[230:233], v[40:43]
	v_mfma_f32_16x16x32_bf16 v[28:31], v[142:145], v[238:241], v[28:31]
	v_mfma_f32_16x16x32_bf16 v[24:27], v[150:153], v[238:241], v[24:27]
	v_mfma_f32_16x16x32_bf16 v[12:15], v[142:145], v[246:249], v[12:15]
	v_mfma_f32_16x16x32_bf16 v[8:11], v[150:153], v[246:249], v[8:11]
	v_mfma_f32_16x16x32_bf16 v[60:63], v[146:149], v[226:229], v[60:63]
	v_mfma_f32_16x16x32_bf16 v[56:59], v[188:191], v[226:229], v[56:59]
	v_mfma_f32_16x16x32_bf16 v[44:47], v[146:149], v[234:237], v[44:47]
	v_mfma_f32_16x16x32_bf16 v[40:43], v[188:191], v[234:237], v[40:43]
	v_mfma_f32_16x16x32_bf16 v[28:31], v[146:149], v[242:245], v[28:31]
	v_mfma_f32_16x16x32_bf16 v[24:27], v[188:191], v[242:245], v[24:27]
	v_mfma_f32_16x16x32_bf16 v[12:15], v[146:149], v[250:253], v[12:15]
	v_mfma_f32_16x16x32_bf16 v[8:11], v[188:191], v[250:253], v[8:11]
	s_setprio 0
	s_setprio 1
	v_mfma_f32_16x16x32_bf16 v[52:55], v[206:209], v[222:225], v[52:55]
	v_mfma_f32_16x16x32_bf16 v[48:51], v[214:217], v[222:225], v[48:51]
	v_mfma_f32_16x16x32_bf16 v[36:39], v[206:209], v[230:233], v[36:39]
	v_mfma_f32_16x16x32_bf16 v[32:35], v[214:217], v[230:233], v[32:35]
	v_mfma_f32_16x16x32_bf16 v[20:23], v[206:209], v[238:241], v[20:23]
	v_mfma_f32_16x16x32_bf16 v[16:19], v[214:217], v[238:241], v[16:19]
	v_mfma_f32_16x16x32_bf16 v[4:7], v[206:209], v[246:249], v[4:7]
	v_mfma_f32_16x16x32_bf16 v[0:3], v[214:217], v[246:249], v[0:3]
	v_mfma_f32_16x16x32_bf16 v[52:55], v[210:213], v[226:229], v[52:55]
	v_mfma_f32_16x16x32_bf16 v[48:51], v[218:221], v[226:229], v[48:51]
	v_mfma_f32_16x16x32_bf16 v[36:39], v[210:213], v[234:237], v[36:39]
	v_mfma_f32_16x16x32_bf16 v[32:35], v[218:221], v[234:237], v[32:35]
	v_mfma_f32_16x16x32_bf16 v[20:23], v[210:213], v[242:245], v[20:23]
	v_mfma_f32_16x16x32_bf16 v[16:19], v[218:221], v[242:245], v[16:19]
	v_mfma_f32_16x16x32_bf16 v[4:7], v[210:213], v[250:253], v[4:7]
	v_mfma_f32_16x16x32_bf16 v[0:3], v[218:221], v[250:253], v[0:3]
	s_setprio 0
	s_barrier
	s_add_i32 s5, 0, 0x18000
	v_add_u32_e32 v187, s5, v157
	s_add_i32 s10, 0, 0x1c000
	ds_read_b128 v[142:145], v187
	ds_read_b128 v[146:149], v187 offset:1024
	ds_read_b128 v[150:153], v187 offset:2048
	ds_read_b128 v[188:191], v187 offset:3072
	v_add_u32_e32 v187, s10, v157
	ds_read_b128 v[206:209], v187
	ds_read_b128 v[210:213], v187 offset:1024
	ds_read_b128 v[214:217], v187 offset:2048
	ds_read_b128 v[218:221], v187 offset:3072
	s_add_u32 s54, s54, 0x80000
	s_addc_u32 s55, s55, 0
	s_mov_b32 m0, s62
	ds_read_b128 v[222:225], v186 offset:32768
	ds_read_b128 v[226:229], v186 offset:33792
	ds_read_b128 v[230:233], v186 offset:34816
	ds_read_b128 v[234:237], v186 offset:35840
	ds_read_b128 v[238:241], v186 offset:36864
	ds_read_b128 v[242:245], v186 offset:37888
	ds_read_b128 v[246:249], v186 offset:38912
	ds_read_b128 v[250:253], v186 offset:39936
	global_load_lds_dwordx4 v128, s[54:55]
	s_mov_b32 m0, s63
	s_nop 0
	global_load_lds_dwordx4 v132, s[54:55]
	s_waitcnt vmcnt(8)
	s_waitcnt lgkmcnt(0)
	s_barrier
	s_setprio 1
	s_waitcnt lgkmcnt(0)
	v_mfma_f32_16x16x32_bf16 v[124:127], v[142:145], v[222:225], v[124:127]
	v_mfma_f32_16x16x32_bf16 v[120:123], v[150:153], v[222:225], v[120:123]
	v_mfma_f32_16x16x32_bf16 v[108:111], v[142:145], v[230:233], v[108:111]
	v_mfma_f32_16x16x32_bf16 v[104:107], v[150:153], v[230:233], v[104:107]
	v_mfma_f32_16x16x32_bf16 v[92:95], v[142:145], v[238:241], v[92:95]
	v_mfma_f32_16x16x32_bf16 v[88:91], v[150:153], v[238:241], v[88:91]
	v_mfma_f32_16x16x32_bf16 v[76:79], v[142:145], v[246:249], v[76:79]
	v_mfma_f32_16x16x32_bf16 v[72:75], v[150:153], v[246:249], v[72:75]
	v_mfma_f32_16x16x32_bf16 v[124:127], v[146:149], v[226:229], v[124:127]
	v_mfma_f32_16x16x32_bf16 v[120:123], v[188:191], v[226:229], v[120:123]
	v_mfma_f32_16x16x32_bf16 v[108:111], v[146:149], v[234:237], v[108:111]
	v_mfma_f32_16x16x32_bf16 v[104:107], v[188:191], v[234:237], v[104:107]
	v_mfma_f32_16x16x32_bf16 v[92:95], v[146:149], v[242:245], v[92:95]
	v_mfma_f32_16x16x32_bf16 v[88:91], v[188:191], v[242:245], v[88:91]
	v_mfma_f32_16x16x32_bf16 v[76:79], v[146:149], v[250:253], v[76:79]
	v_mfma_f32_16x16x32_bf16 v[72:75], v[188:191], v[250:253], v[72:75]
	s_setprio 0
	s_setprio 1
	v_mfma_f32_16x16x32_bf16 v[116:119], v[206:209], v[222:225], v[116:119]
	v_mfma_f32_16x16x32_bf16 v[112:115], v[214:217], v[222:225], v[112:115]
	v_mfma_f32_16x16x32_bf16 v[100:103], v[206:209], v[230:233], v[100:103]
	v_mfma_f32_16x16x32_bf16 v[96:99], v[214:217], v[230:233], v[96:99]
	v_mfma_f32_16x16x32_bf16 v[84:87], v[206:209], v[238:241], v[84:87]
	v_mfma_f32_16x16x32_bf16 v[80:83], v[214:217], v[238:241], v[80:83]
	v_mfma_f32_16x16x32_bf16 v[68:71], v[206:209], v[246:249], v[68:71]
	v_mfma_f32_16x16x32_bf16 v[64:67], v[214:217], v[246:249], v[64:67]
	v_mfma_f32_16x16x32_bf16 v[116:119], v[210:213], v[226:229], v[116:119]
	v_mfma_f32_16x16x32_bf16 v[112:115], v[218:221], v[226:229], v[112:115]
	v_mfma_f32_16x16x32_bf16 v[100:103], v[210:213], v[234:237], v[100:103]
	v_mfma_f32_16x16x32_bf16 v[96:99], v[218:221], v[234:237], v[96:99]
	v_mfma_f32_16x16x32_bf16 v[84:87], v[210:213], v[242:245], v[84:87]
	v_mfma_f32_16x16x32_bf16 v[80:83], v[218:221], v[242:245], v[80:83]
	v_mfma_f32_16x16x32_bf16 v[68:71], v[210:213], v[250:253], v[68:71]
	v_mfma_f32_16x16x32_bf16 v[64:67], v[218:221], v[250:253], v[64:67]
	s_setprio 0
	s_barrier
	s_add_i32 s5, s5, s45
	s_mov_b32 m0, s5
	ds_read_b128 v[222:225], v186 offset:49152
	ds_read_b128 v[226:229], v186 offset:50176
	ds_read_b128 v[230:233], v186 offset:51200
	ds_read_b128 v[234:237], v186 offset:52224
	ds_read_b128 v[238:241], v186 offset:53248
	ds_read_b128 v[242:245], v186 offset:54272
	ds_read_b128 v[246:249], v186 offset:55296
	ds_read_b128 v[250:253], v186 offset:56320
	s_add_u32 s74, s52, 0x80
	s_addc_u32 s75, s53, 0
	global_load_lds_dwordx4 v130, s[74:75]
	s_add_i32 m0, s5, 0x2000
	s_add_u32 s52, s52, 0x80080
	s_addc_u32 s53, s53, 0
	s_add_i32 s5, s10, s45
	s_add_u32 s74, s52, 0xfff80000
	s_addc_u32 s75, s53, -1
	global_load_lds_dwordx4 v134, s[74:75]
	s_mov_b32 m0, s5
	s_nop 0
	global_load_lds_dwordx4 v130, s[52:53]
	s_add_i32 m0, s5, 0x2000
	s_nop 0
	global_load_lds_dwordx4 v134, s[52:53]
	s_mov_b32 m0, s64
	s_nop 0
	s_add_u32 s74, s54, 0xfff80080
	s_addc_u32 s75, s55, -1
	global_load_lds_dwordx4 v128, s[74:75]
	s_mov_b32 m0, s65
	s_nop 0
	s_add_u32 s74, s54, 0xfff80080
	s_addc_u32 s75, s55, -1
	global_load_lds_dwordx4 v132, s[74:75]
	s_waitcnt vmcnt(8)
	s_waitcnt lgkmcnt(0)
	s_barrier
	s_setprio 1
	s_waitcnt lgkmcnt(0)
	v_mfma_f32_16x16x32_bf16 v[60:63], v[142:145], v[222:225], v[60:63]
	v_mfma_f32_16x16x32_bf16 v[56:59], v[150:153], v[222:225], v[56:59]
	v_mfma_f32_16x16x32_bf16 v[44:47], v[142:145], v[230:233], v[44:47]
	v_mfma_f32_16x16x32_bf16 v[40:43], v[150:153], v[230:233], v[40:43]
	v_mfma_f32_16x16x32_bf16 v[28:31], v[142:145], v[238:241], v[28:31]
	v_mfma_f32_16x16x32_bf16 v[24:27], v[150:153], v[238:241], v[24:27]
	v_mfma_f32_16x16x32_bf16 v[12:15], v[142:145], v[246:249], v[12:15]
	v_mfma_f32_16x16x32_bf16 v[8:11], v[150:153], v[246:249], v[8:11]
	v_mfma_f32_16x16x32_bf16 v[60:63], v[146:149], v[226:229], v[60:63]
	v_mfma_f32_16x16x32_bf16 v[56:59], v[188:191], v[226:229], v[56:59]
	v_mfma_f32_16x16x32_bf16 v[44:47], v[146:149], v[234:237], v[44:47]
	v_mfma_f32_16x16x32_bf16 v[40:43], v[188:191], v[234:237], v[40:43]
	v_mfma_f32_16x16x32_bf16 v[28:31], v[146:149], v[242:245], v[28:31]
	v_mfma_f32_16x16x32_bf16 v[24:27], v[188:191], v[242:245], v[24:27]
	v_mfma_f32_16x16x32_bf16 v[12:15], v[146:149], v[250:253], v[12:15]
	v_mfma_f32_16x16x32_bf16 v[8:11], v[188:191], v[250:253], v[8:11]
	s_setprio 0
	s_setprio 1
	v_mfma_f32_16x16x32_bf16 v[52:55], v[206:209], v[222:225], v[52:55]
	v_mfma_f32_16x16x32_bf16 v[48:51], v[214:217], v[222:225], v[48:51]
	v_mfma_f32_16x16x32_bf16 v[36:39], v[206:209], v[230:233], v[36:39]
	v_mfma_f32_16x16x32_bf16 v[32:35], v[214:217], v[230:233], v[32:35]
	v_mfma_f32_16x16x32_bf16 v[20:23], v[206:209], v[238:241], v[20:23]
	v_mfma_f32_16x16x32_bf16 v[16:19], v[214:217], v[238:241], v[16:19]
	v_mfma_f32_16x16x32_bf16 v[4:7], v[206:209], v[246:249], v[4:7]
	v_mfma_f32_16x16x32_bf16 v[0:3], v[214:217], v[246:249], v[0:3]
	v_mfma_f32_16x16x32_bf16 v[52:55], v[210:213], v[226:229], v[52:55]
	v_mfma_f32_16x16x32_bf16 v[48:51], v[218:221], v[226:229], v[48:51]
	v_mfma_f32_16x16x32_bf16 v[36:39], v[210:213], v[234:237], v[36:39]
	v_mfma_f32_16x16x32_bf16 v[32:35], v[218:221], v[234:237], v[32:35]
	v_mfma_f32_16x16x32_bf16 v[20:23], v[210:213], v[242:245], v[20:23]
	v_mfma_f32_16x16x32_bf16 v[16:19], v[218:221], v[242:245], v[16:19]
	v_mfma_f32_16x16x32_bf16 v[4:7], v[210:213], v[250:253], v[4:7]
	v_mfma_f32_16x16x32_bf16 v[0:3], v[218:221], v[250:253], v[0:3]
	s_setprio 0
	s_barrier
	s_add_i32 s27, s27, 2
	s_add_u32 s50, s50, 0x100
	s_addc_u32 s51, s51, 0
	s_add_u32 s14, s14, 0x100
	s_addc_u32 s15, s15, 0
	s_cmp_gt_u32 s27, 29
	s_cbranch_scc0 .LBB0_2084
	s_and_b64 vcc, exec, s[24:25]
	s_cbranch_vccz .LBB0_2087
	s_barrier

.LBB0_2193:
	s_add_u32 s5, s48, 0xfffc0080
	s_addc_u32 s10, s49, -1
	s_add_i32 s31, 0, 0x10000
	s_cmp_eq_u32 s29, 12
	s_cselect_b32 s53, s45, s10
	s_cselect_b32 s52, s44, s5
	v_add_u32_e32 v144, s31, v146
	s_cselect_b32 s51, s47, s15
	s_cselect_b32 s50, s46, s14
	s_add_i32 s5, 0, 0x14000
	ds_read_b128 v[140:143], v144
	ds_read_b128 v[150:153], v144 offset:1024
	ds_read_b128 v[154:157], v144 offset:2048
	ds_read_b128 v[158:161], v144 offset:3072
	v_add_u32_e32 v144, s5, v146
	ds_read_b128 v[162:165], v144
	ds_read_b128 v[166:169], v144 offset:1024
	ds_read_b128 v[170:173], v144 offset:2048
	ds_read_b128 v[182:185], v144 offset:3072
	s_add_i32 m0, s59, 0xc000
	ds_read_b128 v[186:189], v149
	ds_read_b128 v[206:209], v149 offset:1024
	ds_read_b128 v[210:213], v149 offset:2048
	ds_read_b128 v[214:217], v149 offset:3072
	ds_read_b128 v[218:221], v149 offset:4096
	ds_read_b128 v[222:225], v149 offset:5120
	ds_read_b128 v[226:229], v149 offset:6144
	ds_read_b128 v[230:233], v149 offset:7168
	global_load_lds_dwordx4 v136, s[48:49]
	s_add_i32 m0, s59, 0xe000
	s_nop 0
	global_load_lds_dwordx4 v138, s[48:49]
	s_waitcnt vmcnt(8)
	s_waitcnt lgkmcnt(0)
	s_barrier
	s_setprio 1
	s_waitcnt lgkmcnt(0)
	v_mfma_f32_16x16x32_bf16 v[124:127], v[140:143], v[186:189], v[124:127]
	v_mfma_f32_16x16x32_bf16 v[120:123], v[154:157], v[186:189], v[120:123]
	v_mfma_f32_16x16x32_bf16 v[108:111], v[140:143], v[210:213], v[108:111]
	v_mfma_f32_16x16x32_bf16 v[104:107], v[154:157], v[210:213], v[104:107]
	v_mfma_f32_16x16x32_bf16 v[92:95], v[140:143], v[218:221], v[92:95]
	v_mfma_f32_16x16x32_bf16 v[88:91], v[154:157], v[218:221], v[88:91]
	v_mfma_f32_16x16x32_bf16 v[76:79], v[140:143], v[226:229], v[76:79]
	v_mfma_f32_16x16x32_bf16 v[72:75], v[154:157], v[226:229], v[72:75]
	v_mfma_f32_16x16x32_bf16 v[124:127], v[150:153], v[206:209], v[124:127]
	v_mfma_f32_16x16x32_bf16 v[120:123], v[158:161], v[206:209], v[120:123]
	v_mfma_f32_16x16x32_bf16 v[108:111], v[150:153], v[214:217], v[108:111]
	v_mfma_f32_16x16x32_bf16 v[104:107], v[158:161], v[214:217], v[104:107]
	v_mfma_f32_16x16x32_bf16 v[92:95], v[150:153], v[222:225], v[92:95]
	v_mfma_f32_16x16x32_bf16 v[88:91], v[158:161], v[222:225], v[88:91]
	v_mfma_f32_16x16x32_bf16 v[76:79], v[150:153], v[230:233], v[76:79]
	v_mfma_f32_16x16x32_bf16 v[72:75], v[158:161], v[230:233], v[72:75]
	s_setprio 0
	s_setprio 1
	v_mfma_f32_16x16x32_bf16 v[116:119], v[162:165], v[186:189], v[116:119]
	v_mfma_f32_16x16x32_bf16 v[112:115], v[170:173], v[186:189], v[112:115]
	v_mfma_f32_16x16x32_bf16 v[100:103], v[162:165], v[210:213], v[100:103]
	v_mfma_f32_16x16x32_bf16 v[96:99], v[170:173], v[210:213], v[96:99]
	v_mfma_f32_16x16x32_bf16 v[84:87], v[162:165], v[218:221], v[84:87]
	v_mfma_f32_16x16x32_bf16 v[80:83], v[170:173], v[218:221], v[80:83]
	v_mfma_f32_16x16x32_bf16 v[68:71], v[162:165], v[226:229], v[68:71]
	v_mfma_f32_16x16x32_bf16 v[64:67], v[170:173], v[226:229], v[64:67]
	v_mfma_f32_16x16x32_bf16 v[116:119], v[166:169], v[206:209], v[116:119]
	v_mfma_f32_16x16x32_bf16 v[112:115], v[182:185], v[206:209], v[112:115]
	v_mfma_f32_16x16x32_bf16 v[100:103], v[166:169], v[214:217], v[100:103]
	v_mfma_f32_16x16x32_bf16 v[96:99], v[182:185], v[214:217], v[96:99]
	v_mfma_f32_16x16x32_bf16 v[84:87], v[166:169], v[222:225], v[84:87]
	v_mfma_f32_16x16x32_bf16 v[80:83], v[182:185], v[222:225], v[80:83]
	v_mfma_f32_16x16x32_bf16 v[68:71], v[166:169], v[230:233], v[68:71]
	v_mfma_f32_16x16x32_bf16 v[64:67], v[182:185], v[230:233], v[64:67]
	s_setprio 0
	s_barrier
	s_add_i32 s10, s31, s58
	s_mov_b32 m0, s10
	ds_read_b128 v[186:189], v149 offset:16384
	ds_read_b128 v[206:209], v149 offset:17408
	ds_read_b128 v[210:213], v149 offset:18432
	ds_read_b128 v[214:217], v149 offset:19456
	ds_read_b128 v[218:221], v149 offset:20480
	ds_read_b128 v[222:225], v149 offset:21504
	ds_read_b128 v[226:229], v149 offset:22528
	ds_read_b128 v[230:233], v149 offset:23552
	global_load_lds_dwordx4 v176, s[50:51]
	s_add_i32 m0, s10, 0x2000
	s_add_u32 s74, s50, 0x40000
	s_addc_u32 s75, s51, 0
	s_add_i32 s5, s5, s58
	global_load_lds_dwordx4 v132, s[50:51]
	s_mov_b32 m0, s5
	s_nop 0
	global_load_lds_dwordx4 v176, s[74:75]
	s_add_i32 m0, s5, 0x2000
	s_nop 0
	global_load_lds_dwordx4 v132, s[74:75]
	s_mov_b32 m0, s59
	s_nop 0
	global_load_lds_dwordx4 v128, s[52:53]
	s_mov_b32 m0, s60
	s_nop 0
	global_load_lds_dwordx4 v130, s[52:53]
	s_waitcnt vmcnt(8)
	s_waitcnt lgkmcnt(0)
	s_barrier
	s_setprio 1
	s_waitcnt lgkmcnt(0)
	v_mfma_f32_16x16x32_bf16 v[60:63], v[140:143], v[186:189], v[60:63]
	v_mfma_f32_16x16x32_bf16 v[56:59], v[154:157], v[186:189], v[56:59]
	v_mfma_f32_16x16x32_bf16 v[44:47], v[140:143], v[210:213], v[44:47]
	v_mfma_f32_16x16x32_bf16 v[40:43], v[154:157], v[210:213], v[40:43]
	v_mfma_f32_16x16x32_bf16 v[28:31], v[140:143], v[218:221], v[28:31]
	v_mfma_f32_16x16x32_bf16 v[24:27], v[154:157], v[218:221], v[24:27]
	v_mfma_f32_16x16x32_bf16 v[12:15], v[140:143], v[226:229], v[12:15]
	v_mfma_f32_16x16x32_bf16 v[8:11], v[154:157], v[226:229], v[8:11]
	v_mfma_f32_16x16x32_bf16 v[60:63], v[150:153], v[206:209], v[60:63]
	v_mfma_f32_16x16x32_bf16 v[56:59], v[158:161], v[206:209], v[56:59]
	v_mfma_f32_16x16x32_bf16 v[44:47], v[150:153], v[214:217], v[44:47]
	v_mfma_f32_16x16x32_bf16 v[40:43], v[158:161], v[214:217], v[40:43]
	v_mfma_f32_16x16x32_bf16 v[28:31], v[150:153], v[222:225], v[28:31]
	v_mfma_f32_16x16x32_bf16 v[24:27], v[158:161], v[222:225], v[24:27]
	v_mfma_f32_16x16x32_bf16 v[12:15], v[150:153], v[230:233], v[12:15]
	v_mfma_f32_16x16x32_bf16 v[8:11], v[158:161], v[230:233], v[8:11]
	s_setprio 0
	s_setprio 1
	v_mfma_f32_16x16x32_bf16 v[52:55], v[162:165], v[186:189], v[52:55]
	v_mfma_f32_16x16x32_bf16 v[48:51], v[170:173], v[186:189], v[48:51]
	v_mfma_f32_16x16x32_bf16 v[36:39], v[162:165], v[210:213], v[36:39]
	v_mfma_f32_16x16x32_bf16 v[32:35], v[170:173], v[210:213], v[32:35]
	v_mfma_f32_16x16x32_bf16 v[20:23], v[162:165], v[218:221], v[20:23]
	v_mfma_f32_16x16x32_bf16 v[16:19], v[170:173], v[218:221], v[16:19]
	v_mfma_f32_16x16x32_bf16 v[4:7], v[162:165], v[226:229], v[4:7]
	v_mfma_f32_16x16x32_bf16 v[0:3], v[170:173], v[226:229], v[0:3]
	v_mfma_f32_16x16x32_bf16 v[52:55], v[166:169], v[206:209], v[52:55]
	v_mfma_f32_16x16x32_bf16 v[48:51], v[182:185], v[206:209], v[48:51]
	v_mfma_f32_16x16x32_bf16 v[36:39], v[166:169], v[214:217], v[36:39]
	v_mfma_f32_16x16x32_bf16 v[32:35], v[182:185], v[214:217], v[32:35]
	v_mfma_f32_16x16x32_bf16 v[20:23], v[166:169], v[222:225], v[20:23]
	v_mfma_f32_16x16x32_bf16 v[16:19], v[182:185], v[222:225], v[16:19]
	v_mfma_f32_16x16x32_bf16 v[4:7], v[166:169], v[230:233], v[4:7]
	v_mfma_f32_16x16x32_bf16 v[0:3], v[182:185], v[230:233], v[0:3]
	s_setprio 0
	s_barrier
	s_add_i32 s5, 0, 0x18000
	s_add_i32 s10, 0, 0x1c000
	v_add_u32_e32 v158, s5, v146
	v_add_u32_e32 v182, s10, v146
	ds_read_b128 v[140:143], v158
	ds_read_b128 v[150:153], v158 offset:1024
	ds_read_b128 v[154:157], v158 offset:2048
	ds_read_b128 v[158:161], v158 offset:3072
	ds_read_b128 v[162:165], v182
	ds_read_b128 v[166:169], v182 offset:1024
	ds_read_b128 v[170:173], v182 offset:2048
	ds_read_b128 v[182:185], v182 offset:3072
	s_add_u32 s52, s52, 0x40000
	s_addc_u32 s53, s53, 0
	s_mov_b32 m0, s61
	ds_read_b128 v[186:189], v149 offset:32768
	ds_read_b128 v[206:209], v149 offset:33792
	ds_read_b128 v[210:213], v149 offset:34816
	ds_read_b128 v[214:217], v149 offset:35840
	ds_read_b128 v[218:221], v149 offset:36864
	ds_read_b128 v[222:225], v149 offset:37888
	ds_read_b128 v[226:229], v149 offset:38912
	ds_read_b128 v[230:233], v149 offset:39936
	global_load_lds_dwordx4 v128, s[52:53]
	s_mov_b32 m0, s62
	s_nop 0
	global_load_lds_dwordx4 v130, s[52:53]
	s_waitcnt vmcnt(8)
	s_waitcnt lgkmcnt(0)
	s_barrier
	s_setprio 1
	s_waitcnt lgkmcnt(0)
	v_mfma_f32_16x16x32_bf16 v[124:127], v[140:143], v[186:189], v[124:127]
	v_mfma_f32_16x16x32_bf16 v[120:123], v[154:157], v[186:189], v[120:123]
	v_mfma_f32_16x16x32_bf16 v[108:111], v[140:143], v[210:213], v[108:111]
	v_mfma_f32_16x16x32_bf16 v[104:107], v[154:157], v[210:213], v[104:107]
	v_mfma_f32_16x16x32_bf16 v[92:95], v[140:143], v[218:221], v[92:95]
	v_mfma_f32_16x16x32_bf16 v[88:91], v[154:157], v[218:221], v[88:91]
	v_mfma_f32_16x16x32_bf16 v[76:79], v[140:143], v[226:229], v[76:79]
	v_mfma_f32_16x16x32_bf16 v[72:75], v[154:157], v[226:229], v[72:75]
	v_mfma_f32_16x16x32_bf16 v[124:127], v[150:153], v[206:209], v[124:127]
	v_mfma_f32_16x16x32_bf16 v[120:123], v[158:161], v[206:209], v[120:123]
	v_mfma_f32_16x16x32_bf16 v[108:111], v[150:153], v[214:217], v[108:111]
	v_mfma_f32_16x16x32_bf16 v[104:107], v[158:161], v[214:217], v[104:107]
	v_mfma_f32_16x16x32_bf16 v[92:95], v[150:153], v[222:225], v[92:95]
	v_mfma_f32_16x16x32_bf16 v[88:91], v[158:161], v[222:225], v[88:91]
	v_mfma_f32_16x16x32_bf16 v[76:79], v[150:153], v[230:233], v[76:79]
	v_mfma_f32_16x16x32_bf16 v[72:75], v[158:161], v[230:233], v[72:75]
	s_setprio 0
	s_setprio 1
	v_mfma_f32_16x16x32_bf16 v[116:119], v[162:165], v[186:189], v[116:119]
	v_mfma_f32_16x16x32_bf16 v[112:115], v[170:173], v[186:189], v[112:115]
	v_mfma_f32_16x16x32_bf16 v[100:103], v[162:165], v[210:213], v[100:103]
	v_mfma_f32_16x16x32_bf16 v[96:99], v[170:173], v[210:213], v[96:99]
	v_mfma_f32_16x16x32_bf16 v[84:87], v[162:165], v[218:221], v[84:87]
	v_mfma_f32_16x16x32_bf16 v[80:83], v[170:173], v[218:221], v[80:83]
	v_mfma_f32_16x16x32_bf16 v[68:71], v[162:165], v[226:229], v[68:71]
	v_mfma_f32_16x16x32_bf16 v[64:67], v[170:173], v[226:229], v[64:67]
	v_mfma_f32_16x16x32_bf16 v[116:119], v[166:169], v[206:209], v[116:119]
	v_mfma_f32_16x16x32_bf16 v[112:115], v[182:185], v[206:209], v[112:115]
	v_mfma_f32_16x16x32_bf16 v[100:103], v[166:169], v[214:217], v[100:103]
	v_mfma_f32_16x16x32_bf16 v[96:99], v[182:185], v[214:217], v[96:99]
	v_mfma_f32_16x16x32_bf16 v[84:87], v[166:169], v[222:225], v[84:87]
	v_mfma_f32_16x16x32_bf16 v[80:83], v[182:185], v[222:225], v[80:83]
	v_mfma_f32_16x16x32_bf16 v[68:71], v[166:169], v[230:233], v[68:71]
	v_mfma_f32_16x16x32_bf16 v[64:67], v[182:185], v[230:233], v[64:67]
	s_setprio 0
	s_barrier
	s_add_i32 s5, s5, s58
	s_mov_b32 m0, s5
	ds_read_b128 v[186:189], v149 offset:49152
	ds_read_b128 v[206:209], v149 offset:50176
	ds_read_b128 v[210:213], v149 offset:51200
	ds_read_b128 v[214:217], v149 offset:52224
	ds_read_b128 v[218:221], v149 offset:53248
	ds_read_b128 v[222:225], v149 offset:54272
	ds_read_b128 v[226:229], v149 offset:55296
	ds_read_b128 v[230:233], v149 offset:56320
	s_add_u32 s74, s50, 0x80
	s_addc_u32 s75, s51, 0
	global_load_lds_dwordx4 v176, s[74:75]
	s_add_i32 m0, s5, 0x2000
	s_add_u32 s50, s50, 0x40080
	s_addc_u32 s51, s51, 0
	s_add_i32 s5, s10, s58
	s_add_u32 s74, s50, 0xfffc0000
	s_addc_u32 s75, s51, -1
	global_load_lds_dwordx4 v132, s[74:75]
	s_mov_b32 m0, s5
	s_nop 0
	global_load_lds_dwordx4 v176, s[50:51]
	s_add_i32 m0, s5, 0x2000
	s_nop 0
	global_load_lds_dwordx4 v132, s[50:51]
	s_mov_b32 m0, s64
	s_nop 0
	s_add_u32 s74, s52, 0xfffc0080
	s_addc_u32 s75, s53, -1
	global_load_lds_dwordx4 v128, s[74:75]
	s_mov_b32 m0, s65
	s_nop 0
	s_add_u32 s74, s52, 0xfffc0080
	s_addc_u32 s75, s53, -1
	global_load_lds_dwordx4 v130, s[74:75]
	s_waitcnt vmcnt(8)
	s_waitcnt lgkmcnt(0)
	s_barrier
	s_setprio 1
	s_waitcnt lgkmcnt(0)
	v_mfma_f32_16x16x32_bf16 v[60:63], v[140:143], v[186:189], v[60:63]
	v_mfma_f32_16x16x32_bf16 v[56:59], v[154:157], v[186:189], v[56:59]
	v_mfma_f32_16x16x32_bf16 v[44:47], v[140:143], v[210:213], v[44:47]
	v_mfma_f32_16x16x32_bf16 v[40:43], v[154:157], v[210:213], v[40:43]
	v_mfma_f32_16x16x32_bf16 v[28:31], v[140:143], v[218:221], v[28:31]
	v_mfma_f32_16x16x32_bf16 v[24:27], v[154:157], v[218:221], v[24:27]
	v_mfma_f32_16x16x32_bf16 v[12:15], v[140:143], v[226:229], v[12:15]
	v_mfma_f32_16x16x32_bf16 v[8:11], v[154:157], v[226:229], v[8:11]
	v_mfma_f32_16x16x32_bf16 v[60:63], v[150:153], v[206:209], v[60:63]
	v_mfma_f32_16x16x32_bf16 v[56:59], v[158:161], v[206:209], v[56:59]
	v_mfma_f32_16x16x32_bf16 v[44:47], v[150:153], v[214:217], v[44:47]
	v_mfma_f32_16x16x32_bf16 v[40:43], v[158:161], v[214:217], v[40:43]
	v_mfma_f32_16x16x32_bf16 v[28:31], v[150:153], v[222:225], v[28:31]
	v_mfma_f32_16x16x32_bf16 v[24:27], v[158:161], v[222:225], v[24:27]
	v_mfma_f32_16x16x32_bf16 v[12:15], v[150:153], v[230:233], v[12:15]
	v_mfma_f32_16x16x32_bf16 v[8:11], v[158:161], v[230:233], v[8:11]
	s_setprio 0
	s_setprio 1
	v_mfma_f32_16x16x32_bf16 v[52:55], v[162:165], v[186:189], v[52:55]
	v_mfma_f32_16x16x32_bf16 v[48:51], v[170:173], v[186:189], v[48:51]
	v_mfma_f32_16x16x32_bf16 v[36:39], v[162:165], v[210:213], v[36:39]
	v_mfma_f32_16x16x32_bf16 v[32:35], v[170:173], v[210:213], v[32:35]
	v_mfma_f32_16x16x32_bf16 v[20:23], v[162:165], v[218:221], v[20:23]
	v_mfma_f32_16x16x32_bf16 v[16:19], v[170:173], v[218:221], v[16:19]
	v_mfma_f32_16x16x32_bf16 v[4:7], v[162:165], v[226:229], v[4:7]
	v_mfma_f32_16x16x32_bf16 v[0:3], v[170:173], v[226:229], v[0:3]
	v_mfma_f32_16x16x32_bf16 v[52:55], v[166:169], v[206:209], v[52:55]
	v_mfma_f32_16x16x32_bf16 v[48:51], v[182:185], v[206:209], v[48:51]
	v_mfma_f32_16x16x32_bf16 v[36:39], v[166:169], v[214:217], v[36:39]
	v_mfma_f32_16x16x32_bf16 v[32:35], v[182:185], v[214:217], v[32:35]
	v_mfma_f32_16x16x32_bf16 v[20:23], v[166:169], v[222:225], v[20:23]
	v_mfma_f32_16x16x32_bf16 v[16:19], v[182:185], v[222:225], v[16:19]
	v_mfma_f32_16x16x32_bf16 v[4:7], v[166:169], v[230:233], v[4:7]
	v_mfma_f32_16x16x32_bf16 v[0:3], v[182:185], v[230:233], v[0:3]
	s_setprio 0
	s_barrier
	s_add_i32 s29, s29, 2
	s_add_u32 s48, s48, 0x100
	s_addc_u32 s49, s49, 0
	s_add_u32 s14, s14, 0x100
	s_addc_u32 s15, s15, 0
	s_cmp_gt_u32 s29, 13
	s_cbranch_scc0 .LBB0_2193
	s_and_b64 vcc, exec, s[26:27]
	s_cbranch_vccz .LBB0_2196
	s_barrier

.LBB0_2282:
	s_add_u32 s5, s46, 0xfff80080
	s_addc_u32 s10, s47, -1
	s_add_i32 s29, 0, 0x10000
	s_cmp_eq_u32 s27, 28
	s_cselect_b32 s51, s43, s10
	s_cselect_b32 s50, s42, s5
	v_add_u32_e32 v169, s29, v155
	s_cselect_b32 s49, s45, s15
	s_cselect_b32 s48, s44, s14
	s_add_i32 s5, 0, 0x14000
	ds_read_b128 v[142:145], v169
	ds_read_b128 v[146:149], v169 offset:1024
	ds_read_b128 v[150:153], v169 offset:2048
	ds_read_b128 v[170:173], v169 offset:3072
	v_add_u32_e32 v169, s5, v155
	ds_read_b128 v[182:185], v169
	ds_read_b128 v[186:189], v169 offset:1024
	ds_read_b128 v[206:209], v169 offset:2048
	ds_read_b128 v[210:213], v169 offset:3072
	s_add_i32 m0, s57, 0xc000
	ds_read_b128 v[214:217], v168
	ds_read_b128 v[218:221], v168 offset:1024
	ds_read_b128 v[222:225], v168 offset:2048
	ds_read_b128 v[226:229], v168 offset:3072
	ds_read_b128 v[230:233], v168 offset:4096
	ds_read_b128 v[234:237], v168 offset:5120
	ds_read_b128 v[238:241], v168 offset:6144
	ds_read_b128 v[242:245], v168 offset:7168
	global_load_lds_dwordx4 v138, s[46:47]
	s_add_i32 m0, s57, 0xe000
	s_nop 0
	global_load_lds_dwordx4 v140, s[46:47]
	s_waitcnt vmcnt(8)
	s_waitcnt lgkmcnt(0)
	s_barrier
	s_setprio 1
	s_waitcnt lgkmcnt(0)
	v_mfma_f32_16x16x32_bf16 v[124:127], v[142:145], v[214:217], v[124:127]
	v_mfma_f32_16x16x32_bf16 v[120:123], v[150:153], v[214:217], v[120:123]
	v_mfma_f32_16x16x32_bf16 v[108:111], v[142:145], v[222:225], v[108:111]
	v_mfma_f32_16x16x32_bf16 v[104:107], v[150:153], v[222:225], v[104:107]
	v_mfma_f32_16x16x32_bf16 v[92:95], v[142:145], v[230:233], v[92:95]
	v_mfma_f32_16x16x32_bf16 v[88:91], v[150:153], v[230:233], v[88:91]
	v_mfma_f32_16x16x32_bf16 v[76:79], v[142:145], v[238:241], v[76:79]
	v_mfma_f32_16x16x32_bf16 v[72:75], v[150:153], v[238:241], v[72:75]
	v_mfma_f32_16x16x32_bf16 v[124:127], v[146:149], v[218:221], v[124:127]
	v_mfma_f32_16x16x32_bf16 v[120:123], v[170:173], v[218:221], v[120:123]
	v_mfma_f32_16x16x32_bf16 v[108:111], v[146:149], v[226:229], v[108:111]
	v_mfma_f32_16x16x32_bf16 v[104:107], v[170:173], v[226:229], v[104:107]
	v_mfma_f32_16x16x32_bf16 v[92:95], v[146:149], v[234:237], v[92:95]
	v_mfma_f32_16x16x32_bf16 v[88:91], v[170:173], v[234:237], v[88:91]
	v_mfma_f32_16x16x32_bf16 v[76:79], v[146:149], v[242:245], v[76:79]
	v_mfma_f32_16x16x32_bf16 v[72:75], v[170:173], v[242:245], v[72:75]
	s_setprio 0
	s_setprio 1
	v_mfma_f32_16x16x32_bf16 v[116:119], v[182:185], v[214:217], v[116:119]
	v_mfma_f32_16x16x32_bf16 v[112:115], v[206:209], v[214:217], v[112:115]
	v_mfma_f32_16x16x32_bf16 v[100:103], v[182:185], v[222:225], v[100:103]
	v_mfma_f32_16x16x32_bf16 v[96:99], v[206:209], v[222:225], v[96:99]
	v_mfma_f32_16x16x32_bf16 v[84:87], v[182:185], v[230:233], v[84:87]
	v_mfma_f32_16x16x32_bf16 v[80:83], v[206:209], v[230:233], v[80:83]
	v_mfma_f32_16x16x32_bf16 v[68:71], v[182:185], v[238:241], v[68:71]
	v_mfma_f32_16x16x32_bf16 v[64:67], v[206:209], v[238:241], v[64:67]
	v_mfma_f32_16x16x32_bf16 v[116:119], v[186:189], v[218:221], v[116:119]
	v_mfma_f32_16x16x32_bf16 v[112:115], v[210:213], v[218:221], v[112:115]
	v_mfma_f32_16x16x32_bf16 v[100:103], v[186:189], v[226:229], v[100:103]
	v_mfma_f32_16x16x32_bf16 v[96:99], v[210:213], v[226:229], v[96:99]
	v_mfma_f32_16x16x32_bf16 v[84:87], v[186:189], v[234:237], v[84:87]
	v_mfma_f32_16x16x32_bf16 v[80:83], v[210:213], v[234:237], v[80:83]
	v_mfma_f32_16x16x32_bf16 v[68:71], v[186:189], v[242:245], v[68:71]
	v_mfma_f32_16x16x32_bf16 v[64:67], v[210:213], v[242:245], v[64:67]
	s_setprio 0
	s_barrier
	s_add_i32 s10, s29, s56
	s_mov_b32 m0, s10
	ds_read_b128 v[214:217], v168 offset:16384
	ds_read_b128 v[218:221], v168 offset:17408
	ds_read_b128 v[222:225], v168 offset:18432
	ds_read_b128 v[226:229], v168 offset:19456
	ds_read_b128 v[230:233], v168 offset:20480
	ds_read_b128 v[234:237], v168 offset:21504
	ds_read_b128 v[238:241], v168 offset:22528
	ds_read_b128 v[242:245], v168 offset:23552
	global_load_lds_dwordx4 v130, s[48:49]
	s_add_i32 m0, s10, 0x2000
	s_add_u32 s64, s48, 0x80000
	s_addc_u32 s65, s49, 0
	s_add_i32 s5, s5, s56
	global_load_lds_dwordx4 v134, s[48:49]
	s_mov_b32 m0, s5
	s_nop 0
	global_load_lds_dwordx4 v130, s[64:65]
	s_add_i32 m0, s5, 0x2000
	s_nop 0
	global_load_lds_dwordx4 v134, s[64:65]
	s_mov_b32 m0, s57
	s_nop 0
	global_load_lds_dwordx4 v128, s[50:51]
	s_mov_b32 m0, s58
	s_nop 0
	global_load_lds_dwordx4 v132, s[50:51]
	s_waitcnt vmcnt(8)
	s_waitcnt lgkmcnt(0)
	s_barrier
	s_setprio 1
	s_waitcnt lgkmcnt(0)
	v_mfma_f32_16x16x32_bf16 v[60:63], v[142:145], v[214:217], v[60:63]
	v_mfma_f32_16x16x32_bf16 v[56:59], v[150:153], v[214:217], v[56:59]
	v_mfma_f32_16x16x32_bf16 v[44:47], v[142:145], v[222:225], v[44:47]
	v_mfma_f32_16x16x32_bf16 v[40:43], v[150:153], v[222:225], v[40:43]
	v_mfma_f32_16x16x32_bf16 v[28:31], v[142:145], v[230:233], v[28:31]
	v_mfma_f32_16x16x32_bf16 v[24:27], v[150:153], v[230:233], v[24:27]
	v_mfma_f32_16x16x32_bf16 v[12:15], v[142:145], v[238:241], v[12:15]
	v_mfma_f32_16x16x32_bf16 v[8:11], v[150:153], v[238:241], v[8:11]
	v_mfma_f32_16x16x32_bf16 v[60:63], v[146:149], v[218:221], v[60:63]
	v_mfma_f32_16x16x32_bf16 v[56:59], v[170:173], v[218:221], v[56:59]
	v_mfma_f32_16x16x32_bf16 v[44:47], v[146:149], v[226:229], v[44:47]
	v_mfma_f32_16x16x32_bf16 v[40:43], v[170:173], v[226:229], v[40:43]
	v_mfma_f32_16x16x32_bf16 v[28:31], v[146:149], v[234:237], v[28:31]
	v_mfma_f32_16x16x32_bf16 v[24:27], v[170:173], v[234:237], v[24:27]
	v_mfma_f32_16x16x32_bf16 v[12:15], v[146:149], v[242:245], v[12:15]
	v_mfma_f32_16x16x32_bf16 v[8:11], v[170:173], v[242:245], v[8:11]
	s_setprio 0
	s_setprio 1
	v_mfma_f32_16x16x32_bf16 v[52:55], v[182:185], v[214:217], v[52:55]
	v_mfma_f32_16x16x32_bf16 v[48:51], v[206:209], v[214:217], v[48:51]
	v_mfma_f32_16x16x32_bf16 v[36:39], v[182:185], v[222:225], v[36:39]
	v_mfma_f32_16x16x32_bf16 v[32:35], v[206:209], v[222:225], v[32:35]
	v_mfma_f32_16x16x32_bf16 v[20:23], v[182:185], v[230:233], v[20:23]
	v_mfma_f32_16x16x32_bf16 v[16:19], v[206:209], v[230:233], v[16:19]
	v_mfma_f32_16x16x32_bf16 v[4:7], v[182:185], v[238:241], v[4:7]
	v_mfma_f32_16x16x32_bf16 v[0:3], v[206:209], v[238:241], v[0:3]
	v_mfma_f32_16x16x32_bf16 v[52:55], v[186:189], v[218:221], v[52:55]
	v_mfma_f32_16x16x32_bf16 v[48:51], v[210:213], v[218:221], v[48:51]
	v_mfma_f32_16x16x32_bf16 v[36:39], v[186:189], v[226:229], v[36:39]
	v_mfma_f32_16x16x32_bf16 v[32:35], v[210:213], v[226:229], v[32:35]
	v_mfma_f32_16x16x32_bf16 v[20:23], v[186:189], v[234:237], v[20:23]
	v_mfma_f32_16x16x32_bf16 v[16:19], v[210:213], v[234:237], v[16:19]
	v_mfma_f32_16x16x32_bf16 v[4:7], v[186:189], v[242:245], v[4:7]
	v_mfma_f32_16x16x32_bf16 v[0:3], v[210:213], v[242:245], v[0:3]
	s_setprio 0
	s_barrier
	s_add_i32 s5, 0, 0x18000
	v_add_u32_e32 v169, s5, v155
	s_add_i32 s10, 0, 0x1c000
	ds_read_b128 v[142:145], v169
	ds_read_b128 v[146:149], v169 offset:1024
	ds_read_b128 v[150:153], v169 offset:2048
	ds_read_b128 v[170:173], v169 offset:3072
	v_add_u32_e32 v169, s10, v155
	ds_read_b128 v[182:185], v169
	ds_read_b128 v[186:189], v169 offset:1024
	ds_read_b128 v[206:209], v169 offset:2048
	ds_read_b128 v[210:213], v169 offset:3072
	s_add_u32 s50, s50, 0x80000
	s_addc_u32 s51, s51, 0
	s_mov_b32 m0, s59
	ds_read_b128 v[214:217], v168 offset:32768
	ds_read_b128 v[218:221], v168 offset:33792
	ds_read_b128 v[222:225], v168 offset:34816
	ds_read_b128 v[226:229], v168 offset:35840
	ds_read_b128 v[230:233], v168 offset:36864
	ds_read_b128 v[234:237], v168 offset:37888
	ds_read_b128 v[238:241], v168 offset:38912
	ds_read_b128 v[242:245], v168 offset:39936
	global_load_lds_dwordx4 v128, s[50:51]
	s_mov_b32 m0, s60
	s_nop 0
	global_load_lds_dwordx4 v132, s[50:51]
	s_waitcnt vmcnt(8)
	s_waitcnt lgkmcnt(0)
	s_barrier
	s_setprio 1
	s_waitcnt lgkmcnt(0)
	v_mfma_f32_16x16x32_bf16 v[124:127], v[142:145], v[214:217], v[124:127]
	v_mfma_f32_16x16x32_bf16 v[120:123], v[150:153], v[214:217], v[120:123]
	v_mfma_f32_16x16x32_bf16 v[108:111], v[142:145], v[222:225], v[108:111]
	v_mfma_f32_16x16x32_bf16 v[104:107], v[150:153], v[222:225], v[104:107]
	v_mfma_f32_16x16x32_bf16 v[92:95], v[142:145], v[230:233], v[92:95]
	v_mfma_f32_16x16x32_bf16 v[88:91], v[150:153], v[230:233], v[88:91]
	v_mfma_f32_16x16x32_bf16 v[76:79], v[142:145], v[238:241], v[76:79]
	v_mfma_f32_16x16x32_bf16 v[72:75], v[150:153], v[238:241], v[72:75]
	v_mfma_f32_16x16x32_bf16 v[124:127], v[146:149], v[218:221], v[124:127]
	v_mfma_f32_16x16x32_bf16 v[120:123], v[170:173], v[218:221], v[120:123]
	v_mfma_f32_16x16x32_bf16 v[108:111], v[146:149], v[226:229], v[108:111]
	v_mfma_f32_16x16x32_bf16 v[104:107], v[170:173], v[226:229], v[104:107]
	v_mfma_f32_16x16x32_bf16 v[92:95], v[146:149], v[234:237], v[92:95]
	v_mfma_f32_16x16x32_bf16 v[88:91], v[170:173], v[234:237], v[88:91]
	v_mfma_f32_16x16x32_bf16 v[76:79], v[146:149], v[242:245], v[76:79]
	v_mfma_f32_16x16x32_bf16 v[72:75], v[170:173], v[242:245], v[72:75]
	s_setprio 0
	s_setprio 1
	v_mfma_f32_16x16x32_bf16 v[116:119], v[182:185], v[214:217], v[116:119]
	v_mfma_f32_16x16x32_bf16 v[112:115], v[206:209], v[214:217], v[112:115]
	v_mfma_f32_16x16x32_bf16 v[100:103], v[182:185], v[222:225], v[100:103]
	v_mfma_f32_16x16x32_bf16 v[96:99], v[206:209], v[222:225], v[96:99]
	v_mfma_f32_16x16x32_bf16 v[84:87], v[182:185], v[230:233], v[84:87]
	v_mfma_f32_16x16x32_bf16 v[80:83], v[206:209], v[230:233], v[80:83]
	v_mfma_f32_16x16x32_bf16 v[68:71], v[182:185], v[238:241], v[68:71]
	v_mfma_f32_16x16x32_bf16 v[64:67], v[206:209], v[238:241], v[64:67]
	v_mfma_f32_16x16x32_bf16 v[116:119], v[186:189], v[218:221], v[116:119]
	v_mfma_f32_16x16x32_bf16 v[112:115], v[210:213], v[218:221], v[112:115]
	v_mfma_f32_16x16x32_bf16 v[100:103], v[186:189], v[226:229], v[100:103]
	v_mfma_f32_16x16x32_bf16 v[96:99], v[210:213], v[226:229], v[96:99]
	v_mfma_f32_16x16x32_bf16 v[84:87], v[186:189], v[234:237], v[84:87]
	v_mfma_f32_16x16x32_bf16 v[80:83], v[210:213], v[234:237], v[80:83]
	v_mfma_f32_16x16x32_bf16 v[68:71], v[186:189], v[242:245], v[68:71]
	v_mfma_f32_16x16x32_bf16 v[64:67], v[210:213], v[242:245], v[64:67]
	s_setprio 0
	s_barrier
	s_add_i32 s5, s5, s56
	s_mov_b32 m0, s5
	ds_read_b128 v[214:217], v168 offset:49152
	ds_read_b128 v[218:221], v168 offset:50176
	ds_read_b128 v[222:225], v168 offset:51200
	ds_read_b128 v[226:229], v168 offset:52224
	ds_read_b128 v[230:233], v168 offset:53248
	ds_read_b128 v[234:237], v168 offset:54272
	ds_read_b128 v[238:241], v168 offset:55296
	ds_read_b128 v[242:245], v168 offset:56320
	s_add_u32 s64, s48, 0x80
	s_addc_u32 s65, s49, 0
	global_load_lds_dwordx4 v130, s[64:65]
	s_add_i32 m0, s5, 0x2000
	s_add_u32 s48, s48, 0x80080
	s_addc_u32 s49, s49, 0
	s_add_i32 s5, s10, s56
	s_add_u32 s64, s48, 0xfff80000
	s_addc_u32 s65, s49, -1
	global_load_lds_dwordx4 v134, s[64:65]
	s_mov_b32 m0, s5
	s_nop 0
	global_load_lds_dwordx4 v130, s[48:49]
	s_add_i32 m0, s5, 0x2000
	s_nop 0
	global_load_lds_dwordx4 v134, s[48:49]
	s_mov_b32 m0, s61
	s_nop 0
	s_add_u32 s64, s50, 0xfff80080
	s_addc_u32 s65, s51, -1
	global_load_lds_dwordx4 v128, s[64:65]
	s_mov_b32 m0, s62
	s_nop 0
	s_add_u32 s64, s50, 0xfff80080
	s_addc_u32 s65, s51, -1
	global_load_lds_dwordx4 v132, s[64:65]
	s_waitcnt vmcnt(8)
	s_waitcnt lgkmcnt(0)
	s_barrier
	s_setprio 1
	s_waitcnt lgkmcnt(0)
	v_mfma_f32_16x16x32_bf16 v[60:63], v[142:145], v[214:217], v[60:63]
	v_mfma_f32_16x16x32_bf16 v[56:59], v[150:153], v[214:217], v[56:59]
	v_mfma_f32_16x16x32_bf16 v[44:47], v[142:145], v[222:225], v[44:47]
	v_mfma_f32_16x16x32_bf16 v[40:43], v[150:153], v[222:225], v[40:43]
	v_mfma_f32_16x16x32_bf16 v[28:31], v[142:145], v[230:233], v[28:31]
	v_mfma_f32_16x16x32_bf16 v[24:27], v[150:153], v[230:233], v[24:27]
	v_mfma_f32_16x16x32_bf16 v[12:15], v[142:145], v[238:241], v[12:15]
	v_mfma_f32_16x16x32_bf16 v[8:11], v[150:153], v[238:241], v[8:11]
	v_mfma_f32_16x16x32_bf16 v[60:63], v[146:149], v[218:221], v[60:63]
	v_mfma_f32_16x16x32_bf16 v[56:59], v[170:173], v[218:221], v[56:59]
	v_mfma_f32_16x16x32_bf16 v[44:47], v[146:149], v[226:229], v[44:47]
	v_mfma_f32_16x16x32_bf16 v[40:43], v[170:173], v[226:229], v[40:43]
	v_mfma_f32_16x16x32_bf16 v[28:31], v[146:149], v[234:237], v[28:31]
	v_mfma_f32_16x16x32_bf16 v[24:27], v[170:173], v[234:237], v[24:27]
	v_mfma_f32_16x16x32_bf16 v[12:15], v[146:149], v[242:245], v[12:15]
	v_mfma_f32_16x16x32_bf16 v[8:11], v[170:173], v[242:245], v[8:11]
	s_setprio 0
	s_setprio 1
	v_mfma_f32_16x16x32_bf16 v[52:55], v[182:185], v[214:217], v[52:55]
	v_mfma_f32_16x16x32_bf16 v[48:51], v[206:209], v[214:217], v[48:51]
	v_mfma_f32_16x16x32_bf16 v[36:39], v[182:185], v[222:225], v[36:39]
	v_mfma_f32_16x16x32_bf16 v[32:35], v[206:209], v[222:225], v[32:35]
	v_mfma_f32_16x16x32_bf16 v[20:23], v[182:185], v[230:233], v[20:23]
	v_mfma_f32_16x16x32_bf16 v[16:19], v[206:209], v[230:233], v[16:19]
	v_mfma_f32_16x16x32_bf16 v[4:7], v[182:185], v[238:241], v[4:7]
	v_mfma_f32_16x16x32_bf16 v[0:3], v[206:209], v[238:241], v[0:3]
	v_mfma_f32_16x16x32_bf16 v[52:55], v[186:189], v[218:221], v[52:55]
	v_mfma_f32_16x16x32_bf16 v[48:51], v[210:213], v[218:221], v[48:51]
	v_mfma_f32_16x16x32_bf16 v[36:39], v[186:189], v[226:229], v[36:39]
	v_mfma_f32_16x16x32_bf16 v[32:35], v[210:213], v[226:229], v[32:35]
	v_mfma_f32_16x16x32_bf16 v[20:23], v[186:189], v[234:237], v[20:23]
	v_mfma_f32_16x16x32_bf16 v[16:19], v[210:213], v[234:237], v[16:19]
	v_mfma_f32_16x16x32_bf16 v[4:7], v[186:189], v[242:245], v[4:7]
	v_mfma_f32_16x16x32_bf16 v[0:3], v[210:213], v[242:245], v[0:3]
	s_setprio 0
	s_barrier
	s_add_i32 s27, s27, 2
	s_add_u32 s46, s46, 0x100
	s_addc_u32 s47, s47, 0
	s_add_u32 s14, s14, 0x100
	s_addc_u32 s15, s15, 0
	s_cmp_gt_u32 s27, 29
	s_cbranch_scc0 .LBB0_2282
	s_and_b64 vcc, exec, s[24:25]
	s_cbranch_vccz .LBB0_2285
	s_barrier

.LBB0_2357:
	s_add_u32 s5, s48, 0xffe00080
	s_addc_u32 s10, s49, -1
	s_add_i32 s31, 0, 0x10000
	s_cmpk_eq_i32 s29, 0x7c
	s_cselect_b32 s53, s45, s10
	s_cselect_b32 s52, s44, s5
	v_add_u32_e32 v144, s31, v146
	s_cselect_b32 s51, s47, s15
	s_cselect_b32 s50, s46, s14
	s_add_i32 s5, 0, 0x14000
	ds_read_b128 v[140:143], v144
	ds_read_b128 v[150:153], v144 offset:1024
	ds_read_b128 v[154:157], v144 offset:2048
	ds_read_b128 v[158:161], v144 offset:3072
	v_add_u32_e32 v144, s5, v146
	ds_read_b128 v[162:165], v144
	ds_read_b128 v[166:169], v144 offset:1024
	ds_read_b128 v[170:173], v144 offset:2048
	ds_read_b128 v[182:185], v144 offset:3072
	s_add_i32 m0, s59, 0xc000
	ds_read_b128 v[186:189], v149
	ds_read_b128 v[206:209], v149 offset:1024
	ds_read_b128 v[210:213], v149 offset:2048
	ds_read_b128 v[214:217], v149 offset:3072
	ds_read_b128 v[218:221], v149 offset:4096
	ds_read_b128 v[222:225], v149 offset:5120
	ds_read_b128 v[226:229], v149 offset:6144
	ds_read_b128 v[230:233], v149 offset:7168
	global_load_lds_dwordx4 v136, s[48:49]
	s_add_i32 m0, s59, 0xe000
	s_nop 0
	global_load_lds_dwordx4 v138, s[48:49]
	s_waitcnt vmcnt(8)
	s_waitcnt lgkmcnt(0)
	s_barrier
	s_setprio 1
	s_waitcnt lgkmcnt(0)
	v_mfma_f32_16x16x32_bf16 v[124:127], v[140:143], v[186:189], v[124:127]
	v_mfma_f32_16x16x32_bf16 v[120:123], v[154:157], v[186:189], v[120:123]
	v_mfma_f32_16x16x32_bf16 v[108:111], v[140:143], v[210:213], v[108:111]
	v_mfma_f32_16x16x32_bf16 v[104:107], v[154:157], v[210:213], v[104:107]
	v_mfma_f32_16x16x32_bf16 v[92:95], v[140:143], v[218:221], v[92:95]
	v_mfma_f32_16x16x32_bf16 v[88:91], v[154:157], v[218:221], v[88:91]
	v_mfma_f32_16x16x32_bf16 v[76:79], v[140:143], v[226:229], v[76:79]
	v_mfma_f32_16x16x32_bf16 v[72:75], v[154:157], v[226:229], v[72:75]
	v_mfma_f32_16x16x32_bf16 v[124:127], v[150:153], v[206:209], v[124:127]
	v_mfma_f32_16x16x32_bf16 v[120:123], v[158:161], v[206:209], v[120:123]
	v_mfma_f32_16x16x32_bf16 v[108:111], v[150:153], v[214:217], v[108:111]
	v_mfma_f32_16x16x32_bf16 v[104:107], v[158:161], v[214:217], v[104:107]
	v_mfma_f32_16x16x32_bf16 v[92:95], v[150:153], v[222:225], v[92:95]
	v_mfma_f32_16x16x32_bf16 v[88:91], v[158:161], v[222:225], v[88:91]
	v_mfma_f32_16x16x32_bf16 v[76:79], v[150:153], v[230:233], v[76:79]
	v_mfma_f32_16x16x32_bf16 v[72:75], v[158:161], v[230:233], v[72:75]
	s_setprio 0
	s_setprio 1
	v_mfma_f32_16x16x32_bf16 v[116:119], v[162:165], v[186:189], v[116:119]
	v_mfma_f32_16x16x32_bf16 v[112:115], v[170:173], v[186:189], v[112:115]
	v_mfma_f32_16x16x32_bf16 v[100:103], v[162:165], v[210:213], v[100:103]
	v_mfma_f32_16x16x32_bf16 v[96:99], v[170:173], v[210:213], v[96:99]
	v_mfma_f32_16x16x32_bf16 v[84:87], v[162:165], v[218:221], v[84:87]
	v_mfma_f32_16x16x32_bf16 v[80:83], v[170:173], v[218:221], v[80:83]
	v_mfma_f32_16x16x32_bf16 v[68:71], v[162:165], v[226:229], v[68:71]
	v_mfma_f32_16x16x32_bf16 v[64:67], v[170:173], v[226:229], v[64:67]
	v_mfma_f32_16x16x32_bf16 v[116:119], v[166:169], v[206:209], v[116:119]
	v_mfma_f32_16x16x32_bf16 v[112:115], v[182:185], v[206:209], v[112:115]
	v_mfma_f32_16x16x32_bf16 v[100:103], v[166:169], v[214:217], v[100:103]
	v_mfma_f32_16x16x32_bf16 v[96:99], v[182:185], v[214:217], v[96:99]
	v_mfma_f32_16x16x32_bf16 v[84:87], v[166:169], v[222:225], v[84:87]
	v_mfma_f32_16x16x32_bf16 v[80:83], v[182:185], v[222:225], v[80:83]
	v_mfma_f32_16x16x32_bf16 v[68:71], v[166:169], v[230:233], v[68:71]
	v_mfma_f32_16x16x32_bf16 v[64:67], v[182:185], v[230:233], v[64:67]
	s_setprio 0
	s_barrier
	s_add_i32 s10, s31, s58
	s_mov_b32 m0, s10
	ds_read_b128 v[186:189], v149 offset:16384
	ds_read_b128 v[206:209], v149 offset:17408
	ds_read_b128 v[210:213], v149 offset:18432
	ds_read_b128 v[214:217], v149 offset:19456
	ds_read_b128 v[218:221], v149 offset:20480
	ds_read_b128 v[222:225], v149 offset:21504
	ds_read_b128 v[226:229], v149 offset:22528
	ds_read_b128 v[230:233], v149 offset:23552
	global_load_lds_dwordx4 v176, s[50:51]
	s_add_i32 m0, s10, 0x2000
	s_add_u32 s74, s50, 0x200000
	s_addc_u32 s75, s51, 0
	s_add_i32 s5, s5, s58
	global_load_lds_dwordx4 v132, s[50:51]
	s_mov_b32 m0, s5
	s_nop 0
	global_load_lds_dwordx4 v176, s[74:75]
	s_add_i32 m0, s5, 0x2000
	s_nop 0
	global_load_lds_dwordx4 v132, s[74:75]
	s_mov_b32 m0, s59
	s_nop 0
	global_load_lds_dwordx4 v128, s[52:53]
	s_mov_b32 m0, s60
	s_nop 0
	global_load_lds_dwordx4 v130, s[52:53]
	s_waitcnt vmcnt(8)
	s_waitcnt lgkmcnt(0)
	s_barrier
	s_setprio 1
	s_waitcnt lgkmcnt(0)
	v_mfma_f32_16x16x32_bf16 v[60:63], v[140:143], v[186:189], v[60:63]
	v_mfma_f32_16x16x32_bf16 v[56:59], v[154:157], v[186:189], v[56:59]
	v_mfma_f32_16x16x32_bf16 v[44:47], v[140:143], v[210:213], v[44:47]
	v_mfma_f32_16x16x32_bf16 v[40:43], v[154:157], v[210:213], v[40:43]
	v_mfma_f32_16x16x32_bf16 v[28:31], v[140:143], v[218:221], v[28:31]
	v_mfma_f32_16x16x32_bf16 v[24:27], v[154:157], v[218:221], v[24:27]
	v_mfma_f32_16x16x32_bf16 v[12:15], v[140:143], v[226:229], v[12:15]
	v_mfma_f32_16x16x32_bf16 v[8:11], v[154:157], v[226:229], v[8:11]
	v_mfma_f32_16x16x32_bf16 v[60:63], v[150:153], v[206:209], v[60:63]
	v_mfma_f32_16x16x32_bf16 v[56:59], v[158:161], v[206:209], v[56:59]
	v_mfma_f32_16x16x32_bf16 v[44:47], v[150:153], v[214:217], v[44:47]
	v_mfma_f32_16x16x32_bf16 v[40:43], v[158:161], v[214:217], v[40:43]
	v_mfma_f32_16x16x32_bf16 v[28:31], v[150:153], v[222:225], v[28:31]
	v_mfma_f32_16x16x32_bf16 v[24:27], v[158:161], v[222:225], v[24:27]
	v_mfma_f32_16x16x32_bf16 v[12:15], v[150:153], v[230:233], v[12:15]
	v_mfma_f32_16x16x32_bf16 v[8:11], v[158:161], v[230:233], v[8:11]
	s_setprio 0
	s_setprio 1
	v_mfma_f32_16x16x32_bf16 v[52:55], v[162:165], v[186:189], v[52:55]
	v_mfma_f32_16x16x32_bf16 v[48:51], v[170:173], v[186:189], v[48:51]
	v_mfma_f32_16x16x32_bf16 v[36:39], v[162:165], v[210:213], v[36:39]
	v_mfma_f32_16x16x32_bf16 v[32:35], v[170:173], v[210:213], v[32:35]
	v_mfma_f32_16x16x32_bf16 v[20:23], v[162:165], v[218:221], v[20:23]
	v_mfma_f32_16x16x32_bf16 v[16:19], v[170:173], v[218:221], v[16:19]
	v_mfma_f32_16x16x32_bf16 v[4:7], v[162:165], v[226:229], v[4:7]
	v_mfma_f32_16x16x32_bf16 v[0:3], v[170:173], v[226:229], v[0:3]
	v_mfma_f32_16x16x32_bf16 v[52:55], v[166:169], v[206:209], v[52:55]
	v_mfma_f32_16x16x32_bf16 v[48:51], v[182:185], v[206:209], v[48:51]
	v_mfma_f32_16x16x32_bf16 v[36:39], v[166:169], v[214:217], v[36:39]
	v_mfma_f32_16x16x32_bf16 v[32:35], v[182:185], v[214:217], v[32:35]
	v_mfma_f32_16x16x32_bf16 v[20:23], v[166:169], v[222:225], v[20:23]
	v_mfma_f32_16x16x32_bf16 v[16:19], v[182:185], v[222:225], v[16:19]
	v_mfma_f32_16x16x32_bf16 v[4:7], v[166:169], v[230:233], v[4:7]
	v_mfma_f32_16x16x32_bf16 v[0:3], v[182:185], v[230:233], v[0:3]
	s_setprio 0
	s_barrier
	s_add_i32 s5, 0, 0x18000
	s_add_i32 s10, 0, 0x1c000
	v_add_u32_e32 v158, s5, v146
	v_add_u32_e32 v182, s10, v146
	ds_read_b128 v[140:143], v158
	ds_read_b128 v[150:153], v158 offset:1024
	ds_read_b128 v[154:157], v158 offset:2048
	ds_read_b128 v[158:161], v158 offset:3072
	ds_read_b128 v[162:165], v182
	ds_read_b128 v[166:169], v182 offset:1024
	ds_read_b128 v[170:173], v182 offset:2048
	ds_read_b128 v[182:185], v182 offset:3072
	s_add_u32 s52, s52, 0x200000
	s_addc_u32 s53, s53, 0
	s_mov_b32 m0, s61
	ds_read_b128 v[186:189], v149 offset:32768
	ds_read_b128 v[206:209], v149 offset:33792
	ds_read_b128 v[210:213], v149 offset:34816
	ds_read_b128 v[214:217], v149 offset:35840
	ds_read_b128 v[218:221], v149 offset:36864
	ds_read_b128 v[222:225], v149 offset:37888
	ds_read_b128 v[226:229], v149 offset:38912
	ds_read_b128 v[230:233], v149 offset:39936
	global_load_lds_dwordx4 v128, s[52:53]
	s_mov_b32 m0, s62
	s_nop 0
	global_load_lds_dwordx4 v130, s[52:53]
	s_waitcnt vmcnt(8)
	s_waitcnt lgkmcnt(0)
	s_barrier
	s_setprio 1
	s_waitcnt lgkmcnt(0)
	v_mfma_f32_16x16x32_bf16 v[124:127], v[140:143], v[186:189], v[124:127]
	v_mfma_f32_16x16x32_bf16 v[120:123], v[154:157], v[186:189], v[120:123]
	v_mfma_f32_16x16x32_bf16 v[108:111], v[140:143], v[210:213], v[108:111]
	v_mfma_f32_16x16x32_bf16 v[104:107], v[154:157], v[210:213], v[104:107]
	v_mfma_f32_16x16x32_bf16 v[92:95], v[140:143], v[218:221], v[92:95]
	v_mfma_f32_16x16x32_bf16 v[88:91], v[154:157], v[218:221], v[88:91]
	v_mfma_f32_16x16x32_bf16 v[76:79], v[140:143], v[226:229], v[76:79]
	v_mfma_f32_16x16x32_bf16 v[72:75], v[154:157], v[226:229], v[72:75]
	v_mfma_f32_16x16x32_bf16 v[124:127], v[150:153], v[206:209], v[124:127]
	v_mfma_f32_16x16x32_bf16 v[120:123], v[158:161], v[206:209], v[120:123]
	v_mfma_f32_16x16x32_bf16 v[108:111], v[150:153], v[214:217], v[108:111]
	v_mfma_f32_16x16x32_bf16 v[104:107], v[158:161], v[214:217], v[104:107]
	v_mfma_f32_16x16x32_bf16 v[92:95], v[150:153], v[222:225], v[92:95]
	v_mfma_f32_16x16x32_bf16 v[88:91], v[158:161], v[222:225], v[88:91]
	v_mfma_f32_16x16x32_bf16 v[76:79], v[150:153], v[230:233], v[76:79]
	v_mfma_f32_16x16x32_bf16 v[72:75], v[158:161], v[230:233], v[72:75]
	s_setprio 0
	s_setprio 1
	v_mfma_f32_16x16x32_bf16 v[116:119], v[162:165], v[186:189], v[116:119]
	v_mfma_f32_16x16x32_bf16 v[112:115], v[170:173], v[186:189], v[112:115]
	v_mfma_f32_16x16x32_bf16 v[100:103], v[162:165], v[210:213], v[100:103]
	v_mfma_f32_16x16x32_bf16 v[96:99], v[170:173], v[210:213], v[96:99]
	v_mfma_f32_16x16x32_bf16 v[84:87], v[162:165], v[218:221], v[84:87]
	v_mfma_f32_16x16x32_bf16 v[80:83], v[170:173], v[218:221], v[80:83]
	v_mfma_f32_16x16x32_bf16 v[68:71], v[162:165], v[226:229], v[68:71]
	v_mfma_f32_16x16x32_bf16 v[64:67], v[170:173], v[226:229], v[64:67]
	v_mfma_f32_16x16x32_bf16 v[116:119], v[166:169], v[206:209], v[116:119]
	v_mfma_f32_16x16x32_bf16 v[112:115], v[182:185], v[206:209], v[112:115]
	v_mfma_f32_16x16x32_bf16 v[100:103], v[166:169], v[214:217], v[100:103]
	v_mfma_f32_16x16x32_bf16 v[96:99], v[182:185], v[214:217], v[96:99]
	v_mfma_f32_16x16x32_bf16 v[84:87], v[166:169], v[222:225], v[84:87]
	v_mfma_f32_16x16x32_bf16 v[80:83], v[182:185], v[222:225], v[80:83]
	v_mfma_f32_16x16x32_bf16 v[68:71], v[166:169], v[230:233], v[68:71]
	v_mfma_f32_16x16x32_bf16 v[64:67], v[182:185], v[230:233], v[64:67]
	s_setprio 0
	s_barrier
	s_add_i32 s5, s5, s58
	s_mov_b32 m0, s5
	ds_read_b128 v[186:189], v149 offset:49152
	ds_read_b128 v[206:209], v149 offset:50176
	ds_read_b128 v[210:213], v149 offset:51200
	ds_read_b128 v[214:217], v149 offset:52224
	ds_read_b128 v[218:221], v149 offset:53248
	ds_read_b128 v[222:225], v149 offset:54272
	ds_read_b128 v[226:229], v149 offset:55296
	ds_read_b128 v[230:233], v149 offset:56320
	s_add_u32 s74, s50, 0x80
	s_addc_u32 s75, s51, 0
	global_load_lds_dwordx4 v176, s[74:75]
	s_add_i32 m0, s5, 0x2000
	s_add_u32 s50, s50, 0x200080
	s_addc_u32 s51, s51, 0
	s_add_i32 s5, s10, s58
	s_add_u32 s74, s50, 0xffe00000
	s_addc_u32 s75, s51, -1
	global_load_lds_dwordx4 v132, s[74:75]
	s_mov_b32 m0, s5
	s_nop 0
	global_load_lds_dwordx4 v176, s[50:51]
	s_add_i32 m0, s5, 0x2000
	s_nop 0
	global_load_lds_dwordx4 v132, s[50:51]
	s_mov_b32 m0, s64
	s_nop 0
	s_add_u32 s74, s52, 0xffe00080
	s_addc_u32 s75, s53, -1
	global_load_lds_dwordx4 v128, s[74:75]
	s_mov_b32 m0, s65
	s_nop 0
	s_add_u32 s74, s52, 0xffe00080
	s_addc_u32 s75, s53, -1
	global_load_lds_dwordx4 v130, s[74:75]
	s_waitcnt vmcnt(8)
	s_waitcnt lgkmcnt(0)
	s_barrier
	s_setprio 1
	s_waitcnt lgkmcnt(0)
	v_mfma_f32_16x16x32_bf16 v[60:63], v[140:143], v[186:189], v[60:63]
	v_mfma_f32_16x16x32_bf16 v[56:59], v[154:157], v[186:189], v[56:59]
	v_mfma_f32_16x16x32_bf16 v[44:47], v[140:143], v[210:213], v[44:47]
	v_mfma_f32_16x16x32_bf16 v[40:43], v[154:157], v[210:213], v[40:43]
	v_mfma_f32_16x16x32_bf16 v[28:31], v[140:143], v[218:221], v[28:31]
	v_mfma_f32_16x16x32_bf16 v[24:27], v[154:157], v[218:221], v[24:27]
	v_mfma_f32_16x16x32_bf16 v[12:15], v[140:143], v[226:229], v[12:15]
	v_mfma_f32_16x16x32_bf16 v[8:11], v[154:157], v[226:229], v[8:11]
	v_mfma_f32_16x16x32_bf16 v[60:63], v[150:153], v[206:209], v[60:63]
	v_mfma_f32_16x16x32_bf16 v[56:59], v[158:161], v[206:209], v[56:59]
	v_mfma_f32_16x16x32_bf16 v[44:47], v[150:153], v[214:217], v[44:47]
	v_mfma_f32_16x16x32_bf16 v[40:43], v[158:161], v[214:217], v[40:43]
	v_mfma_f32_16x16x32_bf16 v[28:31], v[150:153], v[222:225], v[28:31]
	v_mfma_f32_16x16x32_bf16 v[24:27], v[158:161], v[222:225], v[24:27]
	v_mfma_f32_16x16x32_bf16 v[12:15], v[150:153], v[230:233], v[12:15]
	v_mfma_f32_16x16x32_bf16 v[8:11], v[158:161], v[230:233], v[8:11]
	s_setprio 0
	s_setprio 1
	v_mfma_f32_16x16x32_bf16 v[52:55], v[162:165], v[186:189], v[52:55]
	v_mfma_f32_16x16x32_bf16 v[48:51], v[170:173], v[186:189], v[48:51]
	v_mfma_f32_16x16x32_bf16 v[36:39], v[162:165], v[210:213], v[36:39]
	v_mfma_f32_16x16x32_bf16 v[32:35], v[170:173], v[210:213], v[32:35]
	v_mfma_f32_16x16x32_bf16 v[20:23], v[162:165], v[218:221], v[20:23]
	v_mfma_f32_16x16x32_bf16 v[16:19], v[170:173], v[218:221], v[16:19]
	v_mfma_f32_16x16x32_bf16 v[4:7], v[162:165], v[226:229], v[4:7]
	v_mfma_f32_16x16x32_bf16 v[0:3], v[170:173], v[226:229], v[0:3]
	v_mfma_f32_16x16x32_bf16 v[52:55], v[166:169], v[206:209], v[52:55]
	v_mfma_f32_16x16x32_bf16 v[48:51], v[182:185], v[206:209], v[48:51]
	v_mfma_f32_16x16x32_bf16 v[36:39], v[166:169], v[214:217], v[36:39]
	v_mfma_f32_16x16x32_bf16 v[32:35], v[182:185], v[214:217], v[32:35]
	v_mfma_f32_16x16x32_bf16 v[20:23], v[166:169], v[222:225], v[20:23]
	v_mfma_f32_16x16x32_bf16 v[16:19], v[182:185], v[222:225], v[16:19]
	v_mfma_f32_16x16x32_bf16 v[4:7], v[166:169], v[230:233], v[4:7]
	v_mfma_f32_16x16x32_bf16 v[0:3], v[182:185], v[230:233], v[0:3]
	s_setprio 0
	s_barrier
	s_add_i32 s29, s29, 2
	s_add_u32 s48, s48, 0x100
	s_addc_u32 s49, s49, 0
	s_add_u32 s14, s14, 0x100
	s_addc_u32 s15, s15, 0
	s_cmpk_gt_u32 s29, 0x7d
	s_cbranch_scc0 .LBB0_2357
	s_and_b64 vcc, exec, s[26:27]
	s_cbranch_vccz .LBB0_2360
	s_barrier
